# removed the redundant s_setprio 0/1 pair between the two MFMA blocks of each GEMM super-phase (60 sites)
# baseline (speedup 1.0000x reference)
.LBB0_417:
	s_add_u32 s28, s6, 0xfffc0080
	s_addc_u32 s29, s7, -1
	s_add_i32 s43, 0, 0x10000
	s_cmp_eq_u32 s42, 12
	s_cselect_b32 s31, s5, s29
	s_cselect_b32 s30, s8, s28
	s_cselect_b32 s29, s9, s33
	s_cselect_b32 s28, s21, s23
	s_add_i32 s63, 0, 0x14000
	v_add_u32_e32 v142, s43, v186
	v_add_u32_e32 v168, s63, v186
	ds_read_b128 v[130:133], v142
	ds_read_b128 v[134:137], v142 offset:1024
	ds_read_b128 v[138:141], v142 offset:2048
	ds_read_b128 v[142:145], v142 offset:3072
	ds_read_b128 v[146:149], v168
	ds_read_b128 v[150:153], v168 offset:1024
	ds_read_b128 v[154:157], v168 offset:2048
	ds_read_b128 v[168:171], v168 offset:3072
	v_lshl_add_u64 v[216:217], s[6:7], 0, v[166:167]
	s_add_i32 m0, s45, 0xc000
	ds_read_b128 v[172:175], v188
	ds_read_b128 v[176:179], v188 offset:1024
	ds_read_b128 v[180:183], v188 offset:2048
	ds_read_b128 v[190:193], v188 offset:3072
	ds_read_b128 v[194:197], v188 offset:4096
	ds_read_b128 v[198:201], v188 offset:5120
	ds_read_b128 v[202:205], v188 offset:6144
	ds_read_b128 v[206:209], v188 offset:7168
	global_load_lds_dwordx4 v[216:217], off
	v_lshl_add_u64 v[216:217], s[6:7], 0, v[164:165]
	s_add_i32 m0, s45, 0xe000
	s_nop 0
	global_load_lds_dwordx4 v[216:217], off
	s_waitcnt vmcnt(8)
	s_waitcnt lgkmcnt(0)
	s_barrier
	s_setprio 1
	s_waitcnt lgkmcnt(0)
	v_mfma_f32_16x16x32_bf16 v[126:129], v[130:133], v[172:175], v[126:129]
	v_mfma_f32_16x16x32_bf16 v[122:125], v[138:141], v[172:175], v[122:125]
	v_mfma_f32_16x16x32_bf16 v[114:117], v[130:133], v[180:183], v[114:117]
	v_mfma_f32_16x16x32_bf16 v[106:109], v[138:141], v[180:183], v[106:109]
	v_mfma_f32_16x16x32_bf16 v[98:101], v[130:133], v[194:197], v[98:101]
	v_mfma_f32_16x16x32_bf16 v[90:93], v[138:141], v[194:197], v[90:93]
	v_mfma_f32_16x16x32_bf16 v[82:85], v[130:133], v[202:205], v[82:85]
	v_mfma_f32_16x16x32_bf16 v[74:77], v[138:141], v[202:205], v[74:77]
	v_mfma_f32_16x16x32_bf16 v[126:129], v[134:137], v[176:179], v[126:129]
	v_mfma_f32_16x16x32_bf16 v[122:125], v[142:145], v[176:179], v[122:125]
	v_mfma_f32_16x16x32_bf16 v[114:117], v[134:137], v[190:193], v[114:117]
	v_mfma_f32_16x16x32_bf16 v[106:109], v[142:145], v[190:193], v[106:109]
	v_mfma_f32_16x16x32_bf16 v[98:101], v[134:137], v[198:201], v[98:101]
	v_mfma_f32_16x16x32_bf16 v[90:93], v[142:145], v[198:201], v[90:93]
	v_mfma_f32_16x16x32_bf16 v[82:85], v[134:137], v[206:209], v[82:85]
	v_mfma_f32_16x16x32_bf16 v[74:77], v[142:145], v[206:209], v[74:77]
	v_mfma_f32_16x16x32_bf16 v[118:121], v[146:149], v[172:175], v[118:121]
	v_mfma_f32_16x16x32_bf16 v[110:113], v[154:157], v[172:175], v[110:113]
	v_mfma_f32_16x16x32_bf16 v[102:105], v[146:149], v[180:183], v[102:105]
	v_mfma_f32_16x16x32_bf16 v[94:97], v[154:157], v[180:183], v[94:97]
	v_mfma_f32_16x16x32_bf16 v[86:89], v[146:149], v[194:197], v[86:89]
	v_mfma_f32_16x16x32_bf16 v[78:81], v[154:157], v[194:197], v[78:81]
	v_mfma_f32_16x16x32_bf16 v[70:73], v[146:149], v[202:205], v[70:73]
	v_mfma_f32_16x16x32_bf16 v[66:69], v[154:157], v[202:205], v[66:69]
	v_mfma_f32_16x16x32_bf16 v[118:121], v[150:153], v[176:179], v[118:121]
	v_mfma_f32_16x16x32_bf16 v[110:113], v[168:171], v[176:179], v[110:113]
	v_mfma_f32_16x16x32_bf16 v[102:105], v[150:153], v[190:193], v[102:105]
	v_mfma_f32_16x16x32_bf16 v[94:97], v[168:171], v[190:193], v[94:97]
	v_mfma_f32_16x16x32_bf16 v[86:89], v[150:153], v[198:201], v[86:89]
	v_mfma_f32_16x16x32_bf16 v[78:81], v[168:171], v[198:201], v[78:81]
	v_mfma_f32_16x16x32_bf16 v[70:73], v[150:153], v[206:209], v[70:73]
	v_mfma_f32_16x16x32_bf16 v[66:69], v[168:171], v[206:209], v[66:69]
	s_setprio 0
	s_barrier
	s_add_i32 s43, s43, s44
	v_lshl_add_u64 v[216:217], s[28:29], 0, v[0:1]
	s_mov_b32 m0, s43
	ds_read_b128 v[172:175], v188 offset:16384
	ds_read_b128 v[176:179], v188 offset:17408
	ds_read_b128 v[180:183], v188 offset:18432
	ds_read_b128 v[190:193], v188 offset:19456
	ds_read_b128 v[194:197], v188 offset:20480
	ds_read_b128 v[198:201], v188 offset:21504
	ds_read_b128 v[202:205], v188 offset:22528
	ds_read_b128 v[206:209], v188 offset:23552
	global_load_lds_dwordx4 v[216:217], off
	s_add_i32 m0, s43, 0x2000
	s_add_u32 s58, s28, 0x40000
	v_lshl_add_u64 v[218:219], s[28:29], 0, v[158:159]
	s_addc_u32 s59, s29, 0
	s_add_i32 s43, s63, s44
	global_load_lds_dwordx4 v[218:219], off
	v_lshl_add_u64 v[220:221], s[58:59], 0, v[0:1]
	s_mov_b32 m0, s43
	v_lshl_add_u64 v[222:223], s[30:31], 0, v[160:161]
	global_load_lds_dwordx4 v[220:221], off
	v_lshl_add_u64 v[220:221], s[58:59], 0, v[158:159]
	s_add_i32 m0, s43, 0x2000
	s_nop 0
	global_load_lds_dwordx4 v[220:221], off
	v_lshl_add_u64 v[220:221], s[30:31], 0, v[162:163]
	s_mov_b32 m0, s45
	s_nop 0
	global_load_lds_dwordx4 v[220:221], off
	s_mov_b32 m0, s46
	s_nop 0
	global_load_lds_dwordx4 v[222:223], off
	s_waitcnt vmcnt(8)
	s_waitcnt lgkmcnt(0)
	s_barrier
	s_setprio 1
	s_waitcnt lgkmcnt(0)
	v_mfma_f32_16x16x32_bf16 v[62:65], v[130:133], v[172:175], v[62:65]
	v_mfma_f32_16x16x32_bf16 v[58:61], v[138:141], v[172:175], v[58:61]
	v_mfma_f32_16x16x32_bf16 v[50:53], v[130:133], v[180:183], v[50:53]
	v_mfma_f32_16x16x32_bf16 v[42:45], v[138:141], v[180:183], v[42:45]
	v_mfma_f32_16x16x32_bf16 v[34:37], v[130:133], v[194:197], v[34:37]
	v_mfma_f32_16x16x32_bf16 v[26:29], v[138:141], v[194:197], v[26:29]
	v_mfma_f32_16x16x32_bf16 v[18:21], v[130:133], v[202:205], v[18:21]
	v_mfma_f32_16x16x32_bf16 v[10:13], v[138:141], v[202:205], v[10:13]
	v_mfma_f32_16x16x32_bf16 v[62:65], v[134:137], v[176:179], v[62:65]
	v_mfma_f32_16x16x32_bf16 v[58:61], v[142:145], v[176:179], v[58:61]
	v_mfma_f32_16x16x32_bf16 v[50:53], v[134:137], v[190:193], v[50:53]
	v_mfma_f32_16x16x32_bf16 v[42:45], v[142:145], v[190:193], v[42:45]
	v_mfma_f32_16x16x32_bf16 v[34:37], v[134:137], v[198:201], v[34:37]
	v_mfma_f32_16x16x32_bf16 v[26:29], v[142:145], v[198:201], v[26:29]
	v_mfma_f32_16x16x32_bf16 v[18:21], v[134:137], v[206:209], v[18:21]
	v_mfma_f32_16x16x32_bf16 v[10:13], v[142:145], v[206:209], v[10:13]
	v_mfma_f32_16x16x32_bf16 v[54:57], v[146:149], v[172:175], v[54:57]
	v_mfma_f32_16x16x32_bf16 v[46:49], v[154:157], v[172:175], v[46:49]
	v_mfma_f32_16x16x32_bf16 v[38:41], v[146:149], v[180:183], v[38:41]
	v_mfma_f32_16x16x32_bf16 v[30:33], v[154:157], v[180:183], v[30:33]
	v_mfma_f32_16x16x32_bf16 v[22:25], v[146:149], v[194:197], v[22:25]
	v_mfma_f32_16x16x32_bf16 v[14:17], v[154:157], v[194:197], v[14:17]
	v_mfma_f32_16x16x32_bf16 v[6:9], v[146:149], v[202:205], v[6:9]
	v_mfma_f32_16x16x32_bf16 v[2:5], v[154:157], v[202:205], v[2:5]
	v_mfma_f32_16x16x32_bf16 v[54:57], v[150:153], v[176:179], v[54:57]
	v_mfma_f32_16x16x32_bf16 v[46:49], v[168:171], v[176:179], v[46:49]
	v_mfma_f32_16x16x32_bf16 v[38:41], v[150:153], v[190:193], v[38:41]
	v_mfma_f32_16x16x32_bf16 v[30:33], v[168:171], v[190:193], v[30:33]
	v_mfma_f32_16x16x32_bf16 v[22:25], v[150:153], v[198:201], v[22:25]
	v_mfma_f32_16x16x32_bf16 v[14:17], v[168:171], v[198:201], v[14:17]
	v_mfma_f32_16x16x32_bf16 v[6:9], v[150:153], v[206:209], v[6:9]
	v_mfma_f32_16x16x32_bf16 v[2:5], v[168:171], v[206:209], v[2:5]
	s_setprio 0
	s_barrier
	s_add_i32 s43, 0, 0x18000
	s_add_i32 s58, 0, 0x1c000
	v_add_u32_e32 v142, s43, v186
	v_add_u32_e32 v168, s58, v186
	ds_read_b128 v[130:133], v142
	ds_read_b128 v[134:137], v142 offset:1024
	ds_read_b128 v[138:141], v142 offset:2048
	ds_read_b128 v[142:145], v142 offset:3072
	ds_read_b128 v[146:149], v168
	ds_read_b128 v[150:153], v168 offset:1024
	ds_read_b128 v[154:157], v168 offset:2048
	ds_read_b128 v[168:171], v168 offset:3072
	s_add_u32 s30, s30, 0x40000
	s_addc_u32 s31, s31, 0
	s_mov_b32 m0, s47
	v_lshl_add_u64 v[224:225], s[30:31], 0, v[162:163]
	ds_read_b128 v[172:175], v188 offset:32768
	ds_read_b128 v[176:179], v188 offset:33792
	ds_read_b128 v[180:183], v188 offset:34816
	ds_read_b128 v[190:193], v188 offset:35840
	ds_read_b128 v[194:197], v188 offset:36864
	ds_read_b128 v[198:201], v188 offset:37888
	ds_read_b128 v[202:205], v188 offset:38912
	ds_read_b128 v[206:209], v188 offset:39936
	global_load_lds_dwordx4 v[224:225], off
	v_lshl_add_u64 v[224:225], s[30:31], 0, v[160:161]
	s_mov_b32 m0, s48
	s_nop 0
	global_load_lds_dwordx4 v[224:225], off
	s_waitcnt vmcnt(8)
	s_waitcnt lgkmcnt(0)
	s_barrier
	s_setprio 1
	s_waitcnt lgkmcnt(0)
	v_mfma_f32_16x16x32_bf16 v[126:129], v[130:133], v[172:175], v[126:129]
	v_mfma_f32_16x16x32_bf16 v[122:125], v[138:141], v[172:175], v[122:125]
	v_mfma_f32_16x16x32_bf16 v[114:117], v[130:133], v[180:183], v[114:117]
	v_mfma_f32_16x16x32_bf16 v[106:109], v[138:141], v[180:183], v[106:109]
	v_mfma_f32_16x16x32_bf16 v[98:101], v[130:133], v[194:197], v[98:101]
	v_mfma_f32_16x16x32_bf16 v[90:93], v[138:141], v[194:197], v[90:93]
	v_mfma_f32_16x16x32_bf16 v[82:85], v[130:133], v[202:205], v[82:85]
	v_mfma_f32_16x16x32_bf16 v[74:77], v[138:141], v[202:205], v[74:77]
	v_mfma_f32_16x16x32_bf16 v[126:129], v[134:137], v[176:179], v[126:129]
	v_mfma_f32_16x16x32_bf16 v[122:125], v[142:145], v[176:179], v[122:125]
	v_mfma_f32_16x16x32_bf16 v[114:117], v[134:137], v[190:193], v[114:117]
	v_mfma_f32_16x16x32_bf16 v[106:109], v[142:145], v[190:193], v[106:109]
	v_mfma_f32_16x16x32_bf16 v[98:101], v[134:137], v[198:201], v[98:101]
	v_mfma_f32_16x16x32_bf16 v[90:93], v[142:145], v[198:201], v[90:93]
	v_mfma_f32_16x16x32_bf16 v[82:85], v[134:137], v[206:209], v[82:85]
	v_mfma_f32_16x16x32_bf16 v[74:77], v[142:145], v[206:209], v[74:77]
	v_mfma_f32_16x16x32_bf16 v[118:121], v[146:149], v[172:175], v[118:121]
	v_mfma_f32_16x16x32_bf16 v[110:113], v[154:157], v[172:175], v[110:113]
	v_mfma_f32_16x16x32_bf16 v[102:105], v[146:149], v[180:183], v[102:105]
	v_mfma_f32_16x16x32_bf16 v[94:97], v[154:157], v[180:183], v[94:97]
	v_mfma_f32_16x16x32_bf16 v[86:89], v[146:149], v[194:197], v[86:89]
	v_mfma_f32_16x16x32_bf16 v[78:81], v[154:157], v[194:197], v[78:81]
	v_mfma_f32_16x16x32_bf16 v[70:73], v[146:149], v[202:205], v[70:73]
	v_mfma_f32_16x16x32_bf16 v[66:69], v[154:157], v[202:205], v[66:69]
	v_mfma_f32_16x16x32_bf16 v[118:121], v[150:153], v[176:179], v[118:121]
	v_mfma_f32_16x16x32_bf16 v[110:113], v[168:171], v[176:179], v[110:113]
	v_mfma_f32_16x16x32_bf16 v[102:105], v[150:153], v[190:193], v[102:105]
	v_mfma_f32_16x16x32_bf16 v[94:97], v[168:171], v[190:193], v[94:97]
	v_mfma_f32_16x16x32_bf16 v[86:89], v[150:153], v[198:201], v[86:89]
	v_mfma_f32_16x16x32_bf16 v[78:81], v[168:171], v[198:201], v[78:81]
	v_mfma_f32_16x16x32_bf16 v[70:73], v[150:153], v[206:209], v[70:73]
	v_mfma_f32_16x16x32_bf16 v[66:69], v[168:171], v[206:209], v[66:69]
	s_setprio 0
	s_barrier
	s_add_i32 s30, s43, s44
	v_lshl_add_u64 v[216:217], v[216:217], 0, s[56:57]
	s_mov_b32 m0, s30
	ds_read_b128 v[172:175], v188 offset:49152
	ds_read_b128 v[176:179], v188 offset:50176
	ds_read_b128 v[180:183], v188 offset:51200
	ds_read_b128 v[190:193], v188 offset:52224
	ds_read_b128 v[194:197], v188 offset:53248
	ds_read_b128 v[198:201], v188 offset:54272
	ds_read_b128 v[202:205], v188 offset:55296
	ds_read_b128 v[206:209], v188 offset:56320
	global_load_lds_dwordx4 v[216:217], off
	s_add_i32 m0, s30, 0x2000
	s_add_u32 s28, s28, 0x40080
	v_lshl_add_u64 v[216:217], v[218:219], 0, s[56:57]
	s_addc_u32 s29, s29, 0
	s_add_i32 s30, s58, s44
	global_load_lds_dwordx4 v[216:217], off
	v_lshl_add_u64 v[216:217], s[28:29], 0, v[0:1]
	s_mov_b32 m0, s30
	s_nop 0
	global_load_lds_dwordx4 v[216:217], off
	v_lshl_add_u64 v[216:217], s[28:29], 0, v[158:159]
	s_add_i32 m0, s30, 0x2000
	s_nop 0
	global_load_lds_dwordx4 v[216:217], off
	v_lshl_add_u64 v[216:217], v[220:221], 0, s[56:57]
	s_mov_b32 m0, s49
	s_nop 0
	global_load_lds_dwordx4 v[216:217], off
	v_lshl_add_u64 v[216:217], v[222:223], 0, s[56:57]
	s_mov_b32 m0, s52
	s_nop 0
	global_load_lds_dwordx4 v[216:217], off
	s_waitcnt vmcnt(8)
	s_waitcnt lgkmcnt(0)
	s_barrier
	s_setprio 1
	s_waitcnt lgkmcnt(0)
	v_mfma_f32_16x16x32_bf16 v[62:65], v[130:133], v[172:175], v[62:65]
	v_mfma_f32_16x16x32_bf16 v[58:61], v[138:141], v[172:175], v[58:61]
	v_mfma_f32_16x16x32_bf16 v[50:53], v[130:133], v[180:183], v[50:53]
	v_mfma_f32_16x16x32_bf16 v[42:45], v[138:141], v[180:183], v[42:45]
	v_mfma_f32_16x16x32_bf16 v[34:37], v[130:133], v[194:197], v[34:37]
	v_mfma_f32_16x16x32_bf16 v[26:29], v[138:141], v[194:197], v[26:29]
	v_mfma_f32_16x16x32_bf16 v[18:21], v[130:133], v[202:205], v[18:21]
	v_mfma_f32_16x16x32_bf16 v[10:13], v[138:141], v[202:205], v[10:13]
	v_mfma_f32_16x16x32_bf16 v[62:65], v[134:137], v[176:179], v[62:65]
	v_mfma_f32_16x16x32_bf16 v[58:61], v[142:145], v[176:179], v[58:61]
	v_mfma_f32_16x16x32_bf16 v[50:53], v[134:137], v[190:193], v[50:53]
	v_mfma_f32_16x16x32_bf16 v[42:45], v[142:145], v[190:193], v[42:45]
	v_mfma_f32_16x16x32_bf16 v[34:37], v[134:137], v[198:201], v[34:37]
	v_mfma_f32_16x16x32_bf16 v[26:29], v[142:145], v[198:201], v[26:29]
	v_mfma_f32_16x16x32_bf16 v[18:21], v[134:137], v[206:209], v[18:21]
	v_mfma_f32_16x16x32_bf16 v[10:13], v[142:145], v[206:209], v[10:13]
	v_mfma_f32_16x16x32_bf16 v[54:57], v[146:149], v[172:175], v[54:57]
	v_mfma_f32_16x16x32_bf16 v[46:49], v[154:157], v[172:175], v[46:49]
	v_mfma_f32_16x16x32_bf16 v[38:41], v[146:149], v[180:183], v[38:41]
	v_mfma_f32_16x16x32_bf16 v[30:33], v[154:157], v[180:183], v[30:33]
	v_mfma_f32_16x16x32_bf16 v[22:25], v[146:149], v[194:197], v[22:25]
	v_mfma_f32_16x16x32_bf16 v[14:17], v[154:157], v[194:197], v[14:17]
	v_mfma_f32_16x16x32_bf16 v[6:9], v[146:149], v[202:205], v[6:9]
	v_mfma_f32_16x16x32_bf16 v[2:5], v[154:157], v[202:205], v[2:5]
	v_mfma_f32_16x16x32_bf16 v[54:57], v[150:153], v[176:179], v[54:57]
	v_mfma_f32_16x16x32_bf16 v[46:49], v[168:171], v[176:179], v[46:49]
	v_mfma_f32_16x16x32_bf16 v[38:41], v[150:153], v[190:193], v[38:41]
	v_mfma_f32_16x16x32_bf16 v[30:33], v[168:171], v[190:193], v[30:33]
	v_mfma_f32_16x16x32_bf16 v[22:25], v[150:153], v[198:201], v[22:25]
	v_mfma_f32_16x16x32_bf16 v[14:17], v[168:171], v[198:201], v[14:17]
	v_mfma_f32_16x16x32_bf16 v[6:9], v[150:153], v[206:209], v[6:9]
	v_mfma_f32_16x16x32_bf16 v[2:5], v[168:171], v[206:209], v[2:5]
	s_setprio 0
	s_barrier
	s_add_i32 s42, s42, 2
	s_add_u32 s23, s23, 0x100
	s_addc_u32 s33, s33, 0
	s_add_u32 s6, s6, 0x100
	s_addc_u32 s7, s7, 0
	s_cmp_gt_u32 s42, 13
	s_cbranch_scc0 .LBB0_417
	s_and_b64 vcc, exec, s[18:19]
	s_cbranch_vccz .LBB0_420
	s_barrier

.LBB0_587:
	s_add_u32 s18, s34, s62
	s_addc_u32 s19, s35, s63
	s_add_u32 s18, s18, 0x100
	s_addc_u32 s19, s19, 0
	s_add_u32 s70, s8, s62
	s_addc_u32 s71, s9, s63
	s_add_i32 s26, 0, 0x10000
	s_cmpk_eq_i32 s62, 0x700
	s_cselect_b32 s77, s47, s19
	s_cselect_b32 s76, s59, s18
	s_cselect_b32 s71, s37, s71
	s_cselect_b32 s70, vcc_lo, s70
	s_add_i32 s27, 0, 0x14000
	v_add_u32_e32 v158, s26, v144
	v_add_u32_e32 v176, s27, v144
	ds_read_b128 v[146:149], v158
	ds_read_b128 v[150:153], v158 offset:1024
	ds_read_b128 v[154:157], v158 offset:2048
	ds_read_b128 v[158:161], v158 offset:3072
	ds_read_b128 v[162:165], v176
	ds_read_b128 v[168:171], v176 offset:1024
	ds_read_b128 v[172:175], v176 offset:2048
	ds_read_b128 v[176:179], v176 offset:3072
	v_lshl_add_u64 v[208:209], v[142:143], 0, s[62:63]
	s_add_i32 m0, s4, 0xc000
	ds_read_b128 v[180:183], v145
	ds_read_b128 v[184:187], v145 offset:1024
	ds_read_b128 v[188:191], v145 offset:2048
	ds_read_b128 v[192:195], v145 offset:3072
	ds_read_b128 v[196:199], v145 offset:4096
	ds_read_b128 v[200:203], v145 offset:5120
	ds_read_b128 v[204:207], v145 offset:6144
	ds_read_b128 v[216:219], v145 offset:7168
	global_load_lds_dwordx4 v[208:209], off
	v_lshl_add_u64 v[208:209], v[140:141], 0, s[62:63]
	s_add_i32 m0, s4, 0xe000
	s_nop 0
	global_load_lds_dwordx4 v[208:209], off
	s_waitcnt vmcnt(8)
	s_waitcnt lgkmcnt(0)
	s_barrier
	s_setprio 1
	s_waitcnt lgkmcnt(0)
	v_mfma_f32_16x16x32_bf16 v[134:137], v[146:149], v[180:183], v[134:137]
	v_mfma_f32_16x16x32_bf16 v[130:133], v[154:157], v[180:183], v[130:133]
	v_mfma_f32_16x16x32_bf16 v[110:113], v[146:149], v[188:191], v[110:113]
	v_mfma_f32_16x16x32_bf16 v[106:109], v[154:157], v[188:191], v[106:109]
	v_mfma_f32_16x16x32_bf16 v[94:97], v[146:149], v[196:199], v[94:97]
	v_mfma_f32_16x16x32_bf16 v[90:93], v[154:157], v[196:199], v[90:93]
	v_mfma_f32_16x16x32_bf16 v[78:81], v[146:149], v[204:207], v[78:81]
	v_mfma_f32_16x16x32_bf16 v[74:77], v[154:157], v[204:207], v[74:77]
	v_mfma_f32_16x16x32_bf16 v[134:137], v[150:153], v[184:187], v[134:137]
	v_mfma_f32_16x16x32_bf16 v[130:133], v[158:161], v[184:187], v[130:133]
	v_mfma_f32_16x16x32_bf16 v[110:113], v[150:153], v[192:195], v[110:113]
	v_mfma_f32_16x16x32_bf16 v[106:109], v[158:161], v[192:195], v[106:109]
	v_mfma_f32_16x16x32_bf16 v[94:97], v[150:153], v[200:203], v[94:97]
	v_mfma_f32_16x16x32_bf16 v[90:93], v[158:161], v[200:203], v[90:93]
	v_mfma_f32_16x16x32_bf16 v[78:81], v[150:153], v[216:219], v[78:81]
	v_mfma_f32_16x16x32_bf16 v[74:77], v[158:161], v[216:219], v[74:77]
	v_mfma_f32_16x16x32_bf16 v[122:125], v[162:165], v[180:183], v[122:125]
	v_mfma_f32_16x16x32_bf16 v[114:117], v[172:175], v[180:183], v[114:117]
	v_mfma_f32_16x16x32_bf16 v[102:105], v[162:165], v[188:191], v[102:105]
	v_mfma_f32_16x16x32_bf16 v[98:101], v[172:175], v[188:191], v[98:101]
	v_mfma_f32_16x16x32_bf16 v[86:89], v[162:165], v[196:199], v[86:89]
	v_mfma_f32_16x16x32_bf16 v[82:85], v[172:175], v[196:199], v[82:85]
	v_mfma_f32_16x16x32_bf16 v[70:73], v[162:165], v[204:207], v[70:73]
	v_mfma_f32_16x16x32_bf16 v[66:69], v[172:175], v[204:207], v[66:69]
	v_mfma_f32_16x16x32_bf16 v[122:125], v[168:171], v[184:187], v[122:125]
	v_mfma_f32_16x16x32_bf16 v[114:117], v[176:179], v[184:187], v[114:117]
	v_mfma_f32_16x16x32_bf16 v[102:105], v[168:171], v[192:195], v[102:105]
	v_mfma_f32_16x16x32_bf16 v[98:101], v[176:179], v[192:195], v[98:101]
	v_mfma_f32_16x16x32_bf16 v[86:89], v[168:171], v[200:203], v[86:89]
	v_mfma_f32_16x16x32_bf16 v[82:85], v[176:179], v[200:203], v[82:85]
	v_mfma_f32_16x16x32_bf16 v[70:73], v[168:171], v[216:219], v[70:73]
	v_mfma_f32_16x16x32_bf16 v[66:69], v[176:179], v[216:219], v[66:69]
	s_setprio 0
	s_barrier
	s_add_i32 s18, s26, s84
	v_lshl_add_u64 v[208:209], s[70:71], 0, v[0:1]
	s_mov_b32 m0, s18
	ds_read_b128 v[180:183], v145 offset:16384
	ds_read_b128 v[184:187], v145 offset:17408
	ds_read_b128 v[188:191], v145 offset:18432
	ds_read_b128 v[192:195], v145 offset:19456
	ds_read_b128 v[196:199], v145 offset:20480
	ds_read_b128 v[200:203], v145 offset:21504
	ds_read_b128 v[204:207], v145 offset:22528
	ds_read_b128 v[216:219], v145 offset:23552
	global_load_lds_dwordx4 v[208:209], off
	s_add_i32 m0, s18, 0x2000
	s_add_u32 s18, s70, 0x40000
	v_lshl_add_u64 v[220:221], s[70:71], 0, v[118:119]
	s_addc_u32 s19, s71, 0
	s_add_i32 s26, s27, s84
	global_load_lds_dwordx4 v[220:221], off
	v_lshl_add_u64 v[222:223], s[18:19], 0, v[0:1]
	s_mov_b32 m0, s26
	v_lshl_add_u64 v[224:225], s[76:77], 0, v[120:121]
	global_load_lds_dwordx4 v[222:223], off
	v_lshl_add_u64 v[222:223], s[18:19], 0, v[118:119]
	s_add_i32 m0, s26, 0x2000
	s_nop 0
	global_load_lds_dwordx4 v[222:223], off
	v_lshl_add_u64 v[222:223], s[76:77], 0, v[126:127]
	s_mov_b32 m0, s4
	s_nop 0
	global_load_lds_dwordx4 v[222:223], off
	s_mov_b32 m0, s5
	s_nop 0
	global_load_lds_dwordx4 v[224:225], off
	s_waitcnt vmcnt(8)
	s_waitcnt lgkmcnt(0)
	s_barrier
	s_setprio 1
	s_waitcnt lgkmcnt(0)
	v_mfma_f32_16x16x32_bf16 v[62:65], v[146:149], v[180:183], v[62:65]
	v_mfma_f32_16x16x32_bf16 v[58:61], v[154:157], v[180:183], v[58:61]
	v_mfma_f32_16x16x32_bf16 v[46:49], v[146:149], v[188:191], v[46:49]
	v_mfma_f32_16x16x32_bf16 v[42:45], v[154:157], v[188:191], v[42:45]
	v_mfma_f32_16x16x32_bf16 v[30:33], v[146:149], v[196:199], v[30:33]
	v_mfma_f32_16x16x32_bf16 v[26:29], v[154:157], v[196:199], v[26:29]
	v_mfma_f32_16x16x32_bf16 v[14:17], v[146:149], v[204:207], v[14:17]
	v_mfma_f32_16x16x32_bf16 v[10:13], v[154:157], v[204:207], v[10:13]
	v_mfma_f32_16x16x32_bf16 v[62:65], v[150:153], v[184:187], v[62:65]
	v_mfma_f32_16x16x32_bf16 v[58:61], v[158:161], v[184:187], v[58:61]
	v_mfma_f32_16x16x32_bf16 v[46:49], v[150:153], v[192:195], v[46:49]
	v_mfma_f32_16x16x32_bf16 v[42:45], v[158:161], v[192:195], v[42:45]
	v_mfma_f32_16x16x32_bf16 v[30:33], v[150:153], v[200:203], v[30:33]
	v_mfma_f32_16x16x32_bf16 v[26:29], v[158:161], v[200:203], v[26:29]
	v_mfma_f32_16x16x32_bf16 v[14:17], v[150:153], v[216:219], v[14:17]
	v_mfma_f32_16x16x32_bf16 v[10:13], v[158:161], v[216:219], v[10:13]
	v_mfma_f32_16x16x32_bf16 v[54:57], v[162:165], v[180:183], v[54:57]
	v_mfma_f32_16x16x32_bf16 v[50:53], v[172:175], v[180:183], v[50:53]
	v_mfma_f32_16x16x32_bf16 v[38:41], v[162:165], v[188:191], v[38:41]
	v_mfma_f32_16x16x32_bf16 v[34:37], v[172:175], v[188:191], v[34:37]
	v_mfma_f32_16x16x32_bf16 v[22:25], v[162:165], v[196:199], v[22:25]
	v_mfma_f32_16x16x32_bf16 v[18:21], v[172:175], v[196:199], v[18:21]
	v_mfma_f32_16x16x32_bf16 v[6:9], v[162:165], v[204:207], v[6:9]
	v_mfma_f32_16x16x32_bf16 v[2:5], v[172:175], v[204:207], v[2:5]
	v_mfma_f32_16x16x32_bf16 v[54:57], v[168:171], v[184:187], v[54:57]
	v_mfma_f32_16x16x32_bf16 v[50:53], v[176:179], v[184:187], v[50:53]
	v_mfma_f32_16x16x32_bf16 v[38:41], v[168:171], v[192:195], v[38:41]
	v_mfma_f32_16x16x32_bf16 v[34:37], v[176:179], v[192:195], v[34:37]
	v_mfma_f32_16x16x32_bf16 v[22:25], v[168:171], v[200:203], v[22:25]
	v_mfma_f32_16x16x32_bf16 v[18:21], v[176:179], v[200:203], v[18:21]
	v_mfma_f32_16x16x32_bf16 v[6:9], v[168:171], v[216:219], v[6:9]
	v_mfma_f32_16x16x32_bf16 v[2:5], v[176:179], v[216:219], v[2:5]
	s_setprio 0
	s_barrier
	s_add_i32 s26, 0, 0x18000
	s_add_i32 s27, 0, 0x1c000
	v_add_u32_e32 v158, s26, v144
	v_add_u32_e32 v176, s27, v144
	ds_read_b128 v[146:149], v158
	ds_read_b128 v[150:153], v158 offset:1024
	ds_read_b128 v[154:157], v158 offset:2048
	ds_read_b128 v[158:161], v158 offset:3072
	ds_read_b128 v[162:165], v176
	ds_read_b128 v[168:171], v176 offset:1024
	ds_read_b128 v[172:175], v176 offset:2048
	ds_read_b128 v[176:179], v176 offset:3072
	s_add_u32 s18, s76, 0x40000
	s_addc_u32 s19, s77, 0
	s_mov_b32 m0, s33
	v_lshl_add_u64 v[242:243], s[18:19], 0, v[126:127]
	ds_read_b128 v[180:183], v145 offset:32768
	ds_read_b128 v[184:187], v145 offset:33792
	ds_read_b128 v[188:191], v145 offset:34816
	ds_read_b128 v[192:195], v145 offset:35840
	ds_read_b128 v[196:199], v145 offset:36864
	ds_read_b128 v[200:203], v145 offset:37888
	ds_read_b128 v[204:207], v145 offset:38912
	ds_read_b128 v[216:219], v145 offset:39936
	global_load_lds_dwordx4 v[242:243], off
	v_lshl_add_u64 v[242:243], s[18:19], 0, v[120:121]
	s_mov_b32 m0, s92
	s_nop 0
	global_load_lds_dwordx4 v[242:243], off
	s_waitcnt vmcnt(8)
	s_waitcnt lgkmcnt(0)
	s_barrier
	s_setprio 1
	s_waitcnt lgkmcnt(0)
	v_mfma_f32_16x16x32_bf16 v[134:137], v[146:149], v[180:183], v[134:137]
	v_mfma_f32_16x16x32_bf16 v[130:133], v[154:157], v[180:183], v[130:133]
	v_mfma_f32_16x16x32_bf16 v[110:113], v[146:149], v[188:191], v[110:113]
	v_mfma_f32_16x16x32_bf16 v[106:109], v[154:157], v[188:191], v[106:109]
	v_mfma_f32_16x16x32_bf16 v[94:97], v[146:149], v[196:199], v[94:97]
	v_mfma_f32_16x16x32_bf16 v[90:93], v[154:157], v[196:199], v[90:93]
	v_mfma_f32_16x16x32_bf16 v[78:81], v[146:149], v[204:207], v[78:81]
	v_mfma_f32_16x16x32_bf16 v[74:77], v[154:157], v[204:207], v[74:77]
	v_mfma_f32_16x16x32_bf16 v[134:137], v[150:153], v[184:187], v[134:137]
	v_mfma_f32_16x16x32_bf16 v[130:133], v[158:161], v[184:187], v[130:133]
	v_mfma_f32_16x16x32_bf16 v[110:113], v[150:153], v[192:195], v[110:113]
	v_mfma_f32_16x16x32_bf16 v[106:109], v[158:161], v[192:195], v[106:109]
	v_mfma_f32_16x16x32_bf16 v[94:97], v[150:153], v[200:203], v[94:97]
	v_mfma_f32_16x16x32_bf16 v[90:93], v[158:161], v[200:203], v[90:93]
	v_mfma_f32_16x16x32_bf16 v[78:81], v[150:153], v[216:219], v[78:81]
	v_mfma_f32_16x16x32_bf16 v[74:77], v[158:161], v[216:219], v[74:77]
	v_mfma_f32_16x16x32_bf16 v[122:125], v[162:165], v[180:183], v[122:125]
	v_mfma_f32_16x16x32_bf16 v[114:117], v[172:175], v[180:183], v[114:117]
	v_mfma_f32_16x16x32_bf16 v[102:105], v[162:165], v[188:191], v[102:105]
	v_mfma_f32_16x16x32_bf16 v[98:101], v[172:175], v[188:191], v[98:101]
	v_mfma_f32_16x16x32_bf16 v[86:89], v[162:165], v[196:199], v[86:89]
	v_mfma_f32_16x16x32_bf16 v[82:85], v[172:175], v[196:199], v[82:85]
	v_mfma_f32_16x16x32_bf16 v[70:73], v[162:165], v[204:207], v[70:73]
	v_mfma_f32_16x16x32_bf16 v[66:69], v[172:175], v[204:207], v[66:69]
	v_mfma_f32_16x16x32_bf16 v[122:125], v[168:171], v[184:187], v[122:125]
	v_mfma_f32_16x16x32_bf16 v[114:117], v[176:179], v[184:187], v[114:117]
	v_mfma_f32_16x16x32_bf16 v[102:105], v[168:171], v[192:195], v[102:105]
	v_mfma_f32_16x16x32_bf16 v[98:101], v[176:179], v[192:195], v[98:101]
	v_mfma_f32_16x16x32_bf16 v[86:89], v[168:171], v[200:203], v[86:89]
	v_mfma_f32_16x16x32_bf16 v[82:85], v[176:179], v[200:203], v[82:85]
	v_mfma_f32_16x16x32_bf16 v[70:73], v[168:171], v[216:219], v[70:73]
	v_mfma_f32_16x16x32_bf16 v[66:69], v[176:179], v[216:219], v[66:69]
	s_setprio 0
	s_barrier
	s_add_i32 s18, s26, s84
	v_lshl_add_u64 v[208:209], v[208:209], 0, s[56:57]
	s_mov_b32 m0, s18
	ds_read_b128 v[180:183], v145 offset:49152
	ds_read_b128 v[184:187], v145 offset:50176
	ds_read_b128 v[188:191], v145 offset:51200
	ds_read_b128 v[192:195], v145 offset:52224
	ds_read_b128 v[196:199], v145 offset:53248
	ds_read_b128 v[200:203], v145 offset:54272
	ds_read_b128 v[204:207], v145 offset:55296
	ds_read_b128 v[216:219], v145 offset:56320
	global_load_lds_dwordx4 v[208:209], off
	s_add_i32 m0, s18, 0x2000
	s_add_u32 s18, s70, 0x40080
	v_lshl_add_u64 v[208:209], v[220:221], 0, s[56:57]
	s_addc_u32 s19, s71, 0
	s_add_i32 s26, s27, s84
	global_load_lds_dwordx4 v[208:209], off
	v_lshl_add_u64 v[208:209], s[18:19], 0, v[0:1]
	s_mov_b32 m0, s26
	s_nop 0
	global_load_lds_dwordx4 v[208:209], off
	v_lshl_add_u64 v[208:209], s[18:19], 0, v[118:119]
	s_add_i32 m0, s26, 0x2000
	s_nop 0
	global_load_lds_dwordx4 v[208:209], off
	v_lshl_add_u64 v[208:209], v[222:223], 0, s[56:57]
	s_mov_b32 m0, s90
	s_nop 0
	global_load_lds_dwordx4 v[208:209], off
	v_lshl_add_u64 v[208:209], v[224:225], 0, s[56:57]
	s_mov_b32 m0, s96
	s_nop 0
	global_load_lds_dwordx4 v[208:209], off
	s_waitcnt vmcnt(8)
	s_waitcnt lgkmcnt(0)
	s_barrier
	s_setprio 1
	s_waitcnt lgkmcnt(0)
	v_mfma_f32_16x16x32_bf16 v[62:65], v[146:149], v[180:183], v[62:65]
	v_mfma_f32_16x16x32_bf16 v[58:61], v[154:157], v[180:183], v[58:61]
	v_mfma_f32_16x16x32_bf16 v[46:49], v[146:149], v[188:191], v[46:49]
	v_mfma_f32_16x16x32_bf16 v[42:45], v[154:157], v[188:191], v[42:45]
	v_mfma_f32_16x16x32_bf16 v[30:33], v[146:149], v[196:199], v[30:33]
	v_mfma_f32_16x16x32_bf16 v[26:29], v[154:157], v[196:199], v[26:29]
	v_mfma_f32_16x16x32_bf16 v[14:17], v[146:149], v[204:207], v[14:17]
	v_mfma_f32_16x16x32_bf16 v[10:13], v[154:157], v[204:207], v[10:13]
	v_mfma_f32_16x16x32_bf16 v[62:65], v[150:153], v[184:187], v[62:65]
	v_mfma_f32_16x16x32_bf16 v[58:61], v[158:161], v[184:187], v[58:61]
	v_mfma_f32_16x16x32_bf16 v[46:49], v[150:153], v[192:195], v[46:49]
	v_mfma_f32_16x16x32_bf16 v[42:45], v[158:161], v[192:195], v[42:45]
	v_mfma_f32_16x16x32_bf16 v[30:33], v[150:153], v[200:203], v[30:33]
	v_mfma_f32_16x16x32_bf16 v[26:29], v[158:161], v[200:203], v[26:29]
	v_mfma_f32_16x16x32_bf16 v[14:17], v[150:153], v[216:219], v[14:17]
	v_mfma_f32_16x16x32_bf16 v[10:13], v[158:161], v[216:219], v[10:13]
	v_mfma_f32_16x16x32_bf16 v[54:57], v[162:165], v[180:183], v[54:57]
	v_mfma_f32_16x16x32_bf16 v[50:53], v[172:175], v[180:183], v[50:53]
	v_mfma_f32_16x16x32_bf16 v[38:41], v[162:165], v[188:191], v[38:41]
	v_mfma_f32_16x16x32_bf16 v[34:37], v[172:175], v[188:191], v[34:37]
	v_mfma_f32_16x16x32_bf16 v[22:25], v[162:165], v[196:199], v[22:25]
	v_mfma_f32_16x16x32_bf16 v[18:21], v[172:175], v[196:199], v[18:21]
	v_mfma_f32_16x16x32_bf16 v[6:9], v[162:165], v[204:207], v[6:9]
	v_mfma_f32_16x16x32_bf16 v[2:5], v[172:175], v[204:207], v[2:5]
	v_mfma_f32_16x16x32_bf16 v[54:57], v[168:171], v[184:187], v[54:57]
	v_mfma_f32_16x16x32_bf16 v[50:53], v[176:179], v[184:187], v[50:53]
	v_mfma_f32_16x16x32_bf16 v[38:41], v[168:171], v[192:195], v[38:41]
	v_mfma_f32_16x16x32_bf16 v[34:37], v[176:179], v[192:195], v[34:37]
	v_mfma_f32_16x16x32_bf16 v[22:25], v[168:171], v[200:203], v[22:25]
	v_mfma_f32_16x16x32_bf16 v[18:21], v[176:179], v[200:203], v[18:21]
	v_mfma_f32_16x16x32_bf16 v[6:9], v[168:171], v[216:219], v[6:9]
	v_mfma_f32_16x16x32_bf16 v[2:5], v[176:179], v[216:219], v[2:5]
	s_setprio 0
	s_barrier
	s_add_i32 vcc_hi, vcc_hi, 2
	s_add_u32 s62, s62, 0x100
	s_addc_u32 s63, s63, 0
	s_cmp_gt_u32 vcc_hi, 13
	s_cbranch_scc0 .LBB0_587
	s_add_u32 s62, s8, 0xffffff00
	s_addc_u32 s63, s9, -1
	s_andn2_b64 vcc, exec, s[44:45]
	s_cbranch_vccnz .LBB0_590
	v_mov_b32_e32 v2, 0
	s_mov_b32 s20, s36
	s_mov_b32 s83, s46
	s_mov_b64 s[34:35], s[52:53]
	s_mov_b32 s68, s58
	v_mov_b32_e32 v3, v2
	v_mov_b32_e32 v4, v2
	v_mov_b32_e32 v5, v2
	v_mov_b32_e32 v6, v2
	v_mov_b32_e32 v7, v2
	v_mov_b32_e32 v8, v2
	v_mov_b32_e32 v9, v2
	v_mov_b32_e32 v18, v2
	v_mov_b32_e32 v19, v2
	v_mov_b32_e32 v20, v2
	v_mov_b32_e32 v21, v2
	v_mov_b32_e32 v22, v2
	v_mov_b32_e32 v23, v2
	v_mov_b32_e32 v24, v2
	v_mov_b32_e32 v25, v2
	v_mov_b32_e32 v34, v2
	v_mov_b32_e32 v35, v2
	v_mov_b32_e32 v36, v2
	v_mov_b32_e32 v37, v2
	v_mov_b32_e32 v38, v2
	v_mov_b32_e32 v39, v2
	v_mov_b32_e32 v40, v2
	v_mov_b32_e32 v41, v2
	v_mov_b32_e32 v50, v2
	v_mov_b32_e32 v51, v2
	v_mov_b32_e32 v52, v2
	v_mov_b32_e32 v53, v2
	v_mov_b32_e32 v54, v2
	v_mov_b32_e32 v55, v2
	v_mov_b32_e32 v56, v2
	v_mov_b32_e32 v57, v2
	v_mov_b32_e32 v10, v2
	v_mov_b32_e32 v11, v2
	v_mov_b32_e32 v12, v2
	v_mov_b32_e32 v13, v2
	v_mov_b32_e32 v14, v2
	v_mov_b32_e32 v15, v2
	v_mov_b32_e32 v16, v2
	v_mov_b32_e32 v17, v2
	v_mov_b32_e32 v26, v2
	v_mov_b32_e32 v27, v2
	v_mov_b32_e32 v28, v2
	v_mov_b32_e32 v29, v2
	v_mov_b32_e32 v30, v2
	v_mov_b32_e32 v31, v2
	v_mov_b32_e32 v32, v2
	v_mov_b32_e32 v33, v2
	v_mov_b32_e32 v42, v2
	v_mov_b32_e32 v43, v2
	v_mov_b32_e32 v44, v2
	v_mov_b32_e32 v45, v2
	v_mov_b32_e32 v46, v2
	v_mov_b32_e32 v47, v2
	v_mov_b32_e32 v48, v2
	v_mov_b32_e32 v49, v2
	v_mov_b32_e32 v58, v2
	v_mov_b32_e32 v59, v2
	v_mov_b32_e32 v60, v2
	v_mov_b32_e32 v61, v2
	v_mov_b32_e32 v62, v2
	v_mov_b32_e32 v63, v2
	v_mov_b32_e32 v64, v2
	v_mov_b32_e32 v65, v2
	v_mov_b32_e32 v66, v2
	v_mov_b32_e32 v67, v2
	v_mov_b32_e32 v68, v2
	v_mov_b32_e32 v69, v2
	v_mov_b32_e32 v70, v2
	v_mov_b32_e32 v71, v2
	v_mov_b32_e32 v72, v2
	v_mov_b32_e32 v73, v2
	v_mov_b32_e32 v82, v2
	v_mov_b32_e32 v83, v2
	v_mov_b32_e32 v84, v2
	v_mov_b32_e32 v85, v2
	v_mov_b32_e32 v86, v2
	v_mov_b32_e32 v87, v2
	v_mov_b32_e32 v88, v2
	v_mov_b32_e32 v89, v2
	v_mov_b32_e32 v98, v2
	v_mov_b32_e32 v99, v2
	v_mov_b32_e32 v100, v2
	v_mov_b32_e32 v101, v2
	v_mov_b32_e32 v102, v2
	v_mov_b32_e32 v103, v2
	v_mov_b32_e32 v104, v2
	v_mov_b32_e32 v105, v2
	v_mov_b32_e32 v114, v2
	v_mov_b32_e32 v115, v2
	v_mov_b32_e32 v116, v2
	v_mov_b32_e32 v117, v2
	v_mov_b32_e32 v122, v2
	v_mov_b32_e32 v123, v2
	v_mov_b32_e32 v124, v2
	v_mov_b32_e32 v125, v2
	v_mov_b32_e32 v74, v2
	v_mov_b32_e32 v75, v2
	v_mov_b32_e32 v76, v2
	v_mov_b32_e32 v77, v2
	v_mov_b32_e32 v78, v2
	v_mov_b32_e32 v79, v2
	v_mov_b32_e32 v80, v2
	v_mov_b32_e32 v81, v2
	v_mov_b32_e32 v90, v2
	v_mov_b32_e32 v91, v2
	v_mov_b32_e32 v92, v2
	v_mov_b32_e32 v93, v2
	v_mov_b32_e32 v94, v2
	v_mov_b32_e32 v95, v2
	v_mov_b32_e32 v96, v2
	v_mov_b32_e32 v97, v2
	v_mov_b32_e32 v106, v2
	v_mov_b32_e32 v107, v2
	v_mov_b32_e32 v108, v2
	v_mov_b32_e32 v109, v2
	v_mov_b32_e32 v110, v2
	v_mov_b32_e32 v111, v2
	v_mov_b32_e32 v112, v2
	v_mov_b32_e32 v113, v2
	v_mov_b32_e32 v130, v2
	v_mov_b32_e32 v131, v2
	v_mov_b32_e32 v132, v2
	v_mov_b32_e32 v133, v2
	v_mov_b32_e32 v134, v2
	v_mov_b32_e32 v135, v2
	v_mov_b32_e32 v136, v2
	v_mov_b32_e32 v137, v2
	s_andn2_b64 vcc, exec, s[42:43]
	s_cbranch_vccnz .LBB0_591
	s_branch .LBB0_592

.LBB0_684:
	s_add_u32 s52, s30, s48
	s_addc_u32 s53, s31, s49
	s_add_u32 s52, s52, 0x100
	s_addc_u32 s53, s53, 0
	s_add_u32 s95, s8, s48
	s_addc_u32 s96, s9, s49
	s_add_i32 vcc_lo, 0, 0x10000
	s_cmpk_eq_i32 s48, 0x700
	s_cselect_b32 s63, s37, s53
	s_cselect_b32 s62, s59, s52
	s_cselect_b32 s53, s35, s96
	s_cselect_b32 s52, s93, s95
	s_add_i32 s95, 0, 0x14000
	v_add_u32_e32 v158, vcc_lo, v144
	v_add_u32_e32 v167, s95, v144
	ds_read_b128 v[146:149], v158
	ds_read_b128 v[150:153], v158 offset:1024
	ds_read_b128 v[154:157], v158 offset:2048
	ds_read_b128 v[158:161], v158 offset:3072
	ds_read_b128 v[162:165], v167
	ds_read_b128 v[168:171], v167 offset:1024
	ds_read_b128 v[172:175], v167 offset:2048
	ds_read_b128 v[176:179], v167 offset:3072
	v_lshl_add_u64 v[208:209], v[142:143], 0, s[48:49]
	s_add_i32 m0, s4, 0xc000
	ds_read_b128 v[180:183], v145
	ds_read_b128 v[184:187], v145 offset:1024
	ds_read_b128 v[188:191], v145 offset:2048
	ds_read_b128 v[192:195], v145 offset:3072
	ds_read_b128 v[196:199], v145 offset:4096
	ds_read_b128 v[200:203], v145 offset:5120
	ds_read_b128 v[204:207], v145 offset:6144
	ds_read_b128 v[216:219], v145 offset:7168
	global_load_lds_dwordx4 v[208:209], off
	v_lshl_add_u64 v[208:209], v[140:141], 0, s[48:49]
	s_add_i32 m0, s4, 0xe000
	s_nop 0
	global_load_lds_dwordx4 v[208:209], off
	s_waitcnt vmcnt(8)
	s_waitcnt lgkmcnt(0)
	s_barrier
	s_setprio 1
	s_waitcnt lgkmcnt(0)
	v_mfma_f32_16x16x32_bf16 v[134:137], v[146:149], v[180:183], v[134:137]
	v_mfma_f32_16x16x32_bf16 v[130:133], v[154:157], v[180:183], v[130:133]
	v_mfma_f32_16x16x32_bf16 v[110:113], v[146:149], v[188:191], v[110:113]
	v_mfma_f32_16x16x32_bf16 v[106:109], v[154:157], v[188:191], v[106:109]
	v_mfma_f32_16x16x32_bf16 v[94:97], v[146:149], v[196:199], v[94:97]
	v_mfma_f32_16x16x32_bf16 v[90:93], v[154:157], v[196:199], v[90:93]
	v_mfma_f32_16x16x32_bf16 v[78:81], v[146:149], v[204:207], v[78:81]
	v_mfma_f32_16x16x32_bf16 v[74:77], v[154:157], v[204:207], v[74:77]
	v_mfma_f32_16x16x32_bf16 v[134:137], v[150:153], v[184:187], v[134:137]
	v_mfma_f32_16x16x32_bf16 v[130:133], v[158:161], v[184:187], v[130:133]
	v_mfma_f32_16x16x32_bf16 v[110:113], v[150:153], v[192:195], v[110:113]
	v_mfma_f32_16x16x32_bf16 v[106:109], v[158:161], v[192:195], v[106:109]
	v_mfma_f32_16x16x32_bf16 v[94:97], v[150:153], v[200:203], v[94:97]
	v_mfma_f32_16x16x32_bf16 v[90:93], v[158:161], v[200:203], v[90:93]
	v_mfma_f32_16x16x32_bf16 v[78:81], v[150:153], v[216:219], v[78:81]
	v_mfma_f32_16x16x32_bf16 v[74:77], v[158:161], v[216:219], v[74:77]
	v_mfma_f32_16x16x32_bf16 v[122:125], v[162:165], v[180:183], v[122:125]
	v_mfma_f32_16x16x32_bf16 v[114:117], v[172:175], v[180:183], v[114:117]
	v_mfma_f32_16x16x32_bf16 v[102:105], v[162:165], v[188:191], v[102:105]
	v_mfma_f32_16x16x32_bf16 v[98:101], v[172:175], v[188:191], v[98:101]
	v_mfma_f32_16x16x32_bf16 v[86:89], v[162:165], v[196:199], v[86:89]
	v_mfma_f32_16x16x32_bf16 v[82:85], v[172:175], v[196:199], v[82:85]
	v_mfma_f32_16x16x32_bf16 v[70:73], v[162:165], v[204:207], v[70:73]
	v_mfma_f32_16x16x32_bf16 v[66:69], v[172:175], v[204:207], v[66:69]
	v_mfma_f32_16x16x32_bf16 v[122:125], v[168:171], v[184:187], v[122:125]
	v_mfma_f32_16x16x32_bf16 v[114:117], v[176:179], v[184:187], v[114:117]
	v_mfma_f32_16x16x32_bf16 v[102:105], v[168:171], v[192:195], v[102:105]
	v_mfma_f32_16x16x32_bf16 v[98:101], v[176:179], v[192:195], v[98:101]
	v_mfma_f32_16x16x32_bf16 v[86:89], v[168:171], v[200:203], v[86:89]
	v_mfma_f32_16x16x32_bf16 v[82:85], v[176:179], v[200:203], v[82:85]
	v_mfma_f32_16x16x32_bf16 v[70:73], v[168:171], v[216:219], v[70:73]
	v_mfma_f32_16x16x32_bf16 v[66:69], v[176:179], v[216:219], v[66:69]
	s_setprio 0
	s_barrier
	s_add_i32 s96, vcc_lo, s77
	v_lshl_add_u64 v[208:209], s[52:53], 0, v[0:1]
	s_mov_b32 m0, s96
	ds_read_b128 v[180:183], v145 offset:16384
	ds_read_b128 v[184:187], v145 offset:17408
	ds_read_b128 v[188:191], v145 offset:18432
	ds_read_b128 v[192:195], v145 offset:19456
	ds_read_b128 v[196:199], v145 offset:20480
	ds_read_b128 v[200:203], v145 offset:21504
	ds_read_b128 v[204:207], v145 offset:22528
	ds_read_b128 v[216:219], v145 offset:23552
	global_load_lds_dwordx4 v[208:209], off
	s_add_i32 m0, s96, 0x2000
	s_add_u32 vcc_lo, s52, 0x40000
	v_lshl_add_u64 v[220:221], s[52:53], 0, v[118:119]
	s_addc_u32 vcc_hi, s53, 0
	s_add_i32 s95, s95, s77
	global_load_lds_dwordx4 v[220:221], off
	v_lshl_add_u64 v[222:223], vcc, 0, v[0:1]
	s_mov_b32 m0, s95
	v_lshl_add_u64 v[224:225], s[62:63], 0, v[120:121]
	global_load_lds_dwordx4 v[222:223], off
	v_lshl_add_u64 v[222:223], vcc, 0, v[118:119]
	s_add_i32 m0, s95, 0x2000
	s_nop 0
	global_load_lds_dwordx4 v[222:223], off
	v_lshl_add_u64 v[222:223], s[62:63], 0, v[126:127]
	s_mov_b32 m0, s4
	s_nop 0
	global_load_lds_dwordx4 v[222:223], off
	s_mov_b32 m0, s5
	s_nop 0
	global_load_lds_dwordx4 v[224:225], off
	s_waitcnt vmcnt(8)
	s_waitcnt lgkmcnt(0)
	s_barrier
	s_setprio 1
	s_waitcnt lgkmcnt(0)
	v_mfma_f32_16x16x32_bf16 v[62:65], v[146:149], v[180:183], v[62:65]
	v_mfma_f32_16x16x32_bf16 v[58:61], v[154:157], v[180:183], v[58:61]
	v_mfma_f32_16x16x32_bf16 v[46:49], v[146:149], v[188:191], v[46:49]
	v_mfma_f32_16x16x32_bf16 v[42:45], v[154:157], v[188:191], v[42:45]
	v_mfma_f32_16x16x32_bf16 v[30:33], v[146:149], v[196:199], v[30:33]
	v_mfma_f32_16x16x32_bf16 v[26:29], v[154:157], v[196:199], v[26:29]
	v_mfma_f32_16x16x32_bf16 v[14:17], v[146:149], v[204:207], v[14:17]
	v_mfma_f32_16x16x32_bf16 v[10:13], v[154:157], v[204:207], v[10:13]
	v_mfma_f32_16x16x32_bf16 v[62:65], v[150:153], v[184:187], v[62:65]
	v_mfma_f32_16x16x32_bf16 v[58:61], v[158:161], v[184:187], v[58:61]
	v_mfma_f32_16x16x32_bf16 v[46:49], v[150:153], v[192:195], v[46:49]
	v_mfma_f32_16x16x32_bf16 v[42:45], v[158:161], v[192:195], v[42:45]
	v_mfma_f32_16x16x32_bf16 v[30:33], v[150:153], v[200:203], v[30:33]
	v_mfma_f32_16x16x32_bf16 v[26:29], v[158:161], v[200:203], v[26:29]
	v_mfma_f32_16x16x32_bf16 v[14:17], v[150:153], v[216:219], v[14:17]
	v_mfma_f32_16x16x32_bf16 v[10:13], v[158:161], v[216:219], v[10:13]
	v_mfma_f32_16x16x32_bf16 v[54:57], v[162:165], v[180:183], v[54:57]
	v_mfma_f32_16x16x32_bf16 v[50:53], v[172:175], v[180:183], v[50:53]
	v_mfma_f32_16x16x32_bf16 v[38:41], v[162:165], v[188:191], v[38:41]
	v_mfma_f32_16x16x32_bf16 v[34:37], v[172:175], v[188:191], v[34:37]
	v_mfma_f32_16x16x32_bf16 v[22:25], v[162:165], v[196:199], v[22:25]
	v_mfma_f32_16x16x32_bf16 v[18:21], v[172:175], v[196:199], v[18:21]
	v_mfma_f32_16x16x32_bf16 v[6:9], v[162:165], v[204:207], v[6:9]
	v_mfma_f32_16x16x32_bf16 v[2:5], v[172:175], v[204:207], v[2:5]
	v_mfma_f32_16x16x32_bf16 v[54:57], v[168:171], v[184:187], v[54:57]
	v_mfma_f32_16x16x32_bf16 v[50:53], v[176:179], v[184:187], v[50:53]
	v_mfma_f32_16x16x32_bf16 v[38:41], v[168:171], v[192:195], v[38:41]
	v_mfma_f32_16x16x32_bf16 v[34:37], v[176:179], v[192:195], v[34:37]
	v_mfma_f32_16x16x32_bf16 v[22:25], v[168:171], v[200:203], v[22:25]
	v_mfma_f32_16x16x32_bf16 v[18:21], v[176:179], v[200:203], v[18:21]
	v_mfma_f32_16x16x32_bf16 v[6:9], v[168:171], v[216:219], v[6:9]
	v_mfma_f32_16x16x32_bf16 v[2:5], v[176:179], v[216:219], v[2:5]
	s_setprio 0
	s_barrier
	s_add_i32 s95, 0, 0x18000
	s_add_i32 s96, 0, 0x1c000
	v_add_u32_e32 v158, s95, v144
	v_add_u32_e32 v167, s96, v144
	ds_read_b128 v[146:149], v158
	ds_read_b128 v[150:153], v158 offset:1024
	ds_read_b128 v[154:157], v158 offset:2048
	ds_read_b128 v[158:161], v158 offset:3072
	ds_read_b128 v[162:165], v167
	ds_read_b128 v[168:171], v167 offset:1024
	ds_read_b128 v[172:175], v167 offset:2048
	ds_read_b128 v[176:179], v167 offset:3072
	s_add_u32 s62, s62, 0x40000
	s_addc_u32 s63, s63, 0
	s_mov_b32 m0, s33
	v_lshl_add_u64 v[242:243], s[62:63], 0, v[126:127]
	ds_read_b128 v[180:183], v145 offset:32768
	ds_read_b128 v[184:187], v145 offset:33792
	ds_read_b128 v[188:191], v145 offset:34816
	ds_read_b128 v[192:195], v145 offset:35840
	ds_read_b128 v[196:199], v145 offset:36864
	ds_read_b128 v[200:203], v145 offset:37888
	ds_read_b128 v[204:207], v145 offset:38912
	ds_read_b128 v[216:219], v145 offset:39936
	global_load_lds_dwordx4 v[242:243], off
	v_lshl_add_u64 v[242:243], s[62:63], 0, v[120:121]
	s_mov_b32 m0, s84
	s_nop 0
	global_load_lds_dwordx4 v[242:243], off
	s_waitcnt vmcnt(8)
	s_waitcnt lgkmcnt(0)
	s_barrier
	s_setprio 1
	s_waitcnt lgkmcnt(0)
	v_mfma_f32_16x16x32_bf16 v[134:137], v[146:149], v[180:183], v[134:137]
	v_mfma_f32_16x16x32_bf16 v[130:133], v[154:157], v[180:183], v[130:133]
	v_mfma_f32_16x16x32_bf16 v[110:113], v[146:149], v[188:191], v[110:113]
	v_mfma_f32_16x16x32_bf16 v[106:109], v[154:157], v[188:191], v[106:109]
	v_mfma_f32_16x16x32_bf16 v[94:97], v[146:149], v[196:199], v[94:97]
	v_mfma_f32_16x16x32_bf16 v[90:93], v[154:157], v[196:199], v[90:93]
	v_mfma_f32_16x16x32_bf16 v[78:81], v[146:149], v[204:207], v[78:81]
	v_mfma_f32_16x16x32_bf16 v[74:77], v[154:157], v[204:207], v[74:77]
	v_mfma_f32_16x16x32_bf16 v[134:137], v[150:153], v[184:187], v[134:137]
	v_mfma_f32_16x16x32_bf16 v[130:133], v[158:161], v[184:187], v[130:133]
	v_mfma_f32_16x16x32_bf16 v[110:113], v[150:153], v[192:195], v[110:113]
	v_mfma_f32_16x16x32_bf16 v[106:109], v[158:161], v[192:195], v[106:109]
	v_mfma_f32_16x16x32_bf16 v[94:97], v[150:153], v[200:203], v[94:97]
	v_mfma_f32_16x16x32_bf16 v[90:93], v[158:161], v[200:203], v[90:93]
	v_mfma_f32_16x16x32_bf16 v[78:81], v[150:153], v[216:219], v[78:81]
	v_mfma_f32_16x16x32_bf16 v[74:77], v[158:161], v[216:219], v[74:77]
	v_mfma_f32_16x16x32_bf16 v[122:125], v[162:165], v[180:183], v[122:125]
	v_mfma_f32_16x16x32_bf16 v[114:117], v[172:175], v[180:183], v[114:117]
	v_mfma_f32_16x16x32_bf16 v[102:105], v[162:165], v[188:191], v[102:105]
	v_mfma_f32_16x16x32_bf16 v[98:101], v[172:175], v[188:191], v[98:101]
	v_mfma_f32_16x16x32_bf16 v[86:89], v[162:165], v[196:199], v[86:89]
	v_mfma_f32_16x16x32_bf16 v[82:85], v[172:175], v[196:199], v[82:85]
	v_mfma_f32_16x16x32_bf16 v[70:73], v[162:165], v[204:207], v[70:73]
	v_mfma_f32_16x16x32_bf16 v[66:69], v[172:175], v[204:207], v[66:69]
	v_mfma_f32_16x16x32_bf16 v[122:125], v[168:171], v[184:187], v[122:125]
	v_mfma_f32_16x16x32_bf16 v[114:117], v[176:179], v[184:187], v[114:117]
	v_mfma_f32_16x16x32_bf16 v[102:105], v[168:171], v[192:195], v[102:105]
	v_mfma_f32_16x16x32_bf16 v[98:101], v[176:179], v[192:195], v[98:101]
	v_mfma_f32_16x16x32_bf16 v[86:89], v[168:171], v[200:203], v[86:89]
	v_mfma_f32_16x16x32_bf16 v[82:85], v[176:179], v[200:203], v[82:85]
	v_mfma_f32_16x16x32_bf16 v[70:73], v[168:171], v[216:219], v[70:73]
	v_mfma_f32_16x16x32_bf16 v[66:69], v[176:179], v[216:219], v[66:69]
	s_setprio 0
	s_barrier
	s_add_i32 s62, s95, s77
	v_lshl_add_u64 v[208:209], v[208:209], 0, s[56:57]
	s_mov_b32 m0, s62
	ds_read_b128 v[180:183], v145 offset:49152
	ds_read_b128 v[184:187], v145 offset:50176
	ds_read_b128 v[188:191], v145 offset:51200
	ds_read_b128 v[192:195], v145 offset:52224
	ds_read_b128 v[196:199], v145 offset:53248
	ds_read_b128 v[200:203], v145 offset:54272
	ds_read_b128 v[204:207], v145 offset:55296
	ds_read_b128 v[216:219], v145 offset:56320
	global_load_lds_dwordx4 v[208:209], off
	s_add_i32 m0, s62, 0x2000
	s_add_u32 s52, s52, 0x40080
	v_lshl_add_u64 v[208:209], v[220:221], 0, s[56:57]
	s_addc_u32 s53, s53, 0
	s_add_i32 s62, s96, s77
	global_load_lds_dwordx4 v[208:209], off
	v_lshl_add_u64 v[208:209], s[52:53], 0, v[0:1]
	s_mov_b32 m0, s62
	s_nop 0
	global_load_lds_dwordx4 v[208:209], off
	v_lshl_add_u64 v[208:209], s[52:53], 0, v[118:119]
	s_add_i32 m0, s62, 0x2000
	s_nop 0
	global_load_lds_dwordx4 v[208:209], off
	v_lshl_add_u64 v[208:209], v[222:223], 0, s[56:57]
	s_mov_b32 m0, s85
	s_nop 0
	global_load_lds_dwordx4 v[208:209], off
	v_lshl_add_u64 v[208:209], v[224:225], 0, s[56:57]
	s_mov_b32 m0, s90
	s_nop 0
	global_load_lds_dwordx4 v[208:209], off
	s_waitcnt vmcnt(8)
	s_waitcnt lgkmcnt(0)
	s_barrier
	s_setprio 1
	s_waitcnt lgkmcnt(0)
	v_mfma_f32_16x16x32_bf16 v[62:65], v[146:149], v[180:183], v[62:65]
	v_mfma_f32_16x16x32_bf16 v[58:61], v[154:157], v[180:183], v[58:61]
	v_mfma_f32_16x16x32_bf16 v[46:49], v[146:149], v[188:191], v[46:49]
	v_mfma_f32_16x16x32_bf16 v[42:45], v[154:157], v[188:191], v[42:45]
	v_mfma_f32_16x16x32_bf16 v[30:33], v[146:149], v[196:199], v[30:33]
	v_mfma_f32_16x16x32_bf16 v[26:29], v[154:157], v[196:199], v[26:29]
	v_mfma_f32_16x16x32_bf16 v[14:17], v[146:149], v[204:207], v[14:17]
	v_mfma_f32_16x16x32_bf16 v[10:13], v[154:157], v[204:207], v[10:13]
	v_mfma_f32_16x16x32_bf16 v[62:65], v[150:153], v[184:187], v[62:65]
	v_mfma_f32_16x16x32_bf16 v[58:61], v[158:161], v[184:187], v[58:61]
	v_mfma_f32_16x16x32_bf16 v[46:49], v[150:153], v[192:195], v[46:49]
	v_mfma_f32_16x16x32_bf16 v[42:45], v[158:161], v[192:195], v[42:45]
	v_mfma_f32_16x16x32_bf16 v[30:33], v[150:153], v[200:203], v[30:33]
	v_mfma_f32_16x16x32_bf16 v[26:29], v[158:161], v[200:203], v[26:29]
	v_mfma_f32_16x16x32_bf16 v[14:17], v[150:153], v[216:219], v[14:17]
	v_mfma_f32_16x16x32_bf16 v[10:13], v[158:161], v[216:219], v[10:13]
	v_mfma_f32_16x16x32_bf16 v[54:57], v[162:165], v[180:183], v[54:57]
	v_mfma_f32_16x16x32_bf16 v[50:53], v[172:175], v[180:183], v[50:53]
	v_mfma_f32_16x16x32_bf16 v[38:41], v[162:165], v[188:191], v[38:41]
	v_mfma_f32_16x16x32_bf16 v[34:37], v[172:175], v[188:191], v[34:37]
	v_mfma_f32_16x16x32_bf16 v[22:25], v[162:165], v[196:199], v[22:25]
	v_mfma_f32_16x16x32_bf16 v[18:21], v[172:175], v[196:199], v[18:21]
	v_mfma_f32_16x16x32_bf16 v[6:9], v[162:165], v[204:207], v[6:9]
	v_mfma_f32_16x16x32_bf16 v[2:5], v[172:175], v[204:207], v[2:5]
	v_mfma_f32_16x16x32_bf16 v[54:57], v[168:171], v[184:187], v[54:57]
	v_mfma_f32_16x16x32_bf16 v[50:53], v[176:179], v[184:187], v[50:53]
	v_mfma_f32_16x16x32_bf16 v[38:41], v[168:171], v[192:195], v[38:41]
	v_mfma_f32_16x16x32_bf16 v[34:37], v[176:179], v[192:195], v[34:37]
	v_mfma_f32_16x16x32_bf16 v[22:25], v[168:171], v[200:203], v[22:25]
	v_mfma_f32_16x16x32_bf16 v[18:21], v[176:179], v[200:203], v[18:21]
	v_mfma_f32_16x16x32_bf16 v[6:9], v[168:171], v[216:219], v[6:9]
	v_mfma_f32_16x16x32_bf16 v[2:5], v[176:179], v[216:219], v[2:5]
	s_setprio 0
	s_barrier
	s_add_i32 s94, s94, 2
	s_add_u32 s48, s48, 0x100
	s_addc_u32 s49, s49, 0
	s_cmp_gt_u32 s94, 13
	s_cbranch_scc0 .LBB0_684
	s_add_u32 s48, s8, 0xffffff00
	s_addc_u32 s49, s9, -1
	s_andn2_b64 vcc, exec, s[42:43]
	s_cbranch_vccnz .LBB0_687
	v_mov_b32_e32 v2, 0
	s_mov_b32 s18, s34
	s_mov_b32 s92, s36
	s_mov_b64 s[30:31], s[46:47]
	s_mov_b32 s68, s58
	v_mov_b32_e32 v3, v2
	v_mov_b32_e32 v4, v2
	v_mov_b32_e32 v5, v2
	v_mov_b32_e32 v6, v2
	v_mov_b32_e32 v7, v2
	v_mov_b32_e32 v8, v2
	v_mov_b32_e32 v9, v2
	v_mov_b32_e32 v18, v2
	v_mov_b32_e32 v19, v2
	v_mov_b32_e32 v20, v2
	v_mov_b32_e32 v21, v2
	v_mov_b32_e32 v22, v2
	v_mov_b32_e32 v23, v2
	v_mov_b32_e32 v24, v2
	v_mov_b32_e32 v25, v2
	v_mov_b32_e32 v34, v2
	v_mov_b32_e32 v35, v2
	v_mov_b32_e32 v36, v2
	v_mov_b32_e32 v37, v2
	v_mov_b32_e32 v38, v2
	v_mov_b32_e32 v39, v2
	v_mov_b32_e32 v40, v2
	v_mov_b32_e32 v41, v2
	v_mov_b32_e32 v50, v2
	v_mov_b32_e32 v51, v2
	v_mov_b32_e32 v52, v2
	v_mov_b32_e32 v53, v2
	v_mov_b32_e32 v54, v2
	v_mov_b32_e32 v55, v2
	v_mov_b32_e32 v56, v2
	v_mov_b32_e32 v57, v2
	v_mov_b32_e32 v10, v2
	v_mov_b32_e32 v11, v2
	v_mov_b32_e32 v12, v2
	v_mov_b32_e32 v13, v2
	v_mov_b32_e32 v14, v2
	v_mov_b32_e32 v15, v2
	v_mov_b32_e32 v16, v2
	v_mov_b32_e32 v17, v2
	v_mov_b32_e32 v26, v2
	v_mov_b32_e32 v27, v2
	v_mov_b32_e32 v28, v2
	v_mov_b32_e32 v29, v2
	v_mov_b32_e32 v30, v2
	v_mov_b32_e32 v31, v2
	v_mov_b32_e32 v32, v2
	v_mov_b32_e32 v33, v2
	v_mov_b32_e32 v42, v2
	v_mov_b32_e32 v43, v2
	v_mov_b32_e32 v44, v2
	v_mov_b32_e32 v45, v2
	v_mov_b32_e32 v46, v2
	v_mov_b32_e32 v47, v2
	v_mov_b32_e32 v48, v2
	v_mov_b32_e32 v49, v2
	v_mov_b32_e32 v58, v2
	v_mov_b32_e32 v59, v2
	v_mov_b32_e32 v60, v2
	v_mov_b32_e32 v61, v2
	v_mov_b32_e32 v62, v2
	v_mov_b32_e32 v63, v2
	v_mov_b32_e32 v64, v2
	v_mov_b32_e32 v65, v2
	v_mov_b32_e32 v66, v2
	v_mov_b32_e32 v67, v2
	v_mov_b32_e32 v68, v2
	v_mov_b32_e32 v69, v2
	v_mov_b32_e32 v70, v2
	v_mov_b32_e32 v71, v2
	v_mov_b32_e32 v72, v2
	v_mov_b32_e32 v73, v2
	v_mov_b32_e32 v82, v2
	v_mov_b32_e32 v83, v2
	v_mov_b32_e32 v84, v2
	v_mov_b32_e32 v85, v2
	v_mov_b32_e32 v86, v2
	v_mov_b32_e32 v87, v2
	v_mov_b32_e32 v88, v2
	v_mov_b32_e32 v89, v2
	v_mov_b32_e32 v98, v2
	v_mov_b32_e32 v99, v2
	v_mov_b32_e32 v100, v2
	v_mov_b32_e32 v101, v2
	v_mov_b32_e32 v102, v2
	v_mov_b32_e32 v103, v2
	v_mov_b32_e32 v104, v2
	v_mov_b32_e32 v105, v2
	v_mov_b32_e32 v114, v2
	v_mov_b32_e32 v115, v2
	v_mov_b32_e32 v116, v2
	v_mov_b32_e32 v117, v2
	v_mov_b32_e32 v122, v2
	v_mov_b32_e32 v123, v2
	v_mov_b32_e32 v124, v2
	v_mov_b32_e32 v125, v2
	v_mov_b32_e32 v74, v2
	v_mov_b32_e32 v75, v2
	v_mov_b32_e32 v76, v2
	v_mov_b32_e32 v77, v2
	v_mov_b32_e32 v78, v2
	v_mov_b32_e32 v79, v2
	v_mov_b32_e32 v80, v2
	v_mov_b32_e32 v81, v2
	v_mov_b32_e32 v90, v2
	v_mov_b32_e32 v91, v2
	v_mov_b32_e32 v92, v2
	v_mov_b32_e32 v93, v2
	v_mov_b32_e32 v94, v2
	v_mov_b32_e32 v95, v2
	v_mov_b32_e32 v96, v2
	v_mov_b32_e32 v97, v2
	v_mov_b32_e32 v106, v2
	v_mov_b32_e32 v107, v2
	v_mov_b32_e32 v108, v2
	v_mov_b32_e32 v109, v2
	v_mov_b32_e32 v110, v2
	v_mov_b32_e32 v111, v2
	v_mov_b32_e32 v112, v2
	v_mov_b32_e32 v113, v2
	v_mov_b32_e32 v130, v2
	v_mov_b32_e32 v131, v2
	v_mov_b32_e32 v132, v2
	v_mov_b32_e32 v133, v2
	v_mov_b32_e32 v134, v2
	v_mov_b32_e32 v135, v2
	v_mov_b32_e32 v136, v2
	v_mov_b32_e32 v137, v2
	s_branch .LBB0_688

.LBB0_836:
	s_add_u32 s28, s6, 0xfffc0080
	s_addc_u32 s29, s7, -1
	s_add_i32 s41, 0, 0x10000
	s_cmp_eq_u32 s40, 12
	s_cselect_b32 s31, s5, s29
	s_cselect_b32 s30, s8, s28
	s_cselect_b32 s29, s9, s33
	s_cselect_b32 s28, s21, s23
	s_add_i32 s53, 0, 0x14000
	v_add_u32_e32 v142, s41, v186
	v_add_u32_e32 v168, s53, v186
	ds_read_b128 v[130:133], v142
	ds_read_b128 v[134:137], v142 offset:1024
	ds_read_b128 v[138:141], v142 offset:2048
	ds_read_b128 v[142:145], v142 offset:3072
	ds_read_b128 v[146:149], v168
	ds_read_b128 v[150:153], v168 offset:1024
	ds_read_b128 v[154:157], v168 offset:2048
	ds_read_b128 v[168:171], v168 offset:3072
	v_lshl_add_u64 v[216:217], s[6:7], 0, v[166:167]
	s_add_i32 m0, s43, 0xc000
	ds_read_b128 v[172:175], v188
	ds_read_b128 v[176:179], v188 offset:1024
	ds_read_b128 v[180:183], v188 offset:2048
	ds_read_b128 v[190:193], v188 offset:3072
	ds_read_b128 v[194:197], v188 offset:4096
	ds_read_b128 v[198:201], v188 offset:5120
	ds_read_b128 v[202:205], v188 offset:6144
	ds_read_b128 v[206:209], v188 offset:7168
	global_load_lds_dwordx4 v[216:217], off
	v_lshl_add_u64 v[216:217], s[6:7], 0, v[164:165]
	s_add_i32 m0, s43, 0xe000
	s_nop 0
	global_load_lds_dwordx4 v[216:217], off
	s_waitcnt vmcnt(8)
	s_waitcnt lgkmcnt(0)
	s_barrier
	s_setprio 1
	s_waitcnt lgkmcnt(0)
	v_mfma_f32_16x16x32_bf16 v[126:129], v[130:133], v[172:175], v[126:129]
	v_mfma_f32_16x16x32_bf16 v[122:125], v[138:141], v[172:175], v[122:125]
	v_mfma_f32_16x16x32_bf16 v[114:117], v[130:133], v[180:183], v[114:117]
	v_mfma_f32_16x16x32_bf16 v[106:109], v[138:141], v[180:183], v[106:109]
	v_mfma_f32_16x16x32_bf16 v[98:101], v[130:133], v[194:197], v[98:101]
	v_mfma_f32_16x16x32_bf16 v[90:93], v[138:141], v[194:197], v[90:93]
	v_mfma_f32_16x16x32_bf16 v[82:85], v[130:133], v[202:205], v[82:85]
	v_mfma_f32_16x16x32_bf16 v[74:77], v[138:141], v[202:205], v[74:77]
	v_mfma_f32_16x16x32_bf16 v[126:129], v[134:137], v[176:179], v[126:129]
	v_mfma_f32_16x16x32_bf16 v[122:125], v[142:145], v[176:179], v[122:125]
	v_mfma_f32_16x16x32_bf16 v[114:117], v[134:137], v[190:193], v[114:117]
	v_mfma_f32_16x16x32_bf16 v[106:109], v[142:145], v[190:193], v[106:109]
	v_mfma_f32_16x16x32_bf16 v[98:101], v[134:137], v[198:201], v[98:101]
	v_mfma_f32_16x16x32_bf16 v[90:93], v[142:145], v[198:201], v[90:93]
	v_mfma_f32_16x16x32_bf16 v[82:85], v[134:137], v[206:209], v[82:85]
	v_mfma_f32_16x16x32_bf16 v[74:77], v[142:145], v[206:209], v[74:77]
	v_mfma_f32_16x16x32_bf16 v[118:121], v[146:149], v[172:175], v[118:121]
	v_mfma_f32_16x16x32_bf16 v[110:113], v[154:157], v[172:175], v[110:113]
	v_mfma_f32_16x16x32_bf16 v[102:105], v[146:149], v[180:183], v[102:105]
	v_mfma_f32_16x16x32_bf16 v[94:97], v[154:157], v[180:183], v[94:97]
	v_mfma_f32_16x16x32_bf16 v[86:89], v[146:149], v[194:197], v[86:89]
	v_mfma_f32_16x16x32_bf16 v[78:81], v[154:157], v[194:197], v[78:81]
	v_mfma_f32_16x16x32_bf16 v[70:73], v[146:149], v[202:205], v[70:73]
	v_mfma_f32_16x16x32_bf16 v[66:69], v[154:157], v[202:205], v[66:69]
	v_mfma_f32_16x16x32_bf16 v[118:121], v[150:153], v[176:179], v[118:121]
	v_mfma_f32_16x16x32_bf16 v[110:113], v[168:171], v[176:179], v[110:113]
	v_mfma_f32_16x16x32_bf16 v[102:105], v[150:153], v[190:193], v[102:105]
	v_mfma_f32_16x16x32_bf16 v[94:97], v[168:171], v[190:193], v[94:97]
	v_mfma_f32_16x16x32_bf16 v[86:89], v[150:153], v[198:201], v[86:89]
	v_mfma_f32_16x16x32_bf16 v[78:81], v[168:171], v[198:201], v[78:81]
	v_mfma_f32_16x16x32_bf16 v[70:73], v[150:153], v[206:209], v[70:73]
	v_mfma_f32_16x16x32_bf16 v[66:69], v[168:171], v[206:209], v[66:69]
	s_setprio 0
	s_barrier
	s_add_i32 s41, s41, s42
	v_lshl_add_u64 v[216:217], s[28:29], 0, v[0:1]
	s_mov_b32 m0, s41
	ds_read_b128 v[172:175], v188 offset:16384
	ds_read_b128 v[176:179], v188 offset:17408
	ds_read_b128 v[180:183], v188 offset:18432
	ds_read_b128 v[190:193], v188 offset:19456
	ds_read_b128 v[194:197], v188 offset:20480
	ds_read_b128 v[198:201], v188 offset:21504
	ds_read_b128 v[202:205], v188 offset:22528
	ds_read_b128 v[206:209], v188 offset:23552
	global_load_lds_dwordx4 v[216:217], off
	s_add_i32 m0, s41, 0x2000
	s_add_u32 s58, s28, 0x40000
	v_lshl_add_u64 v[218:219], s[28:29], 0, v[158:159]
	s_addc_u32 s59, s29, 0
	s_add_i32 s41, s53, s42
	global_load_lds_dwordx4 v[218:219], off
	v_lshl_add_u64 v[220:221], s[58:59], 0, v[0:1]
	s_mov_b32 m0, s41
	v_lshl_add_u64 v[222:223], s[30:31], 0, v[160:161]
	global_load_lds_dwordx4 v[220:221], off
	v_lshl_add_u64 v[220:221], s[58:59], 0, v[158:159]
	s_add_i32 m0, s41, 0x2000
	s_nop 0
	global_load_lds_dwordx4 v[220:221], off
	v_lshl_add_u64 v[220:221], s[30:31], 0, v[162:163]
	s_mov_b32 m0, s43
	s_nop 0
	global_load_lds_dwordx4 v[220:221], off
	s_mov_b32 m0, s44
	s_nop 0
	global_load_lds_dwordx4 v[222:223], off
	s_waitcnt vmcnt(8)
	s_waitcnt lgkmcnt(0)
	s_barrier
	s_setprio 1
	s_waitcnt lgkmcnt(0)
	v_mfma_f32_16x16x32_bf16 v[62:65], v[130:133], v[172:175], v[62:65]
	v_mfma_f32_16x16x32_bf16 v[58:61], v[138:141], v[172:175], v[58:61]
	v_mfma_f32_16x16x32_bf16 v[50:53], v[130:133], v[180:183], v[50:53]
	v_mfma_f32_16x16x32_bf16 v[42:45], v[138:141], v[180:183], v[42:45]
	v_mfma_f32_16x16x32_bf16 v[34:37], v[130:133], v[194:197], v[34:37]
	v_mfma_f32_16x16x32_bf16 v[26:29], v[138:141], v[194:197], v[26:29]
	v_mfma_f32_16x16x32_bf16 v[18:21], v[130:133], v[202:205], v[18:21]
	v_mfma_f32_16x16x32_bf16 v[10:13], v[138:141], v[202:205], v[10:13]
	v_mfma_f32_16x16x32_bf16 v[62:65], v[134:137], v[176:179], v[62:65]
	v_mfma_f32_16x16x32_bf16 v[58:61], v[142:145], v[176:179], v[58:61]
	v_mfma_f32_16x16x32_bf16 v[50:53], v[134:137], v[190:193], v[50:53]
	v_mfma_f32_16x16x32_bf16 v[42:45], v[142:145], v[190:193], v[42:45]
	v_mfma_f32_16x16x32_bf16 v[34:37], v[134:137], v[198:201], v[34:37]
	v_mfma_f32_16x16x32_bf16 v[26:29], v[142:145], v[198:201], v[26:29]
	v_mfma_f32_16x16x32_bf16 v[18:21], v[134:137], v[206:209], v[18:21]
	v_mfma_f32_16x16x32_bf16 v[10:13], v[142:145], v[206:209], v[10:13]
	v_mfma_f32_16x16x32_bf16 v[54:57], v[146:149], v[172:175], v[54:57]
	v_mfma_f32_16x16x32_bf16 v[46:49], v[154:157], v[172:175], v[46:49]
	v_mfma_f32_16x16x32_bf16 v[38:41], v[146:149], v[180:183], v[38:41]
	v_mfma_f32_16x16x32_bf16 v[30:33], v[154:157], v[180:183], v[30:33]
	v_mfma_f32_16x16x32_bf16 v[22:25], v[146:149], v[194:197], v[22:25]
	v_mfma_f32_16x16x32_bf16 v[14:17], v[154:157], v[194:197], v[14:17]
	v_mfma_f32_16x16x32_bf16 v[6:9], v[146:149], v[202:205], v[6:9]
	v_mfma_f32_16x16x32_bf16 v[2:5], v[154:157], v[202:205], v[2:5]
	v_mfma_f32_16x16x32_bf16 v[54:57], v[150:153], v[176:179], v[54:57]
	v_mfma_f32_16x16x32_bf16 v[46:49], v[168:171], v[176:179], v[46:49]
	v_mfma_f32_16x16x32_bf16 v[38:41], v[150:153], v[190:193], v[38:41]
	v_mfma_f32_16x16x32_bf16 v[30:33], v[168:171], v[190:193], v[30:33]
	v_mfma_f32_16x16x32_bf16 v[22:25], v[150:153], v[198:201], v[22:25]
	v_mfma_f32_16x16x32_bf16 v[14:17], v[168:171], v[198:201], v[14:17]
	v_mfma_f32_16x16x32_bf16 v[6:9], v[150:153], v[206:209], v[6:9]
	v_mfma_f32_16x16x32_bf16 v[2:5], v[168:171], v[206:209], v[2:5]
	s_setprio 0
	s_barrier
	s_add_i32 s41, 0, 0x18000
	s_add_i32 s53, 0, 0x1c000
	v_add_u32_e32 v142, s41, v186
	v_add_u32_e32 v168, s53, v186
	ds_read_b128 v[130:133], v142
	ds_read_b128 v[134:137], v142 offset:1024
	ds_read_b128 v[138:141], v142 offset:2048
	ds_read_b128 v[142:145], v142 offset:3072
	ds_read_b128 v[146:149], v168
	ds_read_b128 v[150:153], v168 offset:1024
	ds_read_b128 v[154:157], v168 offset:2048
	ds_read_b128 v[168:171], v168 offset:3072
	s_add_u32 s30, s30, 0x40000
	s_addc_u32 s31, s31, 0
	s_mov_b32 m0, s45
	v_lshl_add_u64 v[224:225], s[30:31], 0, v[162:163]
	ds_read_b128 v[172:175], v188 offset:32768
	ds_read_b128 v[176:179], v188 offset:33792
	ds_read_b128 v[180:183], v188 offset:34816
	ds_read_b128 v[190:193], v188 offset:35840
	ds_read_b128 v[194:197], v188 offset:36864
	ds_read_b128 v[198:201], v188 offset:37888
	ds_read_b128 v[202:205], v188 offset:38912
	ds_read_b128 v[206:209], v188 offset:39936
	global_load_lds_dwordx4 v[224:225], off
	v_lshl_add_u64 v[224:225], s[30:31], 0, v[160:161]
	s_mov_b32 m0, s46
	s_nop 0
	global_load_lds_dwordx4 v[224:225], off
	s_waitcnt vmcnt(8)
	s_waitcnt lgkmcnt(0)
	s_barrier
	s_setprio 1
	s_waitcnt lgkmcnt(0)
	v_mfma_f32_16x16x32_bf16 v[126:129], v[130:133], v[172:175], v[126:129]
	v_mfma_f32_16x16x32_bf16 v[122:125], v[138:141], v[172:175], v[122:125]
	v_mfma_f32_16x16x32_bf16 v[114:117], v[130:133], v[180:183], v[114:117]
	v_mfma_f32_16x16x32_bf16 v[106:109], v[138:141], v[180:183], v[106:109]
	v_mfma_f32_16x16x32_bf16 v[98:101], v[130:133], v[194:197], v[98:101]
	v_mfma_f32_16x16x32_bf16 v[90:93], v[138:141], v[194:197], v[90:93]
	v_mfma_f32_16x16x32_bf16 v[82:85], v[130:133], v[202:205], v[82:85]
	v_mfma_f32_16x16x32_bf16 v[74:77], v[138:141], v[202:205], v[74:77]
	v_mfma_f32_16x16x32_bf16 v[126:129], v[134:137], v[176:179], v[126:129]
	v_mfma_f32_16x16x32_bf16 v[122:125], v[142:145], v[176:179], v[122:125]
	v_mfma_f32_16x16x32_bf16 v[114:117], v[134:137], v[190:193], v[114:117]
	v_mfma_f32_16x16x32_bf16 v[106:109], v[142:145], v[190:193], v[106:109]
	v_mfma_f32_16x16x32_bf16 v[98:101], v[134:137], v[198:201], v[98:101]
	v_mfma_f32_16x16x32_bf16 v[90:93], v[142:145], v[198:201], v[90:93]
	v_mfma_f32_16x16x32_bf16 v[82:85], v[134:137], v[206:209], v[82:85]
	v_mfma_f32_16x16x32_bf16 v[74:77], v[142:145], v[206:209], v[74:77]
	v_mfma_f32_16x16x32_bf16 v[118:121], v[146:149], v[172:175], v[118:121]
	v_mfma_f32_16x16x32_bf16 v[110:113], v[154:157], v[172:175], v[110:113]
	v_mfma_f32_16x16x32_bf16 v[102:105], v[146:149], v[180:183], v[102:105]
	v_mfma_f32_16x16x32_bf16 v[94:97], v[154:157], v[180:183], v[94:97]
	v_mfma_f32_16x16x32_bf16 v[86:89], v[146:149], v[194:197], v[86:89]
	v_mfma_f32_16x16x32_bf16 v[78:81], v[154:157], v[194:197], v[78:81]
	v_mfma_f32_16x16x32_bf16 v[70:73], v[146:149], v[202:205], v[70:73]
	v_mfma_f32_16x16x32_bf16 v[66:69], v[154:157], v[202:205], v[66:69]
	v_mfma_f32_16x16x32_bf16 v[118:121], v[150:153], v[176:179], v[118:121]
	v_mfma_f32_16x16x32_bf16 v[110:113], v[168:171], v[176:179], v[110:113]
	v_mfma_f32_16x16x32_bf16 v[102:105], v[150:153], v[190:193], v[102:105]
	v_mfma_f32_16x16x32_bf16 v[94:97], v[168:171], v[190:193], v[94:97]
	v_mfma_f32_16x16x32_bf16 v[86:89], v[150:153], v[198:201], v[86:89]
	v_mfma_f32_16x16x32_bf16 v[78:81], v[168:171], v[198:201], v[78:81]
	v_mfma_f32_16x16x32_bf16 v[70:73], v[150:153], v[206:209], v[70:73]
	v_mfma_f32_16x16x32_bf16 v[66:69], v[168:171], v[206:209], v[66:69]
	s_setprio 0
	s_barrier
	s_add_i32 s30, s41, s42
	v_lshl_add_u64 v[216:217], v[216:217], 0, s[56:57]
	s_mov_b32 m0, s30
	ds_read_b128 v[172:175], v188 offset:49152
	ds_read_b128 v[176:179], v188 offset:50176
	ds_read_b128 v[180:183], v188 offset:51200
	ds_read_b128 v[190:193], v188 offset:52224
	ds_read_b128 v[194:197], v188 offset:53248
	ds_read_b128 v[198:201], v188 offset:54272
	ds_read_b128 v[202:205], v188 offset:55296
	ds_read_b128 v[206:209], v188 offset:56320
	global_load_lds_dwordx4 v[216:217], off
	s_add_i32 m0, s30, 0x2000
	s_add_u32 s28, s28, 0x40080
	v_lshl_add_u64 v[216:217], v[218:219], 0, s[56:57]
	s_addc_u32 s29, s29, 0
	s_add_i32 s30, s53, s42
	global_load_lds_dwordx4 v[216:217], off
	v_lshl_add_u64 v[216:217], s[28:29], 0, v[0:1]
	s_mov_b32 m0, s30
	s_nop 0
	global_load_lds_dwordx4 v[216:217], off
	v_lshl_add_u64 v[216:217], s[28:29], 0, v[158:159]
	s_add_i32 m0, s30, 0x2000
	s_nop 0
	global_load_lds_dwordx4 v[216:217], off
	v_lshl_add_u64 v[216:217], v[220:221], 0, s[56:57]
	s_mov_b32 m0, s47
	s_nop 0
	global_load_lds_dwordx4 v[216:217], off
	v_lshl_add_u64 v[216:217], v[222:223], 0, s[56:57]
	s_mov_b32 m0, s48
	s_nop 0
	global_load_lds_dwordx4 v[216:217], off
	s_waitcnt vmcnt(8)
	s_waitcnt lgkmcnt(0)
	s_barrier
	s_setprio 1
	s_waitcnt lgkmcnt(0)
	v_mfma_f32_16x16x32_bf16 v[62:65], v[130:133], v[172:175], v[62:65]
	v_mfma_f32_16x16x32_bf16 v[58:61], v[138:141], v[172:175], v[58:61]
	v_mfma_f32_16x16x32_bf16 v[50:53], v[130:133], v[180:183], v[50:53]
	v_mfma_f32_16x16x32_bf16 v[42:45], v[138:141], v[180:183], v[42:45]
	v_mfma_f32_16x16x32_bf16 v[34:37], v[130:133], v[194:197], v[34:37]
	v_mfma_f32_16x16x32_bf16 v[26:29], v[138:141], v[194:197], v[26:29]
	v_mfma_f32_16x16x32_bf16 v[18:21], v[130:133], v[202:205], v[18:21]
	v_mfma_f32_16x16x32_bf16 v[10:13], v[138:141], v[202:205], v[10:13]
	v_mfma_f32_16x16x32_bf16 v[62:65], v[134:137], v[176:179], v[62:65]
	v_mfma_f32_16x16x32_bf16 v[58:61], v[142:145], v[176:179], v[58:61]
	v_mfma_f32_16x16x32_bf16 v[50:53], v[134:137], v[190:193], v[50:53]
	v_mfma_f32_16x16x32_bf16 v[42:45], v[142:145], v[190:193], v[42:45]
	v_mfma_f32_16x16x32_bf16 v[34:37], v[134:137], v[198:201], v[34:37]
	v_mfma_f32_16x16x32_bf16 v[26:29], v[142:145], v[198:201], v[26:29]
	v_mfma_f32_16x16x32_bf16 v[18:21], v[134:137], v[206:209], v[18:21]
	v_mfma_f32_16x16x32_bf16 v[10:13], v[142:145], v[206:209], v[10:13]
	v_mfma_f32_16x16x32_bf16 v[54:57], v[146:149], v[172:175], v[54:57]
	v_mfma_f32_16x16x32_bf16 v[46:49], v[154:157], v[172:175], v[46:49]
	v_mfma_f32_16x16x32_bf16 v[38:41], v[146:149], v[180:183], v[38:41]
	v_mfma_f32_16x16x32_bf16 v[30:33], v[154:157], v[180:183], v[30:33]
	v_mfma_f32_16x16x32_bf16 v[22:25], v[146:149], v[194:197], v[22:25]
	v_mfma_f32_16x16x32_bf16 v[14:17], v[154:157], v[194:197], v[14:17]
	v_mfma_f32_16x16x32_bf16 v[6:9], v[146:149], v[202:205], v[6:9]
	v_mfma_f32_16x16x32_bf16 v[2:5], v[154:157], v[202:205], v[2:5]
	v_mfma_f32_16x16x32_bf16 v[54:57], v[150:153], v[176:179], v[54:57]
	v_mfma_f32_16x16x32_bf16 v[46:49], v[168:171], v[176:179], v[46:49]
	v_mfma_f32_16x16x32_bf16 v[38:41], v[150:153], v[190:193], v[38:41]
	v_mfma_f32_16x16x32_bf16 v[30:33], v[168:171], v[190:193], v[30:33]
	v_mfma_f32_16x16x32_bf16 v[22:25], v[150:153], v[198:201], v[22:25]
	v_mfma_f32_16x16x32_bf16 v[14:17], v[168:171], v[198:201], v[14:17]
	v_mfma_f32_16x16x32_bf16 v[6:9], v[150:153], v[206:209], v[6:9]
	v_mfma_f32_16x16x32_bf16 v[2:5], v[168:171], v[206:209], v[2:5]
	s_setprio 0
	s_barrier
	s_add_i32 s40, s40, 2
	s_add_u32 s23, s23, 0x100
	s_addc_u32 s33, s33, 0
	s_add_u32 s6, s6, 0x100
	s_addc_u32 s7, s7, 0
	s_cmp_gt_u32 s40, 13
	s_cbranch_scc0 .LBB0_836
	s_and_b64 vcc, exec, s[18:19]
	s_cbranch_vccz .LBB0_839
	s_barrier

.LBB0_1525:
	s_add_u32 s36, s26, s34
	s_addc_u32 s37, s27, s35
	s_add_u32 s36, s36, 0x100
	s_addc_u32 s37, s37, 0
	s_add_u32 s82, s8, s34
	s_addc_u32 s83, s9, s35
	s_add_i32 s84, 0, 0x10000
	s_cmpk_eq_i32 s34, 0xb00
	s_cselect_b32 s45, s31, s37
	s_cselect_b32 s44, s30, s36
	s_cselect_b32 s37, s29, s83
	s_cselect_b32 s36, s28, s82
	s_add_i32 s85, 0, 0x14000
	v_add_u32_e32 v158, s84, v144
	v_add_u32_e32 v176, s85, v144
	ds_read_b128 v[146:149], v158
	ds_read_b128 v[150:153], v158 offset:1024
	ds_read_b128 v[154:157], v158 offset:2048
	ds_read_b128 v[158:161], v158 offset:3072
	ds_read_b128 v[162:165], v176
	ds_read_b128 v[168:171], v176 offset:1024
	ds_read_b128 v[172:175], v176 offset:2048
	ds_read_b128 v[176:179], v176 offset:3072
	v_lshl_add_u64 v[208:209], v[142:143], 0, s[34:35]
	s_add_i32 m0, s4, 0xc000
	ds_read_b128 v[180:183], v145
	ds_read_b128 v[184:187], v145 offset:1024
	ds_read_b128 v[188:191], v145 offset:2048
	ds_read_b128 v[192:195], v145 offset:3072
	ds_read_b128 v[196:199], v145 offset:4096
	ds_read_b128 v[200:203], v145 offset:5120
	ds_read_b128 v[204:207], v145 offset:6144
	ds_read_b128 v[216:219], v145 offset:7168
	global_load_lds_dwordx4 v[208:209], off
	v_lshl_add_u64 v[208:209], v[140:141], 0, s[34:35]
	s_add_i32 m0, s4, 0xe000
	s_nop 0
	global_load_lds_dwordx4 v[208:209], off
	s_waitcnt vmcnt(8)
	s_waitcnt lgkmcnt(0)
	s_barrier
	s_setprio 1
	s_waitcnt lgkmcnt(0)
	v_mfma_f32_16x16x32_bf16 v[134:137], v[146:149], v[180:183], v[134:137]
	v_mfma_f32_16x16x32_bf16 v[130:133], v[154:157], v[180:183], v[130:133]
	v_mfma_f32_16x16x32_bf16 v[110:113], v[146:149], v[188:191], v[110:113]
	v_mfma_f32_16x16x32_bf16 v[106:109], v[154:157], v[188:191], v[106:109]
	v_mfma_f32_16x16x32_bf16 v[94:97], v[146:149], v[196:199], v[94:97]
	v_mfma_f32_16x16x32_bf16 v[90:93], v[154:157], v[196:199], v[90:93]
	v_mfma_f32_16x16x32_bf16 v[78:81], v[146:149], v[204:207], v[78:81]
	v_mfma_f32_16x16x32_bf16 v[74:77], v[154:157], v[204:207], v[74:77]
	v_mfma_f32_16x16x32_bf16 v[134:137], v[150:153], v[184:187], v[134:137]
	v_mfma_f32_16x16x32_bf16 v[130:133], v[158:161], v[184:187], v[130:133]
	v_mfma_f32_16x16x32_bf16 v[110:113], v[150:153], v[192:195], v[110:113]
	v_mfma_f32_16x16x32_bf16 v[106:109], v[158:161], v[192:195], v[106:109]
	v_mfma_f32_16x16x32_bf16 v[94:97], v[150:153], v[200:203], v[94:97]
	v_mfma_f32_16x16x32_bf16 v[90:93], v[158:161], v[200:203], v[90:93]
	v_mfma_f32_16x16x32_bf16 v[78:81], v[150:153], v[216:219], v[78:81]
	v_mfma_f32_16x16x32_bf16 v[74:77], v[158:161], v[216:219], v[74:77]
	v_mfma_f32_16x16x32_bf16 v[122:125], v[162:165], v[180:183], v[122:125]
	v_mfma_f32_16x16x32_bf16 v[114:117], v[172:175], v[180:183], v[114:117]
	v_mfma_f32_16x16x32_bf16 v[102:105], v[162:165], v[188:191], v[102:105]
	v_mfma_f32_16x16x32_bf16 v[98:101], v[172:175], v[188:191], v[98:101]
	v_mfma_f32_16x16x32_bf16 v[86:89], v[162:165], v[196:199], v[86:89]
	v_mfma_f32_16x16x32_bf16 v[82:85], v[172:175], v[196:199], v[82:85]
	v_mfma_f32_16x16x32_bf16 v[70:73], v[162:165], v[204:207], v[70:73]
	v_mfma_f32_16x16x32_bf16 v[66:69], v[172:175], v[204:207], v[66:69]
	v_mfma_f32_16x16x32_bf16 v[122:125], v[168:171], v[184:187], v[122:125]
	v_mfma_f32_16x16x32_bf16 v[114:117], v[176:179], v[184:187], v[114:117]
	v_mfma_f32_16x16x32_bf16 v[102:105], v[168:171], v[192:195], v[102:105]
	v_mfma_f32_16x16x32_bf16 v[98:101], v[176:179], v[192:195], v[98:101]
	v_mfma_f32_16x16x32_bf16 v[86:89], v[168:171], v[200:203], v[86:89]
	v_mfma_f32_16x16x32_bf16 v[82:85], v[176:179], v[200:203], v[82:85]
	v_mfma_f32_16x16x32_bf16 v[70:73], v[168:171], v[216:219], v[70:73]
	v_mfma_f32_16x16x32_bf16 v[66:69], v[176:179], v[216:219], v[66:69]
	s_setprio 0
	s_barrier
	s_add_i32 s82, s84, s70
	v_lshl_add_u64 v[208:209], s[36:37], 0, v[0:1]
	s_mov_b32 m0, s82
	ds_read_b128 v[180:183], v145 offset:16384
	ds_read_b128 v[184:187], v145 offset:17408
	ds_read_b128 v[188:191], v145 offset:18432
	ds_read_b128 v[192:195], v145 offset:19456
	ds_read_b128 v[196:199], v145 offset:20480
	ds_read_b128 v[200:203], v145 offset:21504
	ds_read_b128 v[204:207], v145 offset:22528
	ds_read_b128 v[216:219], v145 offset:23552
	global_load_lds_dwordx4 v[208:209], off
	s_add_i32 m0, s82, 0x2000
	s_add_u32 s82, s36, 0x60000
	v_lshl_add_u64 v[220:221], s[36:37], 0, v[118:119]
	s_addc_u32 s83, s37, 0
	s_add_i32 s84, s85, s70
	global_load_lds_dwordx4 v[220:221], off
	v_lshl_add_u64 v[222:223], s[82:83], 0, v[0:1]
	s_mov_b32 m0, s84
	v_lshl_add_u64 v[224:225], s[44:45], 0, v[120:121]
	global_load_lds_dwordx4 v[222:223], off
	v_lshl_add_u64 v[222:223], s[82:83], 0, v[118:119]
	s_add_i32 m0, s84, 0x2000
	s_nop 0
	global_load_lds_dwordx4 v[222:223], off
	v_lshl_add_u64 v[222:223], s[44:45], 0, v[126:127]
	s_mov_b32 m0, s4
	s_nop 0
	global_load_lds_dwordx4 v[222:223], off
	s_mov_b32 m0, s33
	s_nop 0
	global_load_lds_dwordx4 v[224:225], off
	s_waitcnt vmcnt(8)
	s_waitcnt lgkmcnt(0)
	s_barrier
	s_setprio 1
	s_waitcnt lgkmcnt(0)
	v_mfma_f32_16x16x32_bf16 v[62:65], v[146:149], v[180:183], v[62:65]
	v_mfma_f32_16x16x32_bf16 v[58:61], v[154:157], v[180:183], v[58:61]
	v_mfma_f32_16x16x32_bf16 v[46:49], v[146:149], v[188:191], v[46:49]
	v_mfma_f32_16x16x32_bf16 v[42:45], v[154:157], v[188:191], v[42:45]
	v_mfma_f32_16x16x32_bf16 v[30:33], v[146:149], v[196:199], v[30:33]
	v_mfma_f32_16x16x32_bf16 v[26:29], v[154:157], v[196:199], v[26:29]
	v_mfma_f32_16x16x32_bf16 v[14:17], v[146:149], v[204:207], v[14:17]
	v_mfma_f32_16x16x32_bf16 v[10:13], v[154:157], v[204:207], v[10:13]
	v_mfma_f32_16x16x32_bf16 v[62:65], v[150:153], v[184:187], v[62:65]
	v_mfma_f32_16x16x32_bf16 v[58:61], v[158:161], v[184:187], v[58:61]
	v_mfma_f32_16x16x32_bf16 v[46:49], v[150:153], v[192:195], v[46:49]
	v_mfma_f32_16x16x32_bf16 v[42:45], v[158:161], v[192:195], v[42:45]
	v_mfma_f32_16x16x32_bf16 v[30:33], v[150:153], v[200:203], v[30:33]
	v_mfma_f32_16x16x32_bf16 v[26:29], v[158:161], v[200:203], v[26:29]
	v_mfma_f32_16x16x32_bf16 v[14:17], v[150:153], v[216:219], v[14:17]
	v_mfma_f32_16x16x32_bf16 v[10:13], v[158:161], v[216:219], v[10:13]
	v_mfma_f32_16x16x32_bf16 v[54:57], v[162:165], v[180:183], v[54:57]
	v_mfma_f32_16x16x32_bf16 v[50:53], v[172:175], v[180:183], v[50:53]
	v_mfma_f32_16x16x32_bf16 v[38:41], v[162:165], v[188:191], v[38:41]
	v_mfma_f32_16x16x32_bf16 v[34:37], v[172:175], v[188:191], v[34:37]
	v_mfma_f32_16x16x32_bf16 v[22:25], v[162:165], v[196:199], v[22:25]
	v_mfma_f32_16x16x32_bf16 v[18:21], v[172:175], v[196:199], v[18:21]
	v_mfma_f32_16x16x32_bf16 v[6:9], v[162:165], v[204:207], v[6:9]
	v_mfma_f32_16x16x32_bf16 v[2:5], v[172:175], v[204:207], v[2:5]
	v_mfma_f32_16x16x32_bf16 v[54:57], v[168:171], v[184:187], v[54:57]
	v_mfma_f32_16x16x32_bf16 v[50:53], v[176:179], v[184:187], v[50:53]
	v_mfma_f32_16x16x32_bf16 v[38:41], v[168:171], v[192:195], v[38:41]
	v_mfma_f32_16x16x32_bf16 v[34:37], v[176:179], v[192:195], v[34:37]
	v_mfma_f32_16x16x32_bf16 v[22:25], v[168:171], v[200:203], v[22:25]
	v_mfma_f32_16x16x32_bf16 v[18:21], v[176:179], v[200:203], v[18:21]
	v_mfma_f32_16x16x32_bf16 v[6:9], v[168:171], v[216:219], v[6:9]
	v_mfma_f32_16x16x32_bf16 v[2:5], v[176:179], v[216:219], v[2:5]
	s_setprio 0
	s_barrier
	s_add_i32 s82, 0, 0x18000
	s_add_i32 s83, 0, 0x1c000
	v_add_u32_e32 v158, s82, v144
	v_add_u32_e32 v176, s83, v144
	ds_read_b128 v[146:149], v158
	ds_read_b128 v[150:153], v158 offset:1024
	ds_read_b128 v[154:157], v158 offset:2048
	ds_read_b128 v[158:161], v158 offset:3072
	ds_read_b128 v[162:165], v176
	ds_read_b128 v[168:171], v176 offset:1024
	ds_read_b128 v[172:175], v176 offset:2048
	ds_read_b128 v[176:179], v176 offset:3072
	s_add_u32 s44, s44, 0x60000
	s_addc_u32 s45, s45, 0
	s_mov_b32 m0, s71
	v_lshl_add_u64 v[242:243], s[44:45], 0, v[126:127]
	ds_read_b128 v[180:183], v145 offset:32768
	ds_read_b128 v[184:187], v145 offset:33792
	ds_read_b128 v[188:191], v145 offset:34816
	ds_read_b128 v[192:195], v145 offset:35840
	ds_read_b128 v[196:199], v145 offset:36864
	ds_read_b128 v[200:203], v145 offset:37888
	ds_read_b128 v[204:207], v145 offset:38912
	ds_read_b128 v[216:219], v145 offset:39936
	global_load_lds_dwordx4 v[242:243], off
	v_lshl_add_u64 v[242:243], s[44:45], 0, v[120:121]
	s_mov_b32 m0, s76
	s_nop 0
	global_load_lds_dwordx4 v[242:243], off
	s_waitcnt vmcnt(8)
	s_waitcnt lgkmcnt(0)
	s_barrier
	s_setprio 1
	s_waitcnt lgkmcnt(0)
	v_mfma_f32_16x16x32_bf16 v[134:137], v[146:149], v[180:183], v[134:137]
	v_mfma_f32_16x16x32_bf16 v[130:133], v[154:157], v[180:183], v[130:133]
	v_mfma_f32_16x16x32_bf16 v[110:113], v[146:149], v[188:191], v[110:113]
	v_mfma_f32_16x16x32_bf16 v[106:109], v[154:157], v[188:191], v[106:109]
	v_mfma_f32_16x16x32_bf16 v[94:97], v[146:149], v[196:199], v[94:97]
	v_mfma_f32_16x16x32_bf16 v[90:93], v[154:157], v[196:199], v[90:93]
	v_mfma_f32_16x16x32_bf16 v[78:81], v[146:149], v[204:207], v[78:81]
	v_mfma_f32_16x16x32_bf16 v[74:77], v[154:157], v[204:207], v[74:77]
	v_mfma_f32_16x16x32_bf16 v[134:137], v[150:153], v[184:187], v[134:137]
	v_mfma_f32_16x16x32_bf16 v[130:133], v[158:161], v[184:187], v[130:133]
	v_mfma_f32_16x16x32_bf16 v[110:113], v[150:153], v[192:195], v[110:113]
	v_mfma_f32_16x16x32_bf16 v[106:109], v[158:161], v[192:195], v[106:109]
	v_mfma_f32_16x16x32_bf16 v[94:97], v[150:153], v[200:203], v[94:97]
	v_mfma_f32_16x16x32_bf16 v[90:93], v[158:161], v[200:203], v[90:93]
	v_mfma_f32_16x16x32_bf16 v[78:81], v[150:153], v[216:219], v[78:81]
	v_mfma_f32_16x16x32_bf16 v[74:77], v[158:161], v[216:219], v[74:77]
	v_mfma_f32_16x16x32_bf16 v[122:125], v[162:165], v[180:183], v[122:125]
	v_mfma_f32_16x16x32_bf16 v[114:117], v[172:175], v[180:183], v[114:117]
	v_mfma_f32_16x16x32_bf16 v[102:105], v[162:165], v[188:191], v[102:105]
	v_mfma_f32_16x16x32_bf16 v[98:101], v[172:175], v[188:191], v[98:101]
	v_mfma_f32_16x16x32_bf16 v[86:89], v[162:165], v[196:199], v[86:89]
	v_mfma_f32_16x16x32_bf16 v[82:85], v[172:175], v[196:199], v[82:85]
	v_mfma_f32_16x16x32_bf16 v[70:73], v[162:165], v[204:207], v[70:73]
	v_mfma_f32_16x16x32_bf16 v[66:69], v[172:175], v[204:207], v[66:69]
	v_mfma_f32_16x16x32_bf16 v[122:125], v[168:171], v[184:187], v[122:125]
	v_mfma_f32_16x16x32_bf16 v[114:117], v[176:179], v[184:187], v[114:117]
	v_mfma_f32_16x16x32_bf16 v[102:105], v[168:171], v[192:195], v[102:105]
	v_mfma_f32_16x16x32_bf16 v[98:101], v[176:179], v[192:195], v[98:101]
	v_mfma_f32_16x16x32_bf16 v[86:89], v[168:171], v[200:203], v[86:89]
	v_mfma_f32_16x16x32_bf16 v[82:85], v[176:179], v[200:203], v[82:85]
	v_mfma_f32_16x16x32_bf16 v[70:73], v[168:171], v[216:219], v[70:73]
	v_mfma_f32_16x16x32_bf16 v[66:69], v[176:179], v[216:219], v[66:69]
	s_setprio 0
	s_barrier
	s_add_i32 s44, s82, s70
	v_lshl_add_u64 v[208:209], v[208:209], 0, s[56:57]
	s_mov_b32 m0, s44
	ds_read_b128 v[180:183], v145 offset:49152
	ds_read_b128 v[184:187], v145 offset:50176
	ds_read_b128 v[188:191], v145 offset:51200
	ds_read_b128 v[192:195], v145 offset:52224
	ds_read_b128 v[196:199], v145 offset:53248
	ds_read_b128 v[200:203], v145 offset:54272
	ds_read_b128 v[204:207], v145 offset:55296
	ds_read_b128 v[216:219], v145 offset:56320
	global_load_lds_dwordx4 v[208:209], off
	s_add_i32 m0, s44, 0x2000
	s_add_u32 s36, s36, 0x60080
	v_lshl_add_u64 v[208:209], v[220:221], 0, s[56:57]
	s_addc_u32 s37, s37, 0
	s_add_i32 s44, s83, s70
	global_load_lds_dwordx4 v[208:209], off
	v_lshl_add_u64 v[208:209], s[36:37], 0, v[0:1]
	s_mov_b32 m0, s44
	s_nop 0
	global_load_lds_dwordx4 v[208:209], off
	v_lshl_add_u64 v[208:209], s[36:37], 0, v[118:119]
	s_add_i32 m0, s44, 0x2000
	s_nop 0
	global_load_lds_dwordx4 v[208:209], off
	v_lshl_add_u64 v[208:209], v[222:223], 0, s[56:57]
	s_mov_b32 m0, s77
	s_nop 0
	global_load_lds_dwordx4 v[208:209], off
	v_lshl_add_u64 v[208:209], v[224:225], 0, s[56:57]
	s_mov_b32 m0, s79
	s_nop 0
	global_load_lds_dwordx4 v[208:209], off
	s_waitcnt vmcnt(8)
	s_waitcnt lgkmcnt(0)
	s_barrier
	s_setprio 1
	s_waitcnt lgkmcnt(0)
	v_mfma_f32_16x16x32_bf16 v[62:65], v[146:149], v[180:183], v[62:65]
	v_mfma_f32_16x16x32_bf16 v[58:61], v[154:157], v[180:183], v[58:61]
	v_mfma_f32_16x16x32_bf16 v[46:49], v[146:149], v[188:191], v[46:49]
	v_mfma_f32_16x16x32_bf16 v[42:45], v[154:157], v[188:191], v[42:45]
	v_mfma_f32_16x16x32_bf16 v[30:33], v[146:149], v[196:199], v[30:33]
	v_mfma_f32_16x16x32_bf16 v[26:29], v[154:157], v[196:199], v[26:29]
	v_mfma_f32_16x16x32_bf16 v[14:17], v[146:149], v[204:207], v[14:17]
	v_mfma_f32_16x16x32_bf16 v[10:13], v[154:157], v[204:207], v[10:13]
	v_mfma_f32_16x16x32_bf16 v[62:65], v[150:153], v[184:187], v[62:65]
	v_mfma_f32_16x16x32_bf16 v[58:61], v[158:161], v[184:187], v[58:61]
	v_mfma_f32_16x16x32_bf16 v[46:49], v[150:153], v[192:195], v[46:49]
	v_mfma_f32_16x16x32_bf16 v[42:45], v[158:161], v[192:195], v[42:45]
	v_mfma_f32_16x16x32_bf16 v[30:33], v[150:153], v[200:203], v[30:33]
	v_mfma_f32_16x16x32_bf16 v[26:29], v[158:161], v[200:203], v[26:29]
	v_mfma_f32_16x16x32_bf16 v[14:17], v[150:153], v[216:219], v[14:17]
	v_mfma_f32_16x16x32_bf16 v[10:13], v[158:161], v[216:219], v[10:13]
	v_mfma_f32_16x16x32_bf16 v[54:57], v[162:165], v[180:183], v[54:57]
	v_mfma_f32_16x16x32_bf16 v[50:53], v[172:175], v[180:183], v[50:53]
	v_mfma_f32_16x16x32_bf16 v[38:41], v[162:165], v[188:191], v[38:41]
	v_mfma_f32_16x16x32_bf16 v[34:37], v[172:175], v[188:191], v[34:37]
	v_mfma_f32_16x16x32_bf16 v[22:25], v[162:165], v[196:199], v[22:25]
	v_mfma_f32_16x16x32_bf16 v[18:21], v[172:175], v[196:199], v[18:21]
	v_mfma_f32_16x16x32_bf16 v[6:9], v[162:165], v[204:207], v[6:9]
	v_mfma_f32_16x16x32_bf16 v[2:5], v[172:175], v[204:207], v[2:5]
	v_mfma_f32_16x16x32_bf16 v[54:57], v[168:171], v[184:187], v[54:57]
	v_mfma_f32_16x16x32_bf16 v[50:53], v[176:179], v[184:187], v[50:53]
	v_mfma_f32_16x16x32_bf16 v[38:41], v[168:171], v[192:195], v[38:41]
	v_mfma_f32_16x16x32_bf16 v[34:37], v[176:179], v[192:195], v[34:37]
	v_mfma_f32_16x16x32_bf16 v[22:25], v[168:171], v[200:203], v[22:25]
	v_mfma_f32_16x16x32_bf16 v[18:21], v[176:179], v[200:203], v[18:21]
	v_mfma_f32_16x16x32_bf16 v[6:9], v[168:171], v[216:219], v[6:9]
	v_mfma_f32_16x16x32_bf16 v[2:5], v[176:179], v[216:219], v[2:5]
	s_setprio 0
	s_barrier
	s_add_i32 s59, s59, 2
	s_add_u32 s34, s34, 0x100
	s_addc_u32 s35, s35, 0
	s_cmp_gt_u32 s59, 21
	s_cbranch_scc0 .LBB0_1525
	s_add_u32 s34, s8, 0xffffff00
	s_addc_u32 s35, s9, -1
	s_and_b64 vcc, exec, s[42:43]
	s_cbranch_vccnz .LBB0_1528
	v_mov_b32_e32 v2, 0
	s_mov_b32 s16, s80
	s_mov_b32 s47, s81
	s_mov_b64 s[26:27], s[30:31]
	s_mov_b32 s68, s58
	v_mov_b32_e32 v3, v2
	v_mov_b32_e32 v4, v2
	v_mov_b32_e32 v5, v2
	v_mov_b32_e32 v6, v2
	v_mov_b32_e32 v7, v2
	v_mov_b32_e32 v8, v2
	v_mov_b32_e32 v9, v2
	v_mov_b32_e32 v18, v2
	v_mov_b32_e32 v19, v2
	v_mov_b32_e32 v20, v2
	v_mov_b32_e32 v21, v2
	v_mov_b32_e32 v22, v2
	v_mov_b32_e32 v23, v2
	v_mov_b32_e32 v24, v2
	v_mov_b32_e32 v25, v2
	v_mov_b32_e32 v34, v2
	v_mov_b32_e32 v35, v2
	v_mov_b32_e32 v36, v2
	v_mov_b32_e32 v37, v2
	v_mov_b32_e32 v38, v2
	v_mov_b32_e32 v39, v2
	v_mov_b32_e32 v40, v2
	v_mov_b32_e32 v41, v2
	v_mov_b32_e32 v50, v2
	v_mov_b32_e32 v51, v2
	v_mov_b32_e32 v52, v2
	v_mov_b32_e32 v53, v2
	v_mov_b32_e32 v54, v2
	v_mov_b32_e32 v55, v2
	v_mov_b32_e32 v56, v2
	v_mov_b32_e32 v57, v2
	v_mov_b32_e32 v10, v2
	v_mov_b32_e32 v11, v2
	v_mov_b32_e32 v12, v2
	v_mov_b32_e32 v13, v2
	v_mov_b32_e32 v14, v2
	v_mov_b32_e32 v15, v2
	v_mov_b32_e32 v16, v2
	v_mov_b32_e32 v17, v2
	v_mov_b32_e32 v26, v2
	v_mov_b32_e32 v27, v2
	v_mov_b32_e32 v28, v2
	v_mov_b32_e32 v29, v2
	v_mov_b32_e32 v30, v2
	v_mov_b32_e32 v31, v2
	v_mov_b32_e32 v32, v2
	v_mov_b32_e32 v33, v2
	v_mov_b32_e32 v42, v2
	v_mov_b32_e32 v43, v2
	v_mov_b32_e32 v44, v2
	v_mov_b32_e32 v45, v2
	v_mov_b32_e32 v46, v2
	v_mov_b32_e32 v47, v2
	v_mov_b32_e32 v48, v2
	v_mov_b32_e32 v49, v2
	v_mov_b32_e32 v58, v2
	v_mov_b32_e32 v59, v2
	v_mov_b32_e32 v60, v2
	v_mov_b32_e32 v61, v2
	v_mov_b32_e32 v62, v2
	v_mov_b32_e32 v63, v2
	v_mov_b32_e32 v64, v2
	v_mov_b32_e32 v65, v2
	v_mov_b32_e32 v66, v2
	v_mov_b32_e32 v67, v2
	v_mov_b32_e32 v68, v2
	v_mov_b32_e32 v69, v2
	v_mov_b32_e32 v70, v2
	v_mov_b32_e32 v71, v2
	v_mov_b32_e32 v72, v2
	v_mov_b32_e32 v73, v2
	v_mov_b32_e32 v82, v2
	v_mov_b32_e32 v83, v2
	v_mov_b32_e32 v84, v2
	v_mov_b32_e32 v85, v2
	v_mov_b32_e32 v86, v2
	v_mov_b32_e32 v87, v2
	v_mov_b32_e32 v88, v2
	v_mov_b32_e32 v89, v2
	v_mov_b32_e32 v98, v2
	v_mov_b32_e32 v99, v2
	v_mov_b32_e32 v100, v2
	v_mov_b32_e32 v101, v2
	v_mov_b32_e32 v102, v2
	v_mov_b32_e32 v103, v2
	v_mov_b32_e32 v104, v2
	v_mov_b32_e32 v105, v2
	v_mov_b32_e32 v114, v2
	v_mov_b32_e32 v115, v2
	v_mov_b32_e32 v116, v2
	v_mov_b32_e32 v117, v2
	v_mov_b32_e32 v122, v2
	v_mov_b32_e32 v123, v2
	v_mov_b32_e32 v124, v2
	v_mov_b32_e32 v125, v2
	v_mov_b32_e32 v74, v2
	v_mov_b32_e32 v75, v2
	v_mov_b32_e32 v76, v2
	v_mov_b32_e32 v77, v2
	v_mov_b32_e32 v78, v2
	v_mov_b32_e32 v79, v2
	v_mov_b32_e32 v80, v2
	v_mov_b32_e32 v81, v2
	v_mov_b32_e32 v90, v2
	v_mov_b32_e32 v91, v2
	v_mov_b32_e32 v92, v2
	v_mov_b32_e32 v93, v2
	v_mov_b32_e32 v94, v2
	v_mov_b32_e32 v95, v2
	v_mov_b32_e32 v96, v2
	v_mov_b32_e32 v97, v2
	v_mov_b32_e32 v106, v2
	v_mov_b32_e32 v107, v2
	v_mov_b32_e32 v108, v2
	v_mov_b32_e32 v109, v2
	v_mov_b32_e32 v110, v2
	v_mov_b32_e32 v111, v2
	v_mov_b32_e32 v112, v2
	v_mov_b32_e32 v113, v2
	v_mov_b32_e32 v130, v2
	v_mov_b32_e32 v131, v2
	v_mov_b32_e32 v132, v2
	v_mov_b32_e32 v133, v2
	v_mov_b32_e32 v134, v2
	v_mov_b32_e32 v135, v2
	v_mov_b32_e32 v136, v2
	v_mov_b32_e32 v137, v2
	s_andn2_b64 vcc, exec, s[40:41]
	s_cbranch_vccnz .LBB0_1529
	s_branch .LBB0_1531

.LBB0_1623:
	s_add_u32 s36, s26, s34
	s_addc_u32 s37, s27, s35
	s_add_u32 s36, s36, 0x100
	s_addc_u32 s37, s37, 0
	s_add_u32 s80, s8, s34
	s_addc_u32 s81, s9, s35
	s_add_i32 s82, 0, 0x10000
	s_cmpk_eq_i32 s34, 0xb00
	s_cselect_b32 s43, s31, s37
	s_cselect_b32 s42, s30, s36
	s_cselect_b32 s37, s29, s81
	s_cselect_b32 s36, s28, s80
	s_add_i32 s83, 0, 0x14000
	v_add_u32_e32 v158, s82, v144
	v_add_u32_e32 v167, s83, v144
	ds_read_b128 v[146:149], v158
	ds_read_b128 v[150:153], v158 offset:1024
	ds_read_b128 v[154:157], v158 offset:2048
	ds_read_b128 v[158:161], v158 offset:3072
	ds_read_b128 v[162:165], v167
	ds_read_b128 v[168:171], v167 offset:1024
	ds_read_b128 v[172:175], v167 offset:2048
	ds_read_b128 v[176:179], v167 offset:3072
	v_lshl_add_u64 v[208:209], v[142:143], 0, s[34:35]
	s_add_i32 m0, s4, 0xc000
	ds_read_b128 v[180:183], v145
	ds_read_b128 v[184:187], v145 offset:1024
	ds_read_b128 v[188:191], v145 offset:2048
	ds_read_b128 v[192:195], v145 offset:3072
	ds_read_b128 v[196:199], v145 offset:4096
	ds_read_b128 v[200:203], v145 offset:5120
	ds_read_b128 v[204:207], v145 offset:6144
	ds_read_b128 v[216:219], v145 offset:7168
	global_load_lds_dwordx4 v[208:209], off
	v_lshl_add_u64 v[208:209], v[140:141], 0, s[34:35]
	s_add_i32 m0, s4, 0xe000
	s_nop 0
	global_load_lds_dwordx4 v[208:209], off
	s_waitcnt vmcnt(8)
	s_waitcnt lgkmcnt(0)
	s_barrier
	s_setprio 1
	s_waitcnt lgkmcnt(0)
	v_mfma_f32_16x16x32_bf16 v[134:137], v[146:149], v[180:183], v[134:137]
	v_mfma_f32_16x16x32_bf16 v[130:133], v[154:157], v[180:183], v[130:133]
	v_mfma_f32_16x16x32_bf16 v[110:113], v[146:149], v[188:191], v[110:113]
	v_mfma_f32_16x16x32_bf16 v[106:109], v[154:157], v[188:191], v[106:109]
	v_mfma_f32_16x16x32_bf16 v[94:97], v[146:149], v[196:199], v[94:97]
	v_mfma_f32_16x16x32_bf16 v[90:93], v[154:157], v[196:199], v[90:93]
	v_mfma_f32_16x16x32_bf16 v[78:81], v[146:149], v[204:207], v[78:81]
	v_mfma_f32_16x16x32_bf16 v[74:77], v[154:157], v[204:207], v[74:77]
	v_mfma_f32_16x16x32_bf16 v[134:137], v[150:153], v[184:187], v[134:137]
	v_mfma_f32_16x16x32_bf16 v[130:133], v[158:161], v[184:187], v[130:133]
	v_mfma_f32_16x16x32_bf16 v[110:113], v[150:153], v[192:195], v[110:113]
	v_mfma_f32_16x16x32_bf16 v[106:109], v[158:161], v[192:195], v[106:109]
	v_mfma_f32_16x16x32_bf16 v[94:97], v[150:153], v[200:203], v[94:97]
	v_mfma_f32_16x16x32_bf16 v[90:93], v[158:161], v[200:203], v[90:93]
	v_mfma_f32_16x16x32_bf16 v[78:81], v[150:153], v[216:219], v[78:81]
	v_mfma_f32_16x16x32_bf16 v[74:77], v[158:161], v[216:219], v[74:77]
	v_mfma_f32_16x16x32_bf16 v[122:125], v[162:165], v[180:183], v[122:125]
	v_mfma_f32_16x16x32_bf16 v[114:117], v[172:175], v[180:183], v[114:117]
	v_mfma_f32_16x16x32_bf16 v[102:105], v[162:165], v[188:191], v[102:105]
	v_mfma_f32_16x16x32_bf16 v[98:101], v[172:175], v[188:191], v[98:101]
	v_mfma_f32_16x16x32_bf16 v[86:89], v[162:165], v[196:199], v[86:89]
	v_mfma_f32_16x16x32_bf16 v[82:85], v[172:175], v[196:199], v[82:85]
	v_mfma_f32_16x16x32_bf16 v[70:73], v[162:165], v[204:207], v[70:73]
	v_mfma_f32_16x16x32_bf16 v[66:69], v[172:175], v[204:207], v[66:69]
	v_mfma_f32_16x16x32_bf16 v[122:125], v[168:171], v[184:187], v[122:125]
	v_mfma_f32_16x16x32_bf16 v[114:117], v[176:179], v[184:187], v[114:117]
	v_mfma_f32_16x16x32_bf16 v[102:105], v[168:171], v[192:195], v[102:105]
	v_mfma_f32_16x16x32_bf16 v[98:101], v[176:179], v[192:195], v[98:101]
	v_mfma_f32_16x16x32_bf16 v[86:89], v[168:171], v[200:203], v[86:89]
	v_mfma_f32_16x16x32_bf16 v[82:85], v[176:179], v[200:203], v[82:85]
	v_mfma_f32_16x16x32_bf16 v[70:73], v[168:171], v[216:219], v[70:73]
	v_mfma_f32_16x16x32_bf16 v[66:69], v[176:179], v[216:219], v[66:69]
	s_setprio 0
	s_barrier
	s_add_i32 s80, s82, s53
	v_lshl_add_u64 v[208:209], s[36:37], 0, v[0:1]
	s_mov_b32 m0, s80
	ds_read_b128 v[180:183], v145 offset:16384
	ds_read_b128 v[184:187], v145 offset:17408
	ds_read_b128 v[188:191], v145 offset:18432
	ds_read_b128 v[192:195], v145 offset:19456
	ds_read_b128 v[196:199], v145 offset:20480
	ds_read_b128 v[200:203], v145 offset:21504
	ds_read_b128 v[204:207], v145 offset:22528
	ds_read_b128 v[216:219], v145 offset:23552
	global_load_lds_dwordx4 v[208:209], off
	s_add_i32 m0, s80, 0x2000
	s_add_u32 s80, s36, 0x60000
	v_lshl_add_u64 v[220:221], s[36:37], 0, v[118:119]
	s_addc_u32 s81, s37, 0
	s_add_i32 s82, s83, s53
	global_load_lds_dwordx4 v[220:221], off
	v_lshl_add_u64 v[222:223], s[80:81], 0, v[0:1]
	s_mov_b32 m0, s82
	v_lshl_add_u64 v[224:225], s[42:43], 0, v[120:121]
	global_load_lds_dwordx4 v[222:223], off
	v_lshl_add_u64 v[222:223], s[80:81], 0, v[118:119]
	s_add_i32 m0, s82, 0x2000
	s_nop 0
	global_load_lds_dwordx4 v[222:223], off
	v_lshl_add_u64 v[222:223], s[42:43], 0, v[126:127]
	s_mov_b32 m0, s4
	s_nop 0
	global_load_lds_dwordx4 v[222:223], off
	s_mov_b32 m0, s33
	s_nop 0
	global_load_lds_dwordx4 v[224:225], off
	s_waitcnt vmcnt(8)
	s_waitcnt lgkmcnt(0)
	s_barrier
	s_setprio 1
	s_waitcnt lgkmcnt(0)
	v_mfma_f32_16x16x32_bf16 v[62:65], v[146:149], v[180:183], v[62:65]
	v_mfma_f32_16x16x32_bf16 v[58:61], v[154:157], v[180:183], v[58:61]
	v_mfma_f32_16x16x32_bf16 v[46:49], v[146:149], v[188:191], v[46:49]
	v_mfma_f32_16x16x32_bf16 v[42:45], v[154:157], v[188:191], v[42:45]
	v_mfma_f32_16x16x32_bf16 v[30:33], v[146:149], v[196:199], v[30:33]
	v_mfma_f32_16x16x32_bf16 v[26:29], v[154:157], v[196:199], v[26:29]
	v_mfma_f32_16x16x32_bf16 v[14:17], v[146:149], v[204:207], v[14:17]
	v_mfma_f32_16x16x32_bf16 v[10:13], v[154:157], v[204:207], v[10:13]
	v_mfma_f32_16x16x32_bf16 v[62:65], v[150:153], v[184:187], v[62:65]
	v_mfma_f32_16x16x32_bf16 v[58:61], v[158:161], v[184:187], v[58:61]
	v_mfma_f32_16x16x32_bf16 v[46:49], v[150:153], v[192:195], v[46:49]
	v_mfma_f32_16x16x32_bf16 v[42:45], v[158:161], v[192:195], v[42:45]
	v_mfma_f32_16x16x32_bf16 v[30:33], v[150:153], v[200:203], v[30:33]
	v_mfma_f32_16x16x32_bf16 v[26:29], v[158:161], v[200:203], v[26:29]
	v_mfma_f32_16x16x32_bf16 v[14:17], v[150:153], v[216:219], v[14:17]
	v_mfma_f32_16x16x32_bf16 v[10:13], v[158:161], v[216:219], v[10:13]
	v_mfma_f32_16x16x32_bf16 v[54:57], v[162:165], v[180:183], v[54:57]
	v_mfma_f32_16x16x32_bf16 v[50:53], v[172:175], v[180:183], v[50:53]
	v_mfma_f32_16x16x32_bf16 v[38:41], v[162:165], v[188:191], v[38:41]
	v_mfma_f32_16x16x32_bf16 v[34:37], v[172:175], v[188:191], v[34:37]
	v_mfma_f32_16x16x32_bf16 v[22:25], v[162:165], v[196:199], v[22:25]
	v_mfma_f32_16x16x32_bf16 v[18:21], v[172:175], v[196:199], v[18:21]
	v_mfma_f32_16x16x32_bf16 v[6:9], v[162:165], v[204:207], v[6:9]
	v_mfma_f32_16x16x32_bf16 v[2:5], v[172:175], v[204:207], v[2:5]
	v_mfma_f32_16x16x32_bf16 v[54:57], v[168:171], v[184:187], v[54:57]
	v_mfma_f32_16x16x32_bf16 v[50:53], v[176:179], v[184:187], v[50:53]
	v_mfma_f32_16x16x32_bf16 v[38:41], v[168:171], v[192:195], v[38:41]
	v_mfma_f32_16x16x32_bf16 v[34:37], v[176:179], v[192:195], v[34:37]
	v_mfma_f32_16x16x32_bf16 v[22:25], v[168:171], v[200:203], v[22:25]
	v_mfma_f32_16x16x32_bf16 v[18:21], v[176:179], v[200:203], v[18:21]
	v_mfma_f32_16x16x32_bf16 v[6:9], v[168:171], v[216:219], v[6:9]
	v_mfma_f32_16x16x32_bf16 v[2:5], v[176:179], v[216:219], v[2:5]
	s_setprio 0
	s_barrier
	s_add_i32 s80, 0, 0x18000
	s_add_i32 s81, 0, 0x1c000
	v_add_u32_e32 v158, s80, v144
	v_add_u32_e32 v167, s81, v144
	ds_read_b128 v[146:149], v158
	ds_read_b128 v[150:153], v158 offset:1024
	ds_read_b128 v[154:157], v158 offset:2048
	ds_read_b128 v[158:161], v158 offset:3072
	ds_read_b128 v[162:165], v167
	ds_read_b128 v[168:171], v167 offset:1024
	ds_read_b128 v[172:175], v167 offset:2048
	ds_read_b128 v[176:179], v167 offset:3072
	s_add_u32 s42, s42, 0x60000
	s_addc_u32 s43, s43, 0
	s_mov_b32 m0, s62
	v_lshl_add_u64 v[242:243], s[42:43], 0, v[126:127]
	ds_read_b128 v[180:183], v145 offset:32768
	ds_read_b128 v[184:187], v145 offset:33792
	ds_read_b128 v[188:191], v145 offset:34816
	ds_read_b128 v[192:195], v145 offset:35840
	ds_read_b128 v[196:199], v145 offset:36864
	ds_read_b128 v[200:203], v145 offset:37888
	ds_read_b128 v[204:207], v145 offset:38912
	ds_read_b128 v[216:219], v145 offset:39936
	global_load_lds_dwordx4 v[242:243], off
	v_lshl_add_u64 v[242:243], s[42:43], 0, v[120:121]
	s_mov_b32 m0, s63
	s_nop 0
	global_load_lds_dwordx4 v[242:243], off
	s_waitcnt vmcnt(8)
	s_waitcnt lgkmcnt(0)
	s_barrier
	s_setprio 1
	s_waitcnt lgkmcnt(0)
	v_mfma_f32_16x16x32_bf16 v[134:137], v[146:149], v[180:183], v[134:137]
	v_mfma_f32_16x16x32_bf16 v[130:133], v[154:157], v[180:183], v[130:133]
	v_mfma_f32_16x16x32_bf16 v[110:113], v[146:149], v[188:191], v[110:113]
	v_mfma_f32_16x16x32_bf16 v[106:109], v[154:157], v[188:191], v[106:109]
	v_mfma_f32_16x16x32_bf16 v[94:97], v[146:149], v[196:199], v[94:97]
	v_mfma_f32_16x16x32_bf16 v[90:93], v[154:157], v[196:199], v[90:93]
	v_mfma_f32_16x16x32_bf16 v[78:81], v[146:149], v[204:207], v[78:81]
	v_mfma_f32_16x16x32_bf16 v[74:77], v[154:157], v[204:207], v[74:77]
	v_mfma_f32_16x16x32_bf16 v[134:137], v[150:153], v[184:187], v[134:137]
	v_mfma_f32_16x16x32_bf16 v[130:133], v[158:161], v[184:187], v[130:133]
	v_mfma_f32_16x16x32_bf16 v[110:113], v[150:153], v[192:195], v[110:113]
	v_mfma_f32_16x16x32_bf16 v[106:109], v[158:161], v[192:195], v[106:109]
	v_mfma_f32_16x16x32_bf16 v[94:97], v[150:153], v[200:203], v[94:97]
	v_mfma_f32_16x16x32_bf16 v[90:93], v[158:161], v[200:203], v[90:93]
	v_mfma_f32_16x16x32_bf16 v[78:81], v[150:153], v[216:219], v[78:81]
	v_mfma_f32_16x16x32_bf16 v[74:77], v[158:161], v[216:219], v[74:77]
	v_mfma_f32_16x16x32_bf16 v[122:125], v[162:165], v[180:183], v[122:125]
	v_mfma_f32_16x16x32_bf16 v[114:117], v[172:175], v[180:183], v[114:117]
	v_mfma_f32_16x16x32_bf16 v[102:105], v[162:165], v[188:191], v[102:105]
	v_mfma_f32_16x16x32_bf16 v[98:101], v[172:175], v[188:191], v[98:101]
	v_mfma_f32_16x16x32_bf16 v[86:89], v[162:165], v[196:199], v[86:89]
	v_mfma_f32_16x16x32_bf16 v[82:85], v[172:175], v[196:199], v[82:85]
	v_mfma_f32_16x16x32_bf16 v[70:73], v[162:165], v[204:207], v[70:73]
	v_mfma_f32_16x16x32_bf16 v[66:69], v[172:175], v[204:207], v[66:69]
	v_mfma_f32_16x16x32_bf16 v[122:125], v[168:171], v[184:187], v[122:125]
	v_mfma_f32_16x16x32_bf16 v[114:117], v[176:179], v[184:187], v[114:117]
	v_mfma_f32_16x16x32_bf16 v[102:105], v[168:171], v[192:195], v[102:105]
	v_mfma_f32_16x16x32_bf16 v[98:101], v[176:179], v[192:195], v[98:101]
	v_mfma_f32_16x16x32_bf16 v[86:89], v[168:171], v[200:203], v[86:89]
	v_mfma_f32_16x16x32_bf16 v[82:85], v[176:179], v[200:203], v[82:85]
	v_mfma_f32_16x16x32_bf16 v[70:73], v[168:171], v[216:219], v[70:73]
	v_mfma_f32_16x16x32_bf16 v[66:69], v[176:179], v[216:219], v[66:69]
	s_setprio 0
	s_barrier
	s_add_i32 s42, s80, s53
	v_lshl_add_u64 v[208:209], v[208:209], 0, s[56:57]
	s_mov_b32 m0, s42
	ds_read_b128 v[180:183], v145 offset:49152
	ds_read_b128 v[184:187], v145 offset:50176
	ds_read_b128 v[188:191], v145 offset:51200
	ds_read_b128 v[192:195], v145 offset:52224
	ds_read_b128 v[196:199], v145 offset:53248
	ds_read_b128 v[200:203], v145 offset:54272
	ds_read_b128 v[204:207], v145 offset:55296
	ds_read_b128 v[216:219], v145 offset:56320
	global_load_lds_dwordx4 v[208:209], off
	s_add_i32 m0, s42, 0x2000
	s_add_u32 s36, s36, 0x60080
	v_lshl_add_u64 v[208:209], v[220:221], 0, s[56:57]
	s_addc_u32 s37, s37, 0
	s_add_i32 s42, s81, s53
	global_load_lds_dwordx4 v[208:209], off
	v_lshl_add_u64 v[208:209], s[36:37], 0, v[0:1]
	s_mov_b32 m0, s42
	s_nop 0
	global_load_lds_dwordx4 v[208:209], off
	v_lshl_add_u64 v[208:209], s[36:37], 0, v[118:119]
	s_add_i32 m0, s42, 0x2000
	s_nop 0
	global_load_lds_dwordx4 v[208:209], off
	v_lshl_add_u64 v[208:209], v[222:223], 0, s[56:57]
	s_mov_b32 m0, s70
	s_nop 0
	global_load_lds_dwordx4 v[208:209], off
	v_lshl_add_u64 v[208:209], v[224:225], 0, s[56:57]
	s_mov_b32 m0, s71
	s_nop 0
	global_load_lds_dwordx4 v[208:209], off
	s_waitcnt vmcnt(8)
	s_waitcnt lgkmcnt(0)
	s_barrier
	s_setprio 1
	s_waitcnt lgkmcnt(0)
	v_mfma_f32_16x16x32_bf16 v[62:65], v[146:149], v[180:183], v[62:65]
	v_mfma_f32_16x16x32_bf16 v[58:61], v[154:157], v[180:183], v[58:61]
	v_mfma_f32_16x16x32_bf16 v[46:49], v[146:149], v[188:191], v[46:49]
	v_mfma_f32_16x16x32_bf16 v[42:45], v[154:157], v[188:191], v[42:45]
	v_mfma_f32_16x16x32_bf16 v[30:33], v[146:149], v[196:199], v[30:33]
	v_mfma_f32_16x16x32_bf16 v[26:29], v[154:157], v[196:199], v[26:29]
	v_mfma_f32_16x16x32_bf16 v[14:17], v[146:149], v[204:207], v[14:17]
	v_mfma_f32_16x16x32_bf16 v[10:13], v[154:157], v[204:207], v[10:13]
	v_mfma_f32_16x16x32_bf16 v[62:65], v[150:153], v[184:187], v[62:65]
	v_mfma_f32_16x16x32_bf16 v[58:61], v[158:161], v[184:187], v[58:61]
	v_mfma_f32_16x16x32_bf16 v[46:49], v[150:153], v[192:195], v[46:49]
	v_mfma_f32_16x16x32_bf16 v[42:45], v[158:161], v[192:195], v[42:45]
	v_mfma_f32_16x16x32_bf16 v[30:33], v[150:153], v[200:203], v[30:33]
	v_mfma_f32_16x16x32_bf16 v[26:29], v[158:161], v[200:203], v[26:29]
	v_mfma_f32_16x16x32_bf16 v[14:17], v[150:153], v[216:219], v[14:17]
	v_mfma_f32_16x16x32_bf16 v[10:13], v[158:161], v[216:219], v[10:13]
	v_mfma_f32_16x16x32_bf16 v[54:57], v[162:165], v[180:183], v[54:57]
	v_mfma_f32_16x16x32_bf16 v[50:53], v[172:175], v[180:183], v[50:53]
	v_mfma_f32_16x16x32_bf16 v[38:41], v[162:165], v[188:191], v[38:41]
	v_mfma_f32_16x16x32_bf16 v[34:37], v[172:175], v[188:191], v[34:37]
	v_mfma_f32_16x16x32_bf16 v[22:25], v[162:165], v[196:199], v[22:25]
	v_mfma_f32_16x16x32_bf16 v[18:21], v[172:175], v[196:199], v[18:21]
	v_mfma_f32_16x16x32_bf16 v[6:9], v[162:165], v[204:207], v[6:9]
	v_mfma_f32_16x16x32_bf16 v[2:5], v[172:175], v[204:207], v[2:5]
	v_mfma_f32_16x16x32_bf16 v[54:57], v[168:171], v[184:187], v[54:57]
	v_mfma_f32_16x16x32_bf16 v[50:53], v[176:179], v[184:187], v[50:53]
	v_mfma_f32_16x16x32_bf16 v[38:41], v[168:171], v[192:195], v[38:41]
	v_mfma_f32_16x16x32_bf16 v[34:37], v[176:179], v[192:195], v[34:37]
	v_mfma_f32_16x16x32_bf16 v[22:25], v[168:171], v[200:203], v[22:25]
	v_mfma_f32_16x16x32_bf16 v[18:21], v[176:179], v[200:203], v[18:21]
	v_mfma_f32_16x16x32_bf16 v[6:9], v[168:171], v[216:219], v[6:9]
	v_mfma_f32_16x16x32_bf16 v[2:5], v[176:179], v[216:219], v[2:5]
	s_setprio 0
	s_barrier
	s_add_i32 s59, s59, 2
	s_add_u32 s34, s34, 0x100
	s_addc_u32 s35, s35, 0
	s_cmp_gt_u32 s59, 21
	s_cbranch_scc0 .LBB0_1623
	s_add_u32 s34, s8, 0xffffff00
	s_addc_u32 s35, s9, -1
	s_and_b64 vcc, exec, s[40:41]
	s_cbranch_vccnz .LBB0_1626
	v_mov_b32_e32 v2, 0
	s_mov_b32 s16, s77
	s_mov_b32 s76, s79
	s_mov_b64 s[26:27], s[30:31]
	s_mov_b32 s68, s58
	v_mov_b32_e32 v3, v2
	v_mov_b32_e32 v4, v2
	v_mov_b32_e32 v5, v2
	v_mov_b32_e32 v6, v2
	v_mov_b32_e32 v7, v2
	v_mov_b32_e32 v8, v2
	v_mov_b32_e32 v9, v2
	v_mov_b32_e32 v18, v2
	v_mov_b32_e32 v19, v2
	v_mov_b32_e32 v20, v2
	v_mov_b32_e32 v21, v2
	v_mov_b32_e32 v22, v2
	v_mov_b32_e32 v23, v2
	v_mov_b32_e32 v24, v2
	v_mov_b32_e32 v25, v2
	v_mov_b32_e32 v34, v2
	v_mov_b32_e32 v35, v2
	v_mov_b32_e32 v36, v2
	v_mov_b32_e32 v37, v2
	v_mov_b32_e32 v38, v2
	v_mov_b32_e32 v39, v2
	v_mov_b32_e32 v40, v2
	v_mov_b32_e32 v41, v2
	v_mov_b32_e32 v50, v2
	v_mov_b32_e32 v51, v2
	v_mov_b32_e32 v52, v2
	v_mov_b32_e32 v53, v2
	v_mov_b32_e32 v54, v2
	v_mov_b32_e32 v55, v2
	v_mov_b32_e32 v56, v2
	v_mov_b32_e32 v57, v2
	v_mov_b32_e32 v10, v2
	v_mov_b32_e32 v11, v2
	v_mov_b32_e32 v12, v2
	v_mov_b32_e32 v13, v2
	v_mov_b32_e32 v14, v2
	v_mov_b32_e32 v15, v2
	v_mov_b32_e32 v16, v2
	v_mov_b32_e32 v17, v2
	v_mov_b32_e32 v26, v2
	v_mov_b32_e32 v27, v2
	v_mov_b32_e32 v28, v2
	v_mov_b32_e32 v29, v2
	v_mov_b32_e32 v30, v2
	v_mov_b32_e32 v31, v2
	v_mov_b32_e32 v32, v2
	v_mov_b32_e32 v33, v2
	v_mov_b32_e32 v42, v2
	v_mov_b32_e32 v43, v2
	v_mov_b32_e32 v44, v2
	v_mov_b32_e32 v45, v2
	v_mov_b32_e32 v46, v2
	v_mov_b32_e32 v47, v2
	v_mov_b32_e32 v48, v2
	v_mov_b32_e32 v49, v2
	v_mov_b32_e32 v58, v2
	v_mov_b32_e32 v59, v2
	v_mov_b32_e32 v60, v2
	v_mov_b32_e32 v61, v2
	v_mov_b32_e32 v62, v2
	v_mov_b32_e32 v63, v2
	v_mov_b32_e32 v64, v2
	v_mov_b32_e32 v65, v2
	v_mov_b32_e32 v66, v2
	v_mov_b32_e32 v67, v2
	v_mov_b32_e32 v68, v2
	v_mov_b32_e32 v69, v2
	v_mov_b32_e32 v70, v2
	v_mov_b32_e32 v71, v2
	v_mov_b32_e32 v72, v2
	v_mov_b32_e32 v73, v2
	v_mov_b32_e32 v82, v2
	v_mov_b32_e32 v83, v2
	v_mov_b32_e32 v84, v2
	v_mov_b32_e32 v85, v2
	v_mov_b32_e32 v86, v2
	v_mov_b32_e32 v87, v2
	v_mov_b32_e32 v88, v2
	v_mov_b32_e32 v89, v2
	v_mov_b32_e32 v98, v2
	v_mov_b32_e32 v99, v2
	v_mov_b32_e32 v100, v2
	v_mov_b32_e32 v101, v2
	v_mov_b32_e32 v102, v2
	v_mov_b32_e32 v103, v2
	v_mov_b32_e32 v104, v2
	v_mov_b32_e32 v105, v2
	v_mov_b32_e32 v114, v2
	v_mov_b32_e32 v115, v2
	v_mov_b32_e32 v116, v2
	v_mov_b32_e32 v117, v2
	v_mov_b32_e32 v122, v2
	v_mov_b32_e32 v123, v2
	v_mov_b32_e32 v124, v2
	v_mov_b32_e32 v125, v2
	v_mov_b32_e32 v74, v2
	v_mov_b32_e32 v75, v2
	v_mov_b32_e32 v76, v2
	v_mov_b32_e32 v77, v2
	v_mov_b32_e32 v78, v2
	v_mov_b32_e32 v79, v2
	v_mov_b32_e32 v80, v2
	v_mov_b32_e32 v81, v2
	v_mov_b32_e32 v90, v2
	v_mov_b32_e32 v91, v2
	v_mov_b32_e32 v92, v2
	v_mov_b32_e32 v93, v2
	v_mov_b32_e32 v94, v2
	v_mov_b32_e32 v95, v2
	v_mov_b32_e32 v96, v2
	v_mov_b32_e32 v97, v2
	v_mov_b32_e32 v106, v2
	v_mov_b32_e32 v107, v2
	v_mov_b32_e32 v108, v2
	v_mov_b32_e32 v109, v2
	v_mov_b32_e32 v110, v2
	v_mov_b32_e32 v111, v2
	v_mov_b32_e32 v112, v2
	v_mov_b32_e32 v113, v2
	v_mov_b32_e32 v130, v2
	v_mov_b32_e32 v131, v2
	v_mov_b32_e32 v132, v2
	v_mov_b32_e32 v133, v2
	v_mov_b32_e32 v134, v2
	v_mov_b32_e32 v135, v2
	v_mov_b32_e32 v136, v2
	v_mov_b32_e32 v137, v2
	s_andn2_b64 vcc, exec, s[38:39]
	s_cbranch_vccnz .LBB0_1627
	s_branch .LBB0_1628

.LBB0_1783:
	s_add_u32 s28, s6, 0xfffc0080
	s_addc_u32 s29, s7, -1
	s_add_i32 s53, 0, 0x10000
	s_cmp_eq_u32 s41, 12
	s_cselect_b32 s31, s8, s29
	s_cselect_b32 s30, s9, s28
	s_cselect_b32 s29, s21, s40
	s_cselect_b32 s28, s23, s33
	s_add_i32 s62, 0, 0x14000
	v_add_u32_e32 v142, s53, v181
	v_add_u32_e32 v168, s62, v181
	ds_read_b128 v[130:133], v142
	ds_read_b128 v[134:137], v142 offset:1024
	ds_read_b128 v[138:141], v142 offset:2048
	ds_read_b128 v[142:145], v142 offset:3072
	ds_read_b128 v[146:149], v168
	ds_read_b128 v[150:153], v168 offset:1024
	ds_read_b128 v[154:157], v168 offset:2048
	ds_read_b128 v[168:171], v168 offset:3072
	v_lshl_add_u64 v[176:177], s[6:7], 0, v[166:167]
	s_add_i32 m0, s37, 0xc000
	ds_read_b128 v[172:175], v183
	ds_read_b128 v[184:187], v183 offset:1024
	ds_read_b128 v[188:191], v183 offset:2048
	ds_read_b128 v[192:195], v183 offset:3072
	ds_read_b128 v[196:199], v183 offset:4096
	ds_read_b128 v[200:203], v183 offset:5120
	ds_read_b128 v[204:207], v183 offset:6144
	ds_read_b128 v[216:219], v183 offset:7168
	global_load_lds_dwordx4 v[176:177], off
	v_lshl_add_u64 v[176:177], s[6:7], 0, v[164:165]
	s_add_i32 m0, s37, 0xe000
	s_nop 0
	global_load_lds_dwordx4 v[176:177], off
	s_waitcnt vmcnt(8)
	s_waitcnt lgkmcnt(0)
	s_barrier
	s_setprio 1
	s_waitcnt lgkmcnt(0)
	v_mfma_f32_16x16x32_bf16 v[126:129], v[130:133], v[172:175], v[126:129]
	v_mfma_f32_16x16x32_bf16 v[122:125], v[138:141], v[172:175], v[122:125]
	v_mfma_f32_16x16x32_bf16 v[114:117], v[130:133], v[188:191], v[114:117]
	v_mfma_f32_16x16x32_bf16 v[106:109], v[138:141], v[188:191], v[106:109]
	v_mfma_f32_16x16x32_bf16 v[98:101], v[130:133], v[196:199], v[98:101]
	v_mfma_f32_16x16x32_bf16 v[90:93], v[138:141], v[196:199], v[90:93]
	v_mfma_f32_16x16x32_bf16 v[82:85], v[130:133], v[204:207], v[82:85]
	v_mfma_f32_16x16x32_bf16 v[74:77], v[138:141], v[204:207], v[74:77]
	v_mfma_f32_16x16x32_bf16 v[126:129], v[134:137], v[184:187], v[126:129]
	v_mfma_f32_16x16x32_bf16 v[122:125], v[142:145], v[184:187], v[122:125]
	v_mfma_f32_16x16x32_bf16 v[114:117], v[134:137], v[192:195], v[114:117]
	v_mfma_f32_16x16x32_bf16 v[106:109], v[142:145], v[192:195], v[106:109]
	v_mfma_f32_16x16x32_bf16 v[98:101], v[134:137], v[200:203], v[98:101]
	v_mfma_f32_16x16x32_bf16 v[90:93], v[142:145], v[200:203], v[90:93]
	v_mfma_f32_16x16x32_bf16 v[82:85], v[134:137], v[216:219], v[82:85]
	v_mfma_f32_16x16x32_bf16 v[74:77], v[142:145], v[216:219], v[74:77]
	v_mfma_f32_16x16x32_bf16 v[118:121], v[146:149], v[172:175], v[118:121]
	v_mfma_f32_16x16x32_bf16 v[110:113], v[154:157], v[172:175], v[110:113]
	v_mfma_f32_16x16x32_bf16 v[102:105], v[146:149], v[188:191], v[102:105]
	v_mfma_f32_16x16x32_bf16 v[94:97], v[154:157], v[188:191], v[94:97]
	v_mfma_f32_16x16x32_bf16 v[86:89], v[146:149], v[196:199], v[86:89]
	v_mfma_f32_16x16x32_bf16 v[78:81], v[154:157], v[196:199], v[78:81]
	v_mfma_f32_16x16x32_bf16 v[70:73], v[146:149], v[204:207], v[70:73]
	v_mfma_f32_16x16x32_bf16 v[66:69], v[154:157], v[204:207], v[66:69]
	v_mfma_f32_16x16x32_bf16 v[118:121], v[150:153], v[184:187], v[118:121]
	v_mfma_f32_16x16x32_bf16 v[110:113], v[168:171], v[184:187], v[110:113]
	v_mfma_f32_16x16x32_bf16 v[102:105], v[150:153], v[192:195], v[102:105]
	v_mfma_f32_16x16x32_bf16 v[94:97], v[168:171], v[192:195], v[94:97]
	v_mfma_f32_16x16x32_bf16 v[86:89], v[150:153], v[200:203], v[86:89]
	v_mfma_f32_16x16x32_bf16 v[78:81], v[168:171], v[200:203], v[78:81]
	v_mfma_f32_16x16x32_bf16 v[70:73], v[150:153], v[216:219], v[70:73]
	v_mfma_f32_16x16x32_bf16 v[66:69], v[168:171], v[216:219], v[66:69]
	s_setprio 0
	s_barrier
	s_add_i32 s53, s53, s36
	v_lshl_add_u64 v[176:177], s[28:29], 0, v[162:163]
	s_mov_b32 m0, s53
	ds_read_b128 v[172:175], v183 offset:16384
	ds_read_b128 v[184:187], v183 offset:17408
	ds_read_b128 v[188:191], v183 offset:18432
	ds_read_b128 v[192:195], v183 offset:19456
	ds_read_b128 v[196:199], v183 offset:20480
	ds_read_b128 v[200:203], v183 offset:21504
	ds_read_b128 v[204:207], v183 offset:22528
	ds_read_b128 v[216:219], v183 offset:23552
	global_load_lds_dwordx4 v[176:177], off
	s_add_i32 m0, s53, 0x2000
	s_add_u32 s58, s28, 0x40000
	v_lshl_add_u64 v[208:209], s[28:29], 0, v[158:159]
	s_addc_u32 s59, s29, 0
	s_add_i32 s53, s62, s36
	global_load_lds_dwordx4 v[208:209], off
	v_lshl_add_u64 v[220:221], s[58:59], 0, v[162:163]
	s_mov_b32 m0, s53
	v_lshl_add_u64 v[222:223], s[30:31], 0, v[160:161]
	global_load_lds_dwordx4 v[220:221], off
	v_lshl_add_u64 v[220:221], s[58:59], 0, v[158:159]
	s_add_i32 m0, s53, 0x2000
	s_nop 0
	global_load_lds_dwordx4 v[220:221], off
	v_lshl_add_u64 v[220:221], s[30:31], 0, v[0:1]
	s_mov_b32 m0, s37
	s_nop 0
	global_load_lds_dwordx4 v[220:221], off
	s_mov_b32 m0, s44
	s_nop 0
	global_load_lds_dwordx4 v[222:223], off
	s_waitcnt vmcnt(8)
	s_waitcnt lgkmcnt(0)
	s_barrier
	s_setprio 1
	s_waitcnt lgkmcnt(0)
	v_mfma_f32_16x16x32_bf16 v[62:65], v[130:133], v[172:175], v[62:65]
	v_mfma_f32_16x16x32_bf16 v[58:61], v[138:141], v[172:175], v[58:61]
	v_mfma_f32_16x16x32_bf16 v[50:53], v[130:133], v[188:191], v[50:53]
	v_mfma_f32_16x16x32_bf16 v[42:45], v[138:141], v[188:191], v[42:45]
	v_mfma_f32_16x16x32_bf16 v[34:37], v[130:133], v[196:199], v[34:37]
	v_mfma_f32_16x16x32_bf16 v[26:29], v[138:141], v[196:199], v[26:29]
	v_mfma_f32_16x16x32_bf16 v[18:21], v[130:133], v[204:207], v[18:21]
	v_mfma_f32_16x16x32_bf16 v[10:13], v[138:141], v[204:207], v[10:13]
	v_mfma_f32_16x16x32_bf16 v[62:65], v[134:137], v[184:187], v[62:65]
	v_mfma_f32_16x16x32_bf16 v[58:61], v[142:145], v[184:187], v[58:61]
	v_mfma_f32_16x16x32_bf16 v[50:53], v[134:137], v[192:195], v[50:53]
	v_mfma_f32_16x16x32_bf16 v[42:45], v[142:145], v[192:195], v[42:45]
	v_mfma_f32_16x16x32_bf16 v[34:37], v[134:137], v[200:203], v[34:37]
	v_mfma_f32_16x16x32_bf16 v[26:29], v[142:145], v[200:203], v[26:29]
	v_mfma_f32_16x16x32_bf16 v[18:21], v[134:137], v[216:219], v[18:21]
	v_mfma_f32_16x16x32_bf16 v[10:13], v[142:145], v[216:219], v[10:13]
	v_mfma_f32_16x16x32_bf16 v[54:57], v[146:149], v[172:175], v[54:57]
	v_mfma_f32_16x16x32_bf16 v[46:49], v[154:157], v[172:175], v[46:49]
	v_mfma_f32_16x16x32_bf16 v[38:41], v[146:149], v[188:191], v[38:41]
	v_mfma_f32_16x16x32_bf16 v[30:33], v[154:157], v[188:191], v[30:33]
	v_mfma_f32_16x16x32_bf16 v[22:25], v[146:149], v[196:199], v[22:25]
	v_mfma_f32_16x16x32_bf16 v[14:17], v[154:157], v[196:199], v[14:17]
	v_mfma_f32_16x16x32_bf16 v[6:9], v[146:149], v[204:207], v[6:9]
	v_mfma_f32_16x16x32_bf16 v[2:5], v[154:157], v[204:207], v[2:5]
	v_mfma_f32_16x16x32_bf16 v[54:57], v[150:153], v[184:187], v[54:57]
	v_mfma_f32_16x16x32_bf16 v[46:49], v[168:171], v[184:187], v[46:49]
	v_mfma_f32_16x16x32_bf16 v[38:41], v[150:153], v[192:195], v[38:41]
	v_mfma_f32_16x16x32_bf16 v[30:33], v[168:171], v[192:195], v[30:33]
	v_mfma_f32_16x16x32_bf16 v[22:25], v[150:153], v[200:203], v[22:25]
	v_mfma_f32_16x16x32_bf16 v[14:17], v[168:171], v[200:203], v[14:17]
	v_mfma_f32_16x16x32_bf16 v[6:9], v[150:153], v[216:219], v[6:9]
	v_mfma_f32_16x16x32_bf16 v[2:5], v[168:171], v[216:219], v[2:5]
	s_setprio 0
	s_barrier
	s_add_i32 s53, 0, 0x18000
	s_add_i32 s58, 0, 0x1c000
	v_add_u32_e32 v142, s53, v181
	v_add_u32_e32 v168, s58, v181
	ds_read_b128 v[130:133], v142
	ds_read_b128 v[134:137], v142 offset:1024
	ds_read_b128 v[138:141], v142 offset:2048
	ds_read_b128 v[142:145], v142 offset:3072
	ds_read_b128 v[146:149], v168
	ds_read_b128 v[150:153], v168 offset:1024
	ds_read_b128 v[154:157], v168 offset:2048
	ds_read_b128 v[168:171], v168 offset:3072
	s_add_u32 s30, s30, 0x40000
	s_addc_u32 s31, s31, 0
	s_mov_b32 m0, s45
	v_lshl_add_u64 v[224:225], s[30:31], 0, v[0:1]
	ds_read_b128 v[172:175], v183 offset:32768
	ds_read_b128 v[184:187], v183 offset:33792
	ds_read_b128 v[188:191], v183 offset:34816
	ds_read_b128 v[192:195], v183 offset:35840
	ds_read_b128 v[196:199], v183 offset:36864
	ds_read_b128 v[200:203], v183 offset:37888
	ds_read_b128 v[204:207], v183 offset:38912
	ds_read_b128 v[216:219], v183 offset:39936
	global_load_lds_dwordx4 v[224:225], off
	v_lshl_add_u64 v[224:225], s[30:31], 0, v[160:161]
	s_mov_b32 m0, s46
	s_nop 0
	global_load_lds_dwordx4 v[224:225], off
	s_waitcnt vmcnt(8)
	s_waitcnt lgkmcnt(0)
	s_barrier
	s_setprio 1
	s_waitcnt lgkmcnt(0)
	v_mfma_f32_16x16x32_bf16 v[126:129], v[130:133], v[172:175], v[126:129]
	v_mfma_f32_16x16x32_bf16 v[122:125], v[138:141], v[172:175], v[122:125]
	v_mfma_f32_16x16x32_bf16 v[114:117], v[130:133], v[188:191], v[114:117]
	v_mfma_f32_16x16x32_bf16 v[106:109], v[138:141], v[188:191], v[106:109]
	v_mfma_f32_16x16x32_bf16 v[98:101], v[130:133], v[196:199], v[98:101]
	v_mfma_f32_16x16x32_bf16 v[90:93], v[138:141], v[196:199], v[90:93]
	v_mfma_f32_16x16x32_bf16 v[82:85], v[130:133], v[204:207], v[82:85]
	v_mfma_f32_16x16x32_bf16 v[74:77], v[138:141], v[204:207], v[74:77]
	v_mfma_f32_16x16x32_bf16 v[126:129], v[134:137], v[184:187], v[126:129]
	v_mfma_f32_16x16x32_bf16 v[122:125], v[142:145], v[184:187], v[122:125]
	v_mfma_f32_16x16x32_bf16 v[114:117], v[134:137], v[192:195], v[114:117]
	v_mfma_f32_16x16x32_bf16 v[106:109], v[142:145], v[192:195], v[106:109]
	v_mfma_f32_16x16x32_bf16 v[98:101], v[134:137], v[200:203], v[98:101]
	v_mfma_f32_16x16x32_bf16 v[90:93], v[142:145], v[200:203], v[90:93]
	v_mfma_f32_16x16x32_bf16 v[82:85], v[134:137], v[216:219], v[82:85]
	v_mfma_f32_16x16x32_bf16 v[74:77], v[142:145], v[216:219], v[74:77]
	v_mfma_f32_16x16x32_bf16 v[118:121], v[146:149], v[172:175], v[118:121]
	v_mfma_f32_16x16x32_bf16 v[110:113], v[154:157], v[172:175], v[110:113]
	v_mfma_f32_16x16x32_bf16 v[102:105], v[146:149], v[188:191], v[102:105]
	v_mfma_f32_16x16x32_bf16 v[94:97], v[154:157], v[188:191], v[94:97]
	v_mfma_f32_16x16x32_bf16 v[86:89], v[146:149], v[196:199], v[86:89]
	v_mfma_f32_16x16x32_bf16 v[78:81], v[154:157], v[196:199], v[78:81]
	v_mfma_f32_16x16x32_bf16 v[70:73], v[146:149], v[204:207], v[70:73]
	v_mfma_f32_16x16x32_bf16 v[66:69], v[154:157], v[204:207], v[66:69]
	v_mfma_f32_16x16x32_bf16 v[118:121], v[150:153], v[184:187], v[118:121]
	v_mfma_f32_16x16x32_bf16 v[110:113], v[168:171], v[184:187], v[110:113]
	v_mfma_f32_16x16x32_bf16 v[102:105], v[150:153], v[192:195], v[102:105]
	v_mfma_f32_16x16x32_bf16 v[94:97], v[168:171], v[192:195], v[94:97]
	v_mfma_f32_16x16x32_bf16 v[86:89], v[150:153], v[200:203], v[86:89]
	v_mfma_f32_16x16x32_bf16 v[78:81], v[168:171], v[200:203], v[78:81]
	v_mfma_f32_16x16x32_bf16 v[70:73], v[150:153], v[216:219], v[70:73]
	v_mfma_f32_16x16x32_bf16 v[66:69], v[168:171], v[216:219], v[66:69]
	s_setprio 0
	s_barrier
	s_add_i32 s30, s53, s36
	v_lshl_add_u64 v[176:177], v[176:177], 0, s[56:57]
	s_mov_b32 m0, s30
	ds_read_b128 v[172:175], v183 offset:49152
	ds_read_b128 v[184:187], v183 offset:50176
	ds_read_b128 v[188:191], v183 offset:51200
	ds_read_b128 v[192:195], v183 offset:52224
	ds_read_b128 v[196:199], v183 offset:53248
	ds_read_b128 v[200:203], v183 offset:54272
	ds_read_b128 v[204:207], v183 offset:55296
	ds_read_b128 v[216:219], v183 offset:56320
	global_load_lds_dwordx4 v[176:177], off
	s_add_i32 m0, s30, 0x2000
	s_add_u32 s28, s28, 0x40080
	v_lshl_add_u64 v[176:177], v[208:209], 0, s[56:57]
	s_addc_u32 s29, s29, 0
	s_add_i32 s30, s58, s36
	global_load_lds_dwordx4 v[176:177], off
	v_lshl_add_u64 v[176:177], s[28:29], 0, v[162:163]
	s_mov_b32 m0, s30
	s_nop 0
	global_load_lds_dwordx4 v[176:177], off
	v_lshl_add_u64 v[176:177], s[28:29], 0, v[158:159]
	s_add_i32 m0, s30, 0x2000
	s_nop 0
	global_load_lds_dwordx4 v[176:177], off
	v_lshl_add_u64 v[176:177], v[220:221], 0, s[56:57]
	s_mov_b32 m0, s47
	s_nop 0
	global_load_lds_dwordx4 v[176:177], off
	v_lshl_add_u64 v[176:177], v[222:223], 0, s[56:57]
	s_mov_b32 m0, s48
	s_nop 0
	global_load_lds_dwordx4 v[176:177], off
	s_waitcnt vmcnt(8)
	s_waitcnt lgkmcnt(0)
	s_barrier
	s_setprio 1
	s_waitcnt lgkmcnt(0)
	v_mfma_f32_16x16x32_bf16 v[62:65], v[130:133], v[172:175], v[62:65]
	v_mfma_f32_16x16x32_bf16 v[58:61], v[138:141], v[172:175], v[58:61]
	v_mfma_f32_16x16x32_bf16 v[50:53], v[130:133], v[188:191], v[50:53]
	v_mfma_f32_16x16x32_bf16 v[42:45], v[138:141], v[188:191], v[42:45]
	v_mfma_f32_16x16x32_bf16 v[34:37], v[130:133], v[196:199], v[34:37]
	v_mfma_f32_16x16x32_bf16 v[26:29], v[138:141], v[196:199], v[26:29]
	v_mfma_f32_16x16x32_bf16 v[18:21], v[130:133], v[204:207], v[18:21]
	v_mfma_f32_16x16x32_bf16 v[10:13], v[138:141], v[204:207], v[10:13]
	v_mfma_f32_16x16x32_bf16 v[62:65], v[134:137], v[184:187], v[62:65]
	v_mfma_f32_16x16x32_bf16 v[58:61], v[142:145], v[184:187], v[58:61]
	v_mfma_f32_16x16x32_bf16 v[50:53], v[134:137], v[192:195], v[50:53]
	v_mfma_f32_16x16x32_bf16 v[42:45], v[142:145], v[192:195], v[42:45]
	v_mfma_f32_16x16x32_bf16 v[34:37], v[134:137], v[200:203], v[34:37]
	v_mfma_f32_16x16x32_bf16 v[26:29], v[142:145], v[200:203], v[26:29]
	v_mfma_f32_16x16x32_bf16 v[18:21], v[134:137], v[216:219], v[18:21]
	v_mfma_f32_16x16x32_bf16 v[10:13], v[142:145], v[216:219], v[10:13]
	v_mfma_f32_16x16x32_bf16 v[54:57], v[146:149], v[172:175], v[54:57]
	v_mfma_f32_16x16x32_bf16 v[46:49], v[154:157], v[172:175], v[46:49]
	v_mfma_f32_16x16x32_bf16 v[38:41], v[146:149], v[188:191], v[38:41]
	v_mfma_f32_16x16x32_bf16 v[30:33], v[154:157], v[188:191], v[30:33]
	v_mfma_f32_16x16x32_bf16 v[22:25], v[146:149], v[196:199], v[22:25]
	v_mfma_f32_16x16x32_bf16 v[14:17], v[154:157], v[196:199], v[14:17]
	v_mfma_f32_16x16x32_bf16 v[6:9], v[146:149], v[204:207], v[6:9]
	v_mfma_f32_16x16x32_bf16 v[2:5], v[154:157], v[204:207], v[2:5]
	v_mfma_f32_16x16x32_bf16 v[54:57], v[150:153], v[184:187], v[54:57]
	v_mfma_f32_16x16x32_bf16 v[46:49], v[168:171], v[184:187], v[46:49]
	v_mfma_f32_16x16x32_bf16 v[38:41], v[150:153], v[192:195], v[38:41]
	v_mfma_f32_16x16x32_bf16 v[30:33], v[168:171], v[192:195], v[30:33]
	v_mfma_f32_16x16x32_bf16 v[22:25], v[150:153], v[200:203], v[22:25]
	v_mfma_f32_16x16x32_bf16 v[14:17], v[168:171], v[200:203], v[14:17]
	v_mfma_f32_16x16x32_bf16 v[6:9], v[150:153], v[216:219], v[6:9]
	v_mfma_f32_16x16x32_bf16 v[2:5], v[168:171], v[216:219], v[2:5]
	s_setprio 0
	s_barrier
	s_add_i32 s41, s41, 2
	s_add_u32 s33, s33, 0x100
	s_addc_u32 s40, s40, 0
	s_add_u32 s6, s6, 0x100
	s_addc_u32 s7, s7, 0
	s_cmp_gt_u32 s41, 13
	s_cbranch_scc0 .LBB0_1783
	s_and_b64 vcc, exec, s[18:19]
	s_cbranch_vccz .LBB0_1786
	s_barrier

.LBB0_1799:
	s_add_u32 s26, s24, 0xfffc0080
	s_addc_u32 s27, s25, -1
	s_add_i32 s48, 0, 0x10000
	s_cmp_eq_u32 s47, 12
	s_cselect_b32 s29, s8, s27
	s_cselect_b32 s28, s9, s26
	v_add_u32_e32 v142, s48, v144
	s_cselect_b32 s27, s15, s46
	s_cselect_b32 s26, s17, s45
	s_add_i32 s52, 0, 0x14000
	ds_read_b128 v[148:151], v142
	ds_read_b128 v[152:155], v142 offset:1024
	ds_read_b128 v[156:159], v142 offset:2048
	ds_read_b128 v[160:163], v142 offset:3072
	v_add_u32_e32 v142, s52, v144
	ds_read_b128 v[164:167], v142
	ds_read_b128 v[168:171], v142 offset:1024
	ds_read_b128 v[172:175], v142 offset:2048
	ds_read_b128 v[180:183], v142 offset:3072
	v_lshl_add_u64 v[142:143], s[24:25], 0, v[140:141]
	s_add_i32 m0, s36, 0xc000
	ds_read_b128 v[184:187], v146
	ds_read_b128 v[188:191], v146 offset:1024
	ds_read_b128 v[192:195], v146 offset:2048
	ds_read_b128 v[196:199], v146 offset:3072
	ds_read_b128 v[200:203], v146 offset:4096
	ds_read_b128 v[204:207], v146 offset:5120
	ds_read_b128 v[216:219], v146 offset:6144
	ds_read_b128 v[220:223], v146 offset:7168
	global_load_lds_dwordx4 v[142:143], off
	v_lshl_add_u64 v[142:143], s[24:25], 0, v[138:139]
	s_add_i32 m0, s36, 0xe000
	s_nop 0
	global_load_lds_dwordx4 v[142:143], off
	s_waitcnt vmcnt(8)
	s_waitcnt lgkmcnt(0)
	s_barrier
	s_setprio 1
	s_waitcnt lgkmcnt(0)
	v_mfma_f32_16x16x32_bf16 v[126:129], v[148:151], v[184:187], v[126:129]
	v_mfma_f32_16x16x32_bf16 v[122:125], v[156:159], v[184:187], v[122:125]
	v_mfma_f32_16x16x32_bf16 v[118:121], v[148:151], v[192:195], v[118:121]
	v_mfma_f32_16x16x32_bf16 v[110:113], v[156:159], v[192:195], v[110:113]
	v_mfma_f32_16x16x32_bf16 v[102:105], v[148:151], v[200:203], v[102:105]
	v_mfma_f32_16x16x32_bf16 v[94:97], v[156:159], v[200:203], v[94:97]
	v_mfma_f32_16x16x32_bf16 v[86:89], v[148:151], v[216:219], v[86:89]
	v_mfma_f32_16x16x32_bf16 v[78:81], v[156:159], v[216:219], v[78:81]
	v_mfma_f32_16x16x32_bf16 v[126:129], v[152:155], v[188:191], v[126:129]
	v_mfma_f32_16x16x32_bf16 v[122:125], v[160:163], v[188:191], v[122:125]
	v_mfma_f32_16x16x32_bf16 v[118:121], v[152:155], v[196:199], v[118:121]
	v_mfma_f32_16x16x32_bf16 v[110:113], v[160:163], v[196:199], v[110:113]
	v_mfma_f32_16x16x32_bf16 v[102:105], v[152:155], v[204:207], v[102:105]
	v_mfma_f32_16x16x32_bf16 v[94:97], v[160:163], v[204:207], v[94:97]
	v_mfma_f32_16x16x32_bf16 v[86:89], v[152:155], v[220:223], v[86:89]
	v_mfma_f32_16x16x32_bf16 v[78:81], v[160:163], v[220:223], v[78:81]
	v_mfma_f32_16x16x32_bf16 v[114:117], v[164:167], v[184:187], v[114:117]
	v_mfma_f32_16x16x32_bf16 v[106:109], v[172:175], v[184:187], v[106:109]
	v_mfma_f32_16x16x32_bf16 v[98:101], v[164:167], v[192:195], v[98:101]
	v_mfma_f32_16x16x32_bf16 v[90:93], v[172:175], v[192:195], v[90:93]
	v_mfma_f32_16x16x32_bf16 v[82:85], v[164:167], v[200:203], v[82:85]
	v_mfma_f32_16x16x32_bf16 v[74:77], v[172:175], v[200:203], v[74:77]
	v_mfma_f32_16x16x32_bf16 v[70:73], v[164:167], v[216:219], v[70:73]
	v_mfma_f32_16x16x32_bf16 v[66:69], v[172:175], v[216:219], v[66:69]
	v_mfma_f32_16x16x32_bf16 v[114:117], v[168:171], v[188:191], v[114:117]
	v_mfma_f32_16x16x32_bf16 v[106:109], v[180:183], v[188:191], v[106:109]
	v_mfma_f32_16x16x32_bf16 v[98:101], v[168:171], v[196:199], v[98:101]
	v_mfma_f32_16x16x32_bf16 v[90:93], v[180:183], v[196:199], v[90:93]
	v_mfma_f32_16x16x32_bf16 v[82:85], v[168:171], v[204:207], v[82:85]
	v_mfma_f32_16x16x32_bf16 v[74:77], v[180:183], v[204:207], v[74:77]
	v_mfma_f32_16x16x32_bf16 v[70:73], v[168:171], v[220:223], v[70:73]
	v_mfma_f32_16x16x32_bf16 v[66:69], v[180:183], v[220:223], v[66:69]
	s_setprio 0
	s_barrier
	s_add_i32 s48, s48, s35
	v_lshl_add_u64 v[142:143], s[26:27], 0, v[134:135]
	s_mov_b32 m0, s48
	ds_read_b128 v[184:187], v146 offset:16384
	ds_read_b128 v[188:191], v146 offset:17408
	ds_read_b128 v[192:195], v146 offset:18432
	ds_read_b128 v[196:199], v146 offset:19456
	ds_read_b128 v[200:203], v146 offset:20480
	ds_read_b128 v[204:207], v146 offset:21504
	ds_read_b128 v[216:219], v146 offset:22528
	ds_read_b128 v[220:223], v146 offset:23552
	global_load_lds_dwordx4 v[142:143], off
	s_add_i32 m0, s48, 0x2000
	s_add_u32 s48, s26, 0x40000
	v_lshl_add_u64 v[176:177], s[26:27], 0, v[130:131]
	s_addc_u32 s49, s27, 0
	s_add_i32 s52, s52, s35
	global_load_lds_dwordx4 v[176:177], off
	v_lshl_add_u64 v[208:209], s[48:49], 0, v[134:135]
	s_mov_b32 m0, s52
	v_lshl_add_u64 v[224:225], s[28:29], 0, v[132:133]
	global_load_lds_dwordx4 v[208:209], off
	v_lshl_add_u64 v[208:209], s[48:49], 0, v[130:131]
	s_add_i32 m0, s52, 0x2000
	s_nop 0
	global_load_lds_dwordx4 v[208:209], off
	v_lshl_add_u64 v[208:209], s[28:29], 0, v[136:137]
	s_mov_b32 m0, s36
	s_nop 0
	global_load_lds_dwordx4 v[208:209], off
	s_mov_b32 m0, s37
	s_nop 0
	global_load_lds_dwordx4 v[224:225], off
	s_waitcnt vmcnt(8)
	s_waitcnt lgkmcnt(0)
	s_barrier
	s_setprio 1
	s_waitcnt lgkmcnt(0)
	v_mfma_f32_16x16x32_bf16 v[62:65], v[148:151], v[184:187], v[62:65]
	v_mfma_f32_16x16x32_bf16 v[58:61], v[156:159], v[184:187], v[58:61]
	v_mfma_f32_16x16x32_bf16 v[54:57], v[148:151], v[192:195], v[54:57]
	v_mfma_f32_16x16x32_bf16 v[46:49], v[156:159], v[192:195], v[46:49]
	v_mfma_f32_16x16x32_bf16 v[38:41], v[148:151], v[200:203], v[38:41]
	v_mfma_f32_16x16x32_bf16 v[30:33], v[156:159], v[200:203], v[30:33]
	v_mfma_f32_16x16x32_bf16 v[22:25], v[148:151], v[216:219], v[22:25]
	v_mfma_f32_16x16x32_bf16 v[14:17], v[156:159], v[216:219], v[14:17]
	v_mfma_f32_16x16x32_bf16 v[62:65], v[152:155], v[188:191], v[62:65]
	v_mfma_f32_16x16x32_bf16 v[58:61], v[160:163], v[188:191], v[58:61]
	v_mfma_f32_16x16x32_bf16 v[54:57], v[152:155], v[196:199], v[54:57]
	v_mfma_f32_16x16x32_bf16 v[46:49], v[160:163], v[196:199], v[46:49]
	v_mfma_f32_16x16x32_bf16 v[38:41], v[152:155], v[204:207], v[38:41]
	v_mfma_f32_16x16x32_bf16 v[30:33], v[160:163], v[204:207], v[30:33]
	v_mfma_f32_16x16x32_bf16 v[22:25], v[152:155], v[220:223], v[22:25]
	v_mfma_f32_16x16x32_bf16 v[14:17], v[160:163], v[220:223], v[14:17]
	v_mfma_f32_16x16x32_bf16 v[50:53], v[164:167], v[184:187], v[50:53]
	v_mfma_f32_16x16x32_bf16 v[42:45], v[172:175], v[184:187], v[42:45]
	v_mfma_f32_16x16x32_bf16 v[34:37], v[164:167], v[192:195], v[34:37]
	v_mfma_f32_16x16x32_bf16 v[26:29], v[172:175], v[192:195], v[26:29]
	v_mfma_f32_16x16x32_bf16 v[18:21], v[164:167], v[200:203], v[18:21]
	v_mfma_f32_16x16x32_bf16 v[10:13], v[172:175], v[200:203], v[10:13]
	v_mfma_f32_16x16x32_bf16 v[6:9], v[164:167], v[216:219], v[6:9]
	v_mfma_f32_16x16x32_bf16 v[2:5], v[172:175], v[216:219], v[2:5]
	v_mfma_f32_16x16x32_bf16 v[50:53], v[168:171], v[188:191], v[50:53]
	v_mfma_f32_16x16x32_bf16 v[42:45], v[180:183], v[188:191], v[42:45]
	v_mfma_f32_16x16x32_bf16 v[34:37], v[168:171], v[196:199], v[34:37]
	v_mfma_f32_16x16x32_bf16 v[26:29], v[180:183], v[196:199], v[26:29]
	v_mfma_f32_16x16x32_bf16 v[18:21], v[168:171], v[204:207], v[18:21]
	v_mfma_f32_16x16x32_bf16 v[10:13], v[180:183], v[204:207], v[10:13]
	v_mfma_f32_16x16x32_bf16 v[6:9], v[168:171], v[220:223], v[6:9]
	v_mfma_f32_16x16x32_bf16 v[2:5], v[180:183], v[220:223], v[2:5]
	s_setprio 0
	s_barrier
	s_add_i32 s48, 0, 0x18000
	v_add_u32_e32 v147, s48, v144
	s_add_i32 s49, 0, 0x1c000
	ds_read_b128 v[148:151], v147
	ds_read_b128 v[152:155], v147 offset:1024
	ds_read_b128 v[156:159], v147 offset:2048
	ds_read_b128 v[160:163], v147 offset:3072
	v_add_u32_e32 v147, s49, v144
	ds_read_b128 v[164:167], v147
	ds_read_b128 v[168:171], v147 offset:1024
	ds_read_b128 v[172:175], v147 offset:2048
	ds_read_b128 v[180:183], v147 offset:3072
	s_add_u32 s28, s28, 0x40000
	s_addc_u32 s29, s29, 0
	s_mov_b32 m0, s4
	v_lshl_add_u64 v[240:241], s[28:29], 0, v[136:137]
	ds_read_b128 v[184:187], v146 offset:32768
	ds_read_b128 v[188:191], v146 offset:33792
	ds_read_b128 v[192:195], v146 offset:34816
	ds_read_b128 v[196:199], v146 offset:35840
	ds_read_b128 v[200:203], v146 offset:36864
	ds_read_b128 v[204:207], v146 offset:37888
	ds_read_b128 v[216:219], v146 offset:38912
	ds_read_b128 v[220:223], v146 offset:39936
	global_load_lds_dwordx4 v[240:241], off
	v_lshl_add_u64 v[240:241], s[28:29], 0, v[132:133]
	s_mov_b32 m0, s33
	s_nop 0
	global_load_lds_dwordx4 v[240:241], off
	s_waitcnt vmcnt(8)
	s_waitcnt lgkmcnt(0)
	s_barrier
	s_setprio 1
	s_waitcnt lgkmcnt(0)
	v_mfma_f32_16x16x32_bf16 v[126:129], v[148:151], v[184:187], v[126:129]
	v_mfma_f32_16x16x32_bf16 v[122:125], v[156:159], v[184:187], v[122:125]
	v_mfma_f32_16x16x32_bf16 v[118:121], v[148:151], v[192:195], v[118:121]
	v_mfma_f32_16x16x32_bf16 v[110:113], v[156:159], v[192:195], v[110:113]
	v_mfma_f32_16x16x32_bf16 v[102:105], v[148:151], v[200:203], v[102:105]
	v_mfma_f32_16x16x32_bf16 v[94:97], v[156:159], v[200:203], v[94:97]
	v_mfma_f32_16x16x32_bf16 v[86:89], v[148:151], v[216:219], v[86:89]
	v_mfma_f32_16x16x32_bf16 v[78:81], v[156:159], v[216:219], v[78:81]
	v_mfma_f32_16x16x32_bf16 v[126:129], v[152:155], v[188:191], v[126:129]
	v_mfma_f32_16x16x32_bf16 v[122:125], v[160:163], v[188:191], v[122:125]
	v_mfma_f32_16x16x32_bf16 v[118:121], v[152:155], v[196:199], v[118:121]
	v_mfma_f32_16x16x32_bf16 v[110:113], v[160:163], v[196:199], v[110:113]
	v_mfma_f32_16x16x32_bf16 v[102:105], v[152:155], v[204:207], v[102:105]
	v_mfma_f32_16x16x32_bf16 v[94:97], v[160:163], v[204:207], v[94:97]
	v_mfma_f32_16x16x32_bf16 v[86:89], v[152:155], v[220:223], v[86:89]
	v_mfma_f32_16x16x32_bf16 v[78:81], v[160:163], v[220:223], v[78:81]
	v_mfma_f32_16x16x32_bf16 v[114:117], v[164:167], v[184:187], v[114:117]
	v_mfma_f32_16x16x32_bf16 v[106:109], v[172:175], v[184:187], v[106:109]
	v_mfma_f32_16x16x32_bf16 v[98:101], v[164:167], v[192:195], v[98:101]
	v_mfma_f32_16x16x32_bf16 v[90:93], v[172:175], v[192:195], v[90:93]
	v_mfma_f32_16x16x32_bf16 v[82:85], v[164:167], v[200:203], v[82:85]
	v_mfma_f32_16x16x32_bf16 v[74:77], v[172:175], v[200:203], v[74:77]
	v_mfma_f32_16x16x32_bf16 v[70:73], v[164:167], v[216:219], v[70:73]
	v_mfma_f32_16x16x32_bf16 v[66:69], v[172:175], v[216:219], v[66:69]
	v_mfma_f32_16x16x32_bf16 v[114:117], v[168:171], v[188:191], v[114:117]
	v_mfma_f32_16x16x32_bf16 v[106:109], v[180:183], v[188:191], v[106:109]
	v_mfma_f32_16x16x32_bf16 v[98:101], v[168:171], v[196:199], v[98:101]
	v_mfma_f32_16x16x32_bf16 v[90:93], v[180:183], v[196:199], v[90:93]
	v_mfma_f32_16x16x32_bf16 v[82:85], v[168:171], v[204:207], v[82:85]
	v_mfma_f32_16x16x32_bf16 v[74:77], v[180:183], v[204:207], v[74:77]
	v_mfma_f32_16x16x32_bf16 v[70:73], v[168:171], v[220:223], v[70:73]
	v_mfma_f32_16x16x32_bf16 v[66:69], v[180:183], v[220:223], v[66:69]
	s_setprio 0
	s_barrier
	s_add_i32 s28, s48, s35
	v_lshl_add_u64 v[142:143], v[142:143], 0, s[56:57]
	s_mov_b32 m0, s28
	ds_read_b128 v[184:187], v146 offset:49152
	ds_read_b128 v[188:191], v146 offset:50176
	ds_read_b128 v[192:195], v146 offset:51200
	ds_read_b128 v[196:199], v146 offset:52224
	ds_read_b128 v[200:203], v146 offset:53248
	ds_read_b128 v[204:207], v146 offset:54272
	ds_read_b128 v[216:219], v146 offset:55296
	ds_read_b128 v[220:223], v146 offset:56320
	global_load_lds_dwordx4 v[142:143], off
	s_add_i32 m0, s28, 0x2000
	s_add_u32 s26, s26, 0x40080
	v_lshl_add_u64 v[142:143], v[176:177], 0, s[56:57]
	s_addc_u32 s27, s27, 0
	s_add_i32 s28, s49, s35
	global_load_lds_dwordx4 v[142:143], off
	v_lshl_add_u64 v[142:143], s[26:27], 0, v[134:135]
	s_mov_b32 m0, s28
	s_nop 0
	global_load_lds_dwordx4 v[142:143], off
	v_lshl_add_u64 v[142:143], s[26:27], 0, v[130:131]
	s_add_i32 m0, s28, 0x2000
	s_nop 0
	global_load_lds_dwordx4 v[142:143], off
	v_lshl_add_u64 v[142:143], v[208:209], 0, s[56:57]
	s_mov_b32 m0, s38
	s_nop 0
	global_load_lds_dwordx4 v[142:143], off
	v_lshl_add_u64 v[142:143], v[224:225], 0, s[56:57]
	s_mov_b32 m0, s39
	s_nop 0
	global_load_lds_dwordx4 v[142:143], off
	s_waitcnt vmcnt(8)
	s_waitcnt lgkmcnt(0)
	s_barrier
	s_setprio 1
	s_waitcnt lgkmcnt(0)
	v_mfma_f32_16x16x32_bf16 v[62:65], v[148:151], v[184:187], v[62:65]
	v_mfma_f32_16x16x32_bf16 v[58:61], v[156:159], v[184:187], v[58:61]
	v_mfma_f32_16x16x32_bf16 v[54:57], v[148:151], v[192:195], v[54:57]
	v_mfma_f32_16x16x32_bf16 v[46:49], v[156:159], v[192:195], v[46:49]
	v_mfma_f32_16x16x32_bf16 v[38:41], v[148:151], v[200:203], v[38:41]
	v_mfma_f32_16x16x32_bf16 v[30:33], v[156:159], v[200:203], v[30:33]
	v_mfma_f32_16x16x32_bf16 v[22:25], v[148:151], v[216:219], v[22:25]
	v_mfma_f32_16x16x32_bf16 v[14:17], v[156:159], v[216:219], v[14:17]
	v_mfma_f32_16x16x32_bf16 v[62:65], v[152:155], v[188:191], v[62:65]
	v_mfma_f32_16x16x32_bf16 v[58:61], v[160:163], v[188:191], v[58:61]
	v_mfma_f32_16x16x32_bf16 v[54:57], v[152:155], v[196:199], v[54:57]
	v_mfma_f32_16x16x32_bf16 v[46:49], v[160:163], v[196:199], v[46:49]
	v_mfma_f32_16x16x32_bf16 v[38:41], v[152:155], v[204:207], v[38:41]
	v_mfma_f32_16x16x32_bf16 v[30:33], v[160:163], v[204:207], v[30:33]
	v_mfma_f32_16x16x32_bf16 v[22:25], v[152:155], v[220:223], v[22:25]
	v_mfma_f32_16x16x32_bf16 v[14:17], v[160:163], v[220:223], v[14:17]
	v_mfma_f32_16x16x32_bf16 v[50:53], v[164:167], v[184:187], v[50:53]
	v_mfma_f32_16x16x32_bf16 v[42:45], v[172:175], v[184:187], v[42:45]
	v_mfma_f32_16x16x32_bf16 v[34:37], v[164:167], v[192:195], v[34:37]
	v_mfma_f32_16x16x32_bf16 v[26:29], v[172:175], v[192:195], v[26:29]
	v_mfma_f32_16x16x32_bf16 v[18:21], v[164:167], v[200:203], v[18:21]
	v_mfma_f32_16x16x32_bf16 v[10:13], v[172:175], v[200:203], v[10:13]
	v_mfma_f32_16x16x32_bf16 v[6:9], v[164:167], v[216:219], v[6:9]
	v_mfma_f32_16x16x32_bf16 v[2:5], v[172:175], v[216:219], v[2:5]
	v_mfma_f32_16x16x32_bf16 v[50:53], v[168:171], v[188:191], v[50:53]
	v_mfma_f32_16x16x32_bf16 v[42:45], v[180:183], v[188:191], v[42:45]
	v_mfma_f32_16x16x32_bf16 v[34:37], v[168:171], v[196:199], v[34:37]
	v_mfma_f32_16x16x32_bf16 v[26:29], v[180:183], v[196:199], v[26:29]
	v_mfma_f32_16x16x32_bf16 v[18:21], v[168:171], v[204:207], v[18:21]
	v_mfma_f32_16x16x32_bf16 v[10:13], v[180:183], v[204:207], v[10:13]
	v_mfma_f32_16x16x32_bf16 v[6:9], v[168:171], v[220:223], v[6:9]
	v_mfma_f32_16x16x32_bf16 v[2:5], v[180:183], v[220:223], v[2:5]
	s_setprio 0
	s_barrier
	s_add_i32 s47, s47, 2
	s_add_u32 s45, s45, 0x100
	s_addc_u32 s46, s46, 0
	s_add_u32 s24, s24, 0x100
	s_addc_u32 s25, s25, 0
	s_cmp_gt_u32 s47, 13
	s_cbranch_scc0 .LBB0_1799
	s_and_b64 vcc, exec, s[12:13]
	s_cbranch_vccz .LBB0_1802
	s_barrier

.LBB0_2367:
	s_add_u32 s10, s34, s38
	s_addc_u32 s11, s35, 0
	s_add_u32 s39, s10, 0x100
	s_addc_u32 s76, s11, 0
	s_and_b64 s[70:71], s[62:63], exec
	s_cselect_b32 s77, s45, s76
	s_cselect_b32 s76, s59, s39
	s_add_u32 s38, s30, s38
	s_addc_u32 s39, s31, 0
	s_add_u32 s70, s38, 0x100
	s_addc_u32 s71, s39, 0
	s_add_i32 s91, 0, 0x10000
	s_and_b64 s[38:39], s[62:63], exec
	s_cselect_b32 s79, s37, s71
	s_cselect_b32 s78, s82, s70
	s_add_i32 s38, 0, 0x14000
	s_add_u32 s10, s10, 0x10080
	s_addc_u32 s11, s11, 0
	s_add_i32 s8, s91, s95
	s_add_i32 m0, s65, 0xc000
	s_add_i32 s14, s65, 0xe000
	s_add_i32 s9, s8, 0x2000
	s_add_u32 s80, s78, 0x10000
	s_addc_u32 s81, s79, 0
	s_add_i32 s50, s38, s95
	v_add_u32_e32 v152, s91, v138
	v_add_u32_e32 v164, s38, v138
	s_add_i32 s74, s50, 0x2000
	s_add_i32 vcc_hi, 0, 0x18000
	s_add_i32 s39, 0, 0x1c000
	ds_read_b128 v[140:143], v152
	ds_read_b128 v[144:147], v152 offset:1024
	ds_read_b128 v[148:151], v152 offset:2048
	ds_read_b128 v[152:155], v152 offset:3072
	ds_read_b128 v[156:159], v164
	ds_read_b128 v[160:163], v164 offset:1024
	ds_read_b128 v[168:171], v164 offset:2048
	ds_read_b128 v[172:175], v164 offset:3072
	s_add_u32 s70, s76, 0x10000
	s_addc_u32 s71, s77, 0
	s_add_i32 vcc_lo, vcc_hi, s95
	s_add_i32 s64, vcc_lo, 0x2000
	s_add_u32 s62, s78, 0x10080
	s_addc_u32 s63, s79, 0
	s_add_i32 s91, s39, s95
	s_add_i32 s38, s91, 0x2000
	v_lshl_add_u64 v[164:165], s[10:11], 0, v[128:129]
	ds_read_b128 v[176:179], v139
	ds_read_b128 v[180:183], v139 offset:1024
	ds_read_b128 v[184:187], v139 offset:2048
	ds_read_b128 v[188:191], v139 offset:3072
	ds_read_b128 v[192:195], v139 offset:4096
	ds_read_b128 v[196:199], v139 offset:5120
	ds_read_b128 v[200:203], v139 offset:6144
	ds_read_b128 v[204:207], v139 offset:7168
	global_load_lds_dwordx4 v[164:165], off
	v_lshl_add_u64 v[164:165], s[10:11], 0, v[124:125]
	s_mov_b32 m0, s14
	s_nop 0
	global_load_lds_dwordx4 v[164:165], off
	s_waitcnt vmcnt(8)
	s_waitcnt lgkmcnt(0)
	s_barrier
	s_setprio 1
	s_waitcnt lgkmcnt(0)
	v_mfma_f32_16x16x32_bf16 v[134:137], v[140:143], v[176:179], v[134:137]
	v_mfma_f32_16x16x32_bf16 v[130:133], v[148:151], v[176:179], v[130:133]
	v_mfma_f32_16x16x32_bf16 v[110:113], v[140:143], v[184:187], v[110:113]
	v_mfma_f32_16x16x32_bf16 v[106:109], v[148:151], v[184:187], v[106:109]
	v_mfma_f32_16x16x32_bf16 v[94:97], v[140:143], v[192:195], v[94:97]
	v_mfma_f32_16x16x32_bf16 v[90:93], v[148:151], v[192:195], v[90:93]
	v_mfma_f32_16x16x32_bf16 v[78:81], v[140:143], v[200:203], v[78:81]
	v_mfma_f32_16x16x32_bf16 v[74:77], v[148:151], v[200:203], v[74:77]
	v_mfma_f32_16x16x32_bf16 v[134:137], v[144:147], v[180:183], v[134:137]
	v_mfma_f32_16x16x32_bf16 v[130:133], v[152:155], v[180:183], v[130:133]
	v_mfma_f32_16x16x32_bf16 v[110:113], v[144:147], v[188:191], v[110:113]
	v_mfma_f32_16x16x32_bf16 v[106:109], v[152:155], v[188:191], v[106:109]
	v_mfma_f32_16x16x32_bf16 v[94:97], v[144:147], v[196:199], v[94:97]
	v_mfma_f32_16x16x32_bf16 v[90:93], v[152:155], v[196:199], v[90:93]
	v_mfma_f32_16x16x32_bf16 v[78:81], v[144:147], v[204:207], v[78:81]
	v_mfma_f32_16x16x32_bf16 v[74:77], v[152:155], v[204:207], v[74:77]
	v_mfma_f32_16x16x32_bf16 v[118:121], v[156:159], v[176:179], v[118:121]
	v_mfma_f32_16x16x32_bf16 v[114:117], v[168:171], v[176:179], v[114:117]
	v_mfma_f32_16x16x32_bf16 v[102:105], v[156:159], v[184:187], v[102:105]
	v_mfma_f32_16x16x32_bf16 v[98:101], v[168:171], v[184:187], v[98:101]
	v_mfma_f32_16x16x32_bf16 v[86:89], v[156:159], v[192:195], v[86:89]
	v_mfma_f32_16x16x32_bf16 v[82:85], v[168:171], v[192:195], v[82:85]
	v_mfma_f32_16x16x32_bf16 v[70:73], v[156:159], v[200:203], v[70:73]
	v_mfma_f32_16x16x32_bf16 v[66:69], v[168:171], v[200:203], v[66:69]
	v_mfma_f32_16x16x32_bf16 v[118:121], v[160:163], v[180:183], v[118:121]
	v_mfma_f32_16x16x32_bf16 v[114:117], v[172:175], v[180:183], v[114:117]
	v_mfma_f32_16x16x32_bf16 v[102:105], v[160:163], v[188:191], v[102:105]
	v_mfma_f32_16x16x32_bf16 v[98:101], v[172:175], v[188:191], v[98:101]
	v_mfma_f32_16x16x32_bf16 v[86:89], v[160:163], v[196:199], v[86:89]
	v_mfma_f32_16x16x32_bf16 v[82:85], v[172:175], v[196:199], v[82:85]
	v_mfma_f32_16x16x32_bf16 v[70:73], v[160:163], v[204:207], v[70:73]
	v_mfma_f32_16x16x32_bf16 v[66:69], v[172:175], v[204:207], v[66:69]
	s_setprio 0
	s_barrier
	s_mov_b32 m0, s8
	v_lshl_add_u64 v[164:165], s[78:79], 0, v[126:127]
	ds_read_b128 v[176:179], v139 offset:16384
	ds_read_b128 v[180:183], v139 offset:17408
	ds_read_b128 v[184:187], v139 offset:18432
	ds_read_b128 v[188:191], v139 offset:19456
	ds_read_b128 v[192:195], v139 offset:20480
	ds_read_b128 v[196:199], v139 offset:21504
	ds_read_b128 v[200:203], v139 offset:22528
	ds_read_b128 v[204:207], v139 offset:23552
	global_load_lds_dwordx4 v[164:165], off
	v_lshl_add_u64 v[208:209], s[78:79], 0, v[122:123]
	s_mov_b32 m0, s9
	v_lshl_add_u64 v[216:217], s[80:81], 0, v[126:127]
	global_load_lds_dwordx4 v[208:209], off
	s_mov_b32 m0, s50
	v_lshl_add_u64 v[218:219], s[76:77], 0, v[124:125]
	global_load_lds_dwordx4 v[216:217], off
	v_lshl_add_u64 v[216:217], s[80:81], 0, v[122:123]
	s_mov_b32 m0, s74
	s_nop 0
	global_load_lds_dwordx4 v[216:217], off
	v_lshl_add_u64 v[216:217], s[76:77], 0, v[128:129]
	s_mov_b32 m0, s65
	s_nop 0
	global_load_lds_dwordx4 v[216:217], off
	s_mov_b32 m0, s15
	s_nop 0
	global_load_lds_dwordx4 v[218:219], off
	s_waitcnt vmcnt(8)
	s_waitcnt lgkmcnt(0)
	s_barrier
	s_setprio 1
	s_waitcnt lgkmcnt(0)
	v_mfma_f32_16x16x32_bf16 v[62:65], v[140:143], v[176:179], v[62:65]
	v_mfma_f32_16x16x32_bf16 v[58:61], v[148:151], v[176:179], v[58:61]
	v_mfma_f32_16x16x32_bf16 v[46:49], v[140:143], v[184:187], v[46:49]
	v_mfma_f32_16x16x32_bf16 v[42:45], v[148:151], v[184:187], v[42:45]
	v_mfma_f32_16x16x32_bf16 v[30:33], v[140:143], v[192:195], v[30:33]
	v_mfma_f32_16x16x32_bf16 v[26:29], v[148:151], v[192:195], v[26:29]
	v_mfma_f32_16x16x32_bf16 v[14:17], v[140:143], v[200:203], v[14:17]
	v_mfma_f32_16x16x32_bf16 v[10:13], v[148:151], v[200:203], v[10:13]
	v_mfma_f32_16x16x32_bf16 v[62:65], v[144:147], v[180:183], v[62:65]
	v_mfma_f32_16x16x32_bf16 v[58:61], v[152:155], v[180:183], v[58:61]
	v_mfma_f32_16x16x32_bf16 v[46:49], v[144:147], v[188:191], v[46:49]
	v_mfma_f32_16x16x32_bf16 v[42:45], v[152:155], v[188:191], v[42:45]
	v_mfma_f32_16x16x32_bf16 v[30:33], v[144:147], v[196:199], v[30:33]
	v_mfma_f32_16x16x32_bf16 v[26:29], v[152:155], v[196:199], v[26:29]
	v_mfma_f32_16x16x32_bf16 v[14:17], v[144:147], v[204:207], v[14:17]
	v_mfma_f32_16x16x32_bf16 v[10:13], v[152:155], v[204:207], v[10:13]
	v_mfma_f32_16x16x32_bf16 v[54:57], v[156:159], v[176:179], v[54:57]
	v_mfma_f32_16x16x32_bf16 v[50:53], v[168:171], v[176:179], v[50:53]
	v_mfma_f32_16x16x32_bf16 v[38:41], v[156:159], v[184:187], v[38:41]
	v_mfma_f32_16x16x32_bf16 v[34:37], v[168:171], v[184:187], v[34:37]
	v_mfma_f32_16x16x32_bf16 v[22:25], v[156:159], v[192:195], v[22:25]
	v_mfma_f32_16x16x32_bf16 v[18:21], v[168:171], v[192:195], v[18:21]
	v_mfma_f32_16x16x32_bf16 v[6:9], v[156:159], v[200:203], v[6:9]
	v_mfma_f32_16x16x32_bf16 v[2:5], v[168:171], v[200:203], v[2:5]
	v_mfma_f32_16x16x32_bf16 v[54:57], v[160:163], v[180:183], v[54:57]
	v_mfma_f32_16x16x32_bf16 v[50:53], v[172:175], v[180:183], v[50:53]
	v_mfma_f32_16x16x32_bf16 v[38:41], v[160:163], v[188:191], v[38:41]
	v_mfma_f32_16x16x32_bf16 v[34:37], v[172:175], v[188:191], v[34:37]
	v_mfma_f32_16x16x32_bf16 v[22:25], v[160:163], v[196:199], v[22:25]
	v_mfma_f32_16x16x32_bf16 v[18:21], v[172:175], v[196:199], v[18:21]
	v_mfma_f32_16x16x32_bf16 v[6:9], v[160:163], v[204:207], v[6:9]
	v_mfma_f32_16x16x32_bf16 v[2:5], v[172:175], v[204:207], v[2:5]
	s_setprio 0
	s_barrier
	v_add_u32_e32 v152, vcc_hi, v138
	v_add_u32_e32 v167, s39, v138
	ds_read_b128 v[140:143], v152
	ds_read_b128 v[144:147], v152 offset:1024
	ds_read_b128 v[148:151], v152 offset:2048
	ds_read_b128 v[152:155], v152 offset:3072
	ds_read_b128 v[156:159], v167
	ds_read_b128 v[160:163], v167 offset:1024
	ds_read_b128 v[168:171], v167 offset:2048
	ds_read_b128 v[172:175], v167 offset:3072
	s_mov_b32 m0, s84
	v_lshl_add_u64 v[220:221], s[70:71], 0, v[128:129]
	ds_read_b128 v[176:179], v139 offset:32768
	ds_read_b128 v[180:183], v139 offset:33792
	ds_read_b128 v[184:187], v139 offset:34816
	ds_read_b128 v[188:191], v139 offset:35840
	ds_read_b128 v[192:195], v139 offset:36864
	ds_read_b128 v[196:199], v139 offset:37888
	ds_read_b128 v[200:203], v139 offset:38912
	ds_read_b128 v[204:207], v139 offset:39936
	global_load_lds_dwordx4 v[220:221], off
	v_lshl_add_u64 v[220:221], s[70:71], 0, v[124:125]
	s_mov_b32 m0, s90
	s_nop 0
	global_load_lds_dwordx4 v[220:221], off
	s_waitcnt vmcnt(8)
	s_waitcnt lgkmcnt(0)
	s_barrier
	s_setprio 1
	s_waitcnt lgkmcnt(0)
	v_mfma_f32_16x16x32_bf16 v[134:137], v[140:143], v[176:179], v[134:137]
	v_mfma_f32_16x16x32_bf16 v[130:133], v[148:151], v[176:179], v[130:133]
	v_mfma_f32_16x16x32_bf16 v[110:113], v[140:143], v[184:187], v[110:113]
	v_mfma_f32_16x16x32_bf16 v[106:109], v[148:151], v[184:187], v[106:109]
	v_mfma_f32_16x16x32_bf16 v[94:97], v[140:143], v[192:195], v[94:97]
	v_mfma_f32_16x16x32_bf16 v[90:93], v[148:151], v[192:195], v[90:93]
	v_mfma_f32_16x16x32_bf16 v[78:81], v[140:143], v[200:203], v[78:81]
	v_mfma_f32_16x16x32_bf16 v[74:77], v[148:151], v[200:203], v[74:77]
	v_mfma_f32_16x16x32_bf16 v[134:137], v[144:147], v[180:183], v[134:137]
	v_mfma_f32_16x16x32_bf16 v[130:133], v[152:155], v[180:183], v[130:133]
	v_mfma_f32_16x16x32_bf16 v[110:113], v[144:147], v[188:191], v[110:113]
	v_mfma_f32_16x16x32_bf16 v[106:109], v[152:155], v[188:191], v[106:109]
	v_mfma_f32_16x16x32_bf16 v[94:97], v[144:147], v[196:199], v[94:97]
	v_mfma_f32_16x16x32_bf16 v[90:93], v[152:155], v[196:199], v[90:93]
	v_mfma_f32_16x16x32_bf16 v[78:81], v[144:147], v[204:207], v[78:81]
	v_mfma_f32_16x16x32_bf16 v[74:77], v[152:155], v[204:207], v[74:77]
	v_mfma_f32_16x16x32_bf16 v[118:121], v[156:159], v[176:179], v[118:121]
	v_mfma_f32_16x16x32_bf16 v[114:117], v[168:171], v[176:179], v[114:117]
	v_mfma_f32_16x16x32_bf16 v[102:105], v[156:159], v[184:187], v[102:105]
	v_mfma_f32_16x16x32_bf16 v[98:101], v[168:171], v[184:187], v[98:101]
	v_mfma_f32_16x16x32_bf16 v[86:89], v[156:159], v[192:195], v[86:89]
	v_mfma_f32_16x16x32_bf16 v[82:85], v[168:171], v[192:195], v[82:85]
	v_mfma_f32_16x16x32_bf16 v[70:73], v[156:159], v[200:203], v[70:73]
	v_mfma_f32_16x16x32_bf16 v[66:69], v[168:171], v[200:203], v[66:69]
	v_mfma_f32_16x16x32_bf16 v[118:121], v[160:163], v[180:183], v[118:121]
	v_mfma_f32_16x16x32_bf16 v[114:117], v[172:175], v[180:183], v[114:117]
	v_mfma_f32_16x16x32_bf16 v[102:105], v[160:163], v[188:191], v[102:105]
	v_mfma_f32_16x16x32_bf16 v[98:101], v[172:175], v[188:191], v[98:101]
	v_mfma_f32_16x16x32_bf16 v[86:89], v[160:163], v[196:199], v[86:89]
	v_mfma_f32_16x16x32_bf16 v[82:85], v[172:175], v[196:199], v[82:85]
	v_mfma_f32_16x16x32_bf16 v[70:73], v[160:163], v[204:207], v[70:73]
	v_mfma_f32_16x16x32_bf16 v[66:69], v[172:175], v[204:207], v[66:69]
	s_setprio 0
	s_barrier
	s_mov_b32 m0, vcc_lo
	v_lshl_add_u64 v[164:165], v[164:165], 0, s[56:57]
	ds_read_b128 v[176:179], v139 offset:49152
	ds_read_b128 v[180:183], v139 offset:50176
	ds_read_b128 v[184:187], v139 offset:51200
	ds_read_b128 v[188:191], v139 offset:52224
	ds_read_b128 v[192:195], v139 offset:53248
	ds_read_b128 v[196:199], v139 offset:54272
	ds_read_b128 v[200:203], v139 offset:55296
	ds_read_b128 v[204:207], v139 offset:56320
	global_load_lds_dwordx4 v[164:165], off
	v_lshl_add_u64 v[164:165], v[208:209], 0, s[56:57]
	s_mov_b32 m0, s64
	s_nop 0
	global_load_lds_dwordx4 v[164:165], off
	v_lshl_add_u64 v[164:165], s[62:63], 0, v[126:127]
	s_mov_b32 m0, s91
	s_nop 0
	global_load_lds_dwordx4 v[164:165], off
	v_lshl_add_u64 v[164:165], s[62:63], 0, v[122:123]
	s_mov_b32 m0, s38
	s_nop 0
	global_load_lds_dwordx4 v[164:165], off
	v_lshl_add_u64 v[164:165], v[216:217], 0, s[56:57]
	s_mov_b32 m0, s68
	s_nop 0
	global_load_lds_dwordx4 v[164:165], off
	v_lshl_add_u64 v[164:165], v[218:219], 0, s[56:57]
	s_mov_b32 m0, s22
	s_nop 0
	global_load_lds_dwordx4 v[164:165], off
	s_waitcnt vmcnt(8)
	s_waitcnt lgkmcnt(0)
	s_barrier
	s_setprio 1
	s_waitcnt lgkmcnt(0)
	v_mfma_f32_16x16x32_bf16 v[62:65], v[140:143], v[176:179], v[62:65]
	v_mfma_f32_16x16x32_bf16 v[58:61], v[148:151], v[176:179], v[58:61]
	v_mfma_f32_16x16x32_bf16 v[46:49], v[140:143], v[184:187], v[46:49]
	v_mfma_f32_16x16x32_bf16 v[42:45], v[148:151], v[184:187], v[42:45]
	v_mfma_f32_16x16x32_bf16 v[30:33], v[140:143], v[192:195], v[30:33]
	v_mfma_f32_16x16x32_bf16 v[26:29], v[148:151], v[192:195], v[26:29]
	v_mfma_f32_16x16x32_bf16 v[14:17], v[140:143], v[200:203], v[14:17]
	v_mfma_f32_16x16x32_bf16 v[10:13], v[148:151], v[200:203], v[10:13]
	v_mfma_f32_16x16x32_bf16 v[62:65], v[144:147], v[180:183], v[62:65]
	v_mfma_f32_16x16x32_bf16 v[58:61], v[152:155], v[180:183], v[58:61]
	v_mfma_f32_16x16x32_bf16 v[46:49], v[144:147], v[188:191], v[46:49]
	v_mfma_f32_16x16x32_bf16 v[42:45], v[152:155], v[188:191], v[42:45]
	v_mfma_f32_16x16x32_bf16 v[30:33], v[144:147], v[196:199], v[30:33]
	v_mfma_f32_16x16x32_bf16 v[26:29], v[152:155], v[196:199], v[26:29]
	v_mfma_f32_16x16x32_bf16 v[14:17], v[144:147], v[204:207], v[14:17]
	v_mfma_f32_16x16x32_bf16 v[10:13], v[152:155], v[204:207], v[10:13]
	v_mfma_f32_16x16x32_bf16 v[54:57], v[156:159], v[176:179], v[54:57]
	v_mfma_f32_16x16x32_bf16 v[50:53], v[168:171], v[176:179], v[50:53]
	v_mfma_f32_16x16x32_bf16 v[38:41], v[156:159], v[184:187], v[38:41]
	v_mfma_f32_16x16x32_bf16 v[34:37], v[168:171], v[184:187], v[34:37]
	v_mfma_f32_16x16x32_bf16 v[22:25], v[156:159], v[192:195], v[22:25]
	v_mfma_f32_16x16x32_bf16 v[18:21], v[168:171], v[192:195], v[18:21]
	v_mfma_f32_16x16x32_bf16 v[6:9], v[156:159], v[200:203], v[6:9]
	v_mfma_f32_16x16x32_bf16 v[2:5], v[168:171], v[200:203], v[2:5]
	v_mfma_f32_16x16x32_bf16 v[54:57], v[160:163], v[180:183], v[54:57]
	v_mfma_f32_16x16x32_bf16 v[50:53], v[172:175], v[180:183], v[50:53]
	v_mfma_f32_16x16x32_bf16 v[38:41], v[160:163], v[188:191], v[38:41]
	v_mfma_f32_16x16x32_bf16 v[34:37], v[172:175], v[188:191], v[34:37]
	v_mfma_f32_16x16x32_bf16 v[22:25], v[160:163], v[196:199], v[22:25]
	v_mfma_f32_16x16x32_bf16 v[18:21], v[172:175], v[196:199], v[18:21]
	v_mfma_f32_16x16x32_bf16 v[6:9], v[160:163], v[204:207], v[6:9]
	v_mfma_f32_16x16x32_bf16 v[2:5], v[172:175], v[204:207], v[2:5]
	s_setprio 0
	s_barrier
	s_movk_i32 s38, 0x100
	s_andn2_b64 vcc, exec, s[52:53]
	s_mov_b64 s[62:63], -1
	s_mov_b64 s[52:53], 0
	s_cbranch_vccz .LBB0_2367
	s_andn2_b64 vcc, exec, s[42:43]
	s_cbranch_vccnz .LBB0_2359
	v_mov_b32_e32 v2, 0
	s_mov_b32 s16, s36
	s_mov_b32 s94, s44
	s_mov_b64 s[30:31], s[48:49]
	s_mov_b64 s[34:35], s[46:47]
	s_mov_b32 s58, s23
	v_mov_b32_e32 v3, v2
	v_mov_b32_e32 v4, v2
	v_mov_b32_e32 v5, v2
	v_mov_b32_e32 v6, v2
	v_mov_b32_e32 v7, v2
	v_mov_b32_e32 v8, v2
	v_mov_b32_e32 v9, v2
	v_mov_b32_e32 v18, v2
	v_mov_b32_e32 v19, v2
	v_mov_b32_e32 v20, v2
	v_mov_b32_e32 v21, v2
	v_mov_b32_e32 v22, v2
	v_mov_b32_e32 v23, v2
	v_mov_b32_e32 v24, v2
	v_mov_b32_e32 v25, v2
	v_mov_b32_e32 v34, v2
	v_mov_b32_e32 v35, v2
	v_mov_b32_e32 v36, v2
	v_mov_b32_e32 v37, v2
	v_mov_b32_e32 v38, v2
	v_mov_b32_e32 v39, v2
	v_mov_b32_e32 v40, v2
	v_mov_b32_e32 v41, v2
	v_mov_b32_e32 v50, v2
	v_mov_b32_e32 v51, v2
	v_mov_b32_e32 v52, v2
	v_mov_b32_e32 v53, v2
	v_mov_b32_e32 v54, v2
	v_mov_b32_e32 v55, v2
	v_mov_b32_e32 v56, v2
	v_mov_b32_e32 v57, v2
	v_mov_b32_e32 v10, v2
	v_mov_b32_e32 v11, v2
	v_mov_b32_e32 v12, v2
	v_mov_b32_e32 v13, v2
	v_mov_b32_e32 v14, v2
	v_mov_b32_e32 v15, v2
	v_mov_b32_e32 v16, v2
	v_mov_b32_e32 v17, v2
	v_mov_b32_e32 v26, v2
	v_mov_b32_e32 v27, v2
	v_mov_b32_e32 v28, v2
	v_mov_b32_e32 v29, v2
	v_mov_b32_e32 v30, v2
	v_mov_b32_e32 v31, v2
	v_mov_b32_e32 v32, v2
	v_mov_b32_e32 v33, v2
	v_mov_b32_e32 v42, v2
	v_mov_b32_e32 v43, v2
	v_mov_b32_e32 v44, v2
	v_mov_b32_e32 v45, v2
	v_mov_b32_e32 v46, v2
	v_mov_b32_e32 v47, v2
	v_mov_b32_e32 v48, v2
	v_mov_b32_e32 v49, v2
	v_mov_b32_e32 v58, v2
	v_mov_b32_e32 v59, v2
	v_mov_b32_e32 v60, v2
	v_mov_b32_e32 v61, v2
	v_mov_b32_e32 v62, v2
	v_mov_b32_e32 v63, v2
	v_mov_b32_e32 v64, v2
	v_mov_b32_e32 v65, v2
	v_mov_b32_e32 v66, v2
	v_mov_b32_e32 v67, v2
	v_mov_b32_e32 v68, v2
	v_mov_b32_e32 v69, v2
	v_mov_b32_e32 v70, v2
	v_mov_b32_e32 v71, v2
	v_mov_b32_e32 v72, v2
	v_mov_b32_e32 v73, v2
	v_mov_b32_e32 v82, v2
	v_mov_b32_e32 v83, v2
	v_mov_b32_e32 v84, v2
	v_mov_b32_e32 v85, v2
	v_mov_b32_e32 v86, v2
	v_mov_b32_e32 v87, v2
	v_mov_b32_e32 v88, v2
	v_mov_b32_e32 v89, v2
	v_mov_b32_e32 v98, v2
	v_mov_b32_e32 v99, v2
	v_mov_b32_e32 v100, v2
	v_mov_b32_e32 v101, v2
	v_mov_b32_e32 v102, v2
	v_mov_b32_e32 v103, v2
	v_mov_b32_e32 v104, v2
	v_mov_b32_e32 v105, v2
	v_mov_b32_e32 v114, v2
	v_mov_b32_e32 v115, v2
	v_mov_b32_e32 v116, v2
	v_mov_b32_e32 v117, v2
	v_mov_b32_e32 v118, v2
	v_mov_b32_e32 v119, v2
	v_mov_b32_e32 v120, v2
	v_mov_b32_e32 v121, v2
	v_mov_b32_e32 v74, v2
	v_mov_b32_e32 v75, v2
	v_mov_b32_e32 v76, v2
	v_mov_b32_e32 v77, v2
	v_mov_b32_e32 v78, v2
	v_mov_b32_e32 v79, v2
	v_mov_b32_e32 v80, v2
	v_mov_b32_e32 v81, v2
	v_mov_b32_e32 v90, v2
	v_mov_b32_e32 v91, v2
	v_mov_b32_e32 v92, v2
	v_mov_b32_e32 v93, v2
	v_mov_b32_e32 v94, v2
	v_mov_b32_e32 v95, v2
	v_mov_b32_e32 v96, v2
	v_mov_b32_e32 v97, v2
	v_mov_b32_e32 v106, v2
	v_mov_b32_e32 v107, v2
	v_mov_b32_e32 v108, v2
	v_mov_b32_e32 v109, v2
	v_mov_b32_e32 v110, v2
	v_mov_b32_e32 v111, v2
	v_mov_b32_e32 v112, v2
	v_mov_b32_e32 v113, v2
	v_mov_b32_e32 v130, v2
	v_mov_b32_e32 v131, v2
	v_mov_b32_e32 v132, v2
	v_mov_b32_e32 v133, v2
	v_mov_b32_e32 v134, v2
	v_mov_b32_e32 v135, v2
	v_mov_b32_e32 v136, v2
	v_mov_b32_e32 v137, v2
	s_branch .LBB0_2359

.LBB0_2467:
	s_add_u32 s8, s30, s12
	s_addc_u32 s9, s31, 0
	s_add_u32 s13, s8, 0x100
	s_addc_u32 s50, s9, 0
	s_and_b64 s[10:11], s[48:49], exec
	s_cselect_b32 s63, s37, s50
	s_cselect_b32 s62, s59, s13
	s_add_u32 s10, s28, s12
	s_addc_u32 s11, s29, 0
	s_add_u32 s12, s10, 0x100
	s_addc_u32 s13, s11, 0
	s_add_i32 s50, 0, 0x10000
	s_and_b64 s[10:11], s[48:49], exec
	s_cselect_b32 s71, s35, s13
	s_cselect_b32 s70, s96, s12
	s_add_i32 s12, 0, 0x14000
	s_add_u32 s10, s8, 0x10080
	s_addc_u32 s11, s9, 0
	s_add_i32 s9, s50, s81
	s_add_i32 m0, s82, 0xc000
	s_add_i32 s8, s82, 0xe000
	s_add_i32 s64, s9, 0x2000
	s_add_u32 s76, s70, 0x10000
	s_addc_u32 s77, s71, 0
	s_add_i32 s65, s12, s81
	v_add_u32_e32 v152, s50, v138
	v_add_u32_e32 v168, s12, v138
	s_add_i32 s74, s65, 0x2000
	s_add_i32 s91, 0, 0x18000
	s_add_i32 s13, 0, 0x1c000
	ds_read_b128 v[140:143], v152
	ds_read_b128 v[144:147], v152 offset:1024
	ds_read_b128 v[148:151], v152 offset:2048
	ds_read_b128 v[152:155], v152 offset:3072
	ds_read_b128 v[156:159], v168
	ds_read_b128 v[160:163], v168 offset:1024
	ds_read_b128 v[164:167], v168 offset:2048
	ds_read_b128 v[168:171], v168 offset:3072
	s_add_u32 s52, s62, 0x10000
	s_addc_u32 s53, s63, 0
	s_add_i32 vcc_hi, s91, s81
	s_add_i32 vcc_lo, vcc_hi, 0x2000
	s_add_u32 s48, s70, 0x10080
	s_addc_u32 s49, s71, 0
	s_add_i32 s50, s13, s81
	s_add_i32 s12, s50, 0x2000
	v_lshl_add_u64 v[204:205], s[10:11], 0, v[128:129]
	ds_read_b128 v[172:175], v139
	ds_read_b128 v[176:179], v139 offset:1024
	ds_read_b128 v[180:183], v139 offset:2048
	ds_read_b128 v[184:187], v139 offset:3072
	ds_read_b128 v[188:191], v139 offset:4096
	ds_read_b128 v[192:195], v139 offset:5120
	ds_read_b128 v[196:199], v139 offset:6144
	ds_read_b128 v[200:203], v139 offset:7168
	global_load_lds_dwordx4 v[204:205], off
	v_lshl_add_u64 v[204:205], s[10:11], 0, v[124:125]
	s_mov_b32 m0, s8
	s_nop 0
	global_load_lds_dwordx4 v[204:205], off
	s_waitcnt vmcnt(8)
	s_waitcnt lgkmcnt(0)
	s_barrier
	s_setprio 1
	s_waitcnt lgkmcnt(0)
	v_mfma_f32_16x16x32_bf16 v[134:137], v[140:143], v[172:175], v[134:137]
	v_mfma_f32_16x16x32_bf16 v[130:133], v[148:151], v[172:175], v[130:133]
	v_mfma_f32_16x16x32_bf16 v[110:113], v[140:143], v[180:183], v[110:113]
	v_mfma_f32_16x16x32_bf16 v[106:109], v[148:151], v[180:183], v[106:109]
	v_mfma_f32_16x16x32_bf16 v[94:97], v[140:143], v[188:191], v[94:97]
	v_mfma_f32_16x16x32_bf16 v[90:93], v[148:151], v[188:191], v[90:93]
	v_mfma_f32_16x16x32_bf16 v[78:81], v[140:143], v[196:199], v[78:81]
	v_mfma_f32_16x16x32_bf16 v[74:77], v[148:151], v[196:199], v[74:77]
	v_mfma_f32_16x16x32_bf16 v[134:137], v[144:147], v[176:179], v[134:137]
	v_mfma_f32_16x16x32_bf16 v[130:133], v[152:155], v[176:179], v[130:133]
	v_mfma_f32_16x16x32_bf16 v[110:113], v[144:147], v[184:187], v[110:113]
	v_mfma_f32_16x16x32_bf16 v[106:109], v[152:155], v[184:187], v[106:109]
	v_mfma_f32_16x16x32_bf16 v[94:97], v[144:147], v[192:195], v[94:97]
	v_mfma_f32_16x16x32_bf16 v[90:93], v[152:155], v[192:195], v[90:93]
	v_mfma_f32_16x16x32_bf16 v[78:81], v[144:147], v[200:203], v[78:81]
	v_mfma_f32_16x16x32_bf16 v[74:77], v[152:155], v[200:203], v[74:77]
	v_mfma_f32_16x16x32_bf16 v[118:121], v[156:159], v[172:175], v[118:121]
	v_mfma_f32_16x16x32_bf16 v[114:117], v[164:167], v[172:175], v[114:117]
	v_mfma_f32_16x16x32_bf16 v[102:105], v[156:159], v[180:183], v[102:105]
	v_mfma_f32_16x16x32_bf16 v[98:101], v[164:167], v[180:183], v[98:101]
	v_mfma_f32_16x16x32_bf16 v[86:89], v[156:159], v[188:191], v[86:89]
	v_mfma_f32_16x16x32_bf16 v[82:85], v[164:167], v[188:191], v[82:85]
	v_mfma_f32_16x16x32_bf16 v[70:73], v[156:159], v[196:199], v[70:73]
	v_mfma_f32_16x16x32_bf16 v[66:69], v[164:167], v[196:199], v[66:69]
	v_mfma_f32_16x16x32_bf16 v[118:121], v[160:163], v[176:179], v[118:121]
	v_mfma_f32_16x16x32_bf16 v[114:117], v[168:171], v[176:179], v[114:117]
	v_mfma_f32_16x16x32_bf16 v[102:105], v[160:163], v[184:187], v[102:105]
	v_mfma_f32_16x16x32_bf16 v[98:101], v[168:171], v[184:187], v[98:101]
	v_mfma_f32_16x16x32_bf16 v[86:89], v[160:163], v[192:195], v[86:89]
	v_mfma_f32_16x16x32_bf16 v[82:85], v[168:171], v[192:195], v[82:85]
	v_mfma_f32_16x16x32_bf16 v[70:73], v[160:163], v[200:203], v[70:73]
	v_mfma_f32_16x16x32_bf16 v[66:69], v[168:171], v[200:203], v[66:69]
	s_setprio 0
	s_barrier
	s_mov_b32 m0, s9
	v_lshl_add_u64 v[204:205], s[70:71], 0, v[126:127]
	ds_read_b128 v[172:175], v139 offset:16384
	ds_read_b128 v[176:179], v139 offset:17408
	ds_read_b128 v[180:183], v139 offset:18432
	ds_read_b128 v[184:187], v139 offset:19456
	ds_read_b128 v[188:191], v139 offset:20480
	ds_read_b128 v[192:195], v139 offset:21504
	ds_read_b128 v[196:199], v139 offset:22528
	ds_read_b128 v[200:203], v139 offset:23552
	global_load_lds_dwordx4 v[204:205], off
	v_lshl_add_u64 v[206:207], s[70:71], 0, v[122:123]
	s_mov_b32 m0, s64
	v_lshl_add_u64 v[208:209], s[76:77], 0, v[126:127]
	global_load_lds_dwordx4 v[206:207], off
	s_mov_b32 m0, s65
	v_lshl_add_u64 v[216:217], s[62:63], 0, v[124:125]
	global_load_lds_dwordx4 v[208:209], off
	v_lshl_add_u64 v[208:209], s[76:77], 0, v[122:123]
	s_mov_b32 m0, s74
	s_nop 0
	global_load_lds_dwordx4 v[208:209], off
	v_lshl_add_u64 v[208:209], s[62:63], 0, v[128:129]
	s_mov_b32 m0, s82
	s_nop 0
	global_load_lds_dwordx4 v[208:209], off
	s_mov_b32 m0, s92
	s_nop 0
	global_load_lds_dwordx4 v[216:217], off
	s_waitcnt vmcnt(8)
	s_waitcnt lgkmcnt(0)
	s_barrier
	s_setprio 1
	s_waitcnt lgkmcnt(0)
	v_mfma_f32_16x16x32_bf16 v[62:65], v[140:143], v[172:175], v[62:65]
	v_mfma_f32_16x16x32_bf16 v[58:61], v[148:151], v[172:175], v[58:61]
	v_mfma_f32_16x16x32_bf16 v[46:49], v[140:143], v[180:183], v[46:49]
	v_mfma_f32_16x16x32_bf16 v[42:45], v[148:151], v[180:183], v[42:45]
	v_mfma_f32_16x16x32_bf16 v[30:33], v[140:143], v[188:191], v[30:33]
	v_mfma_f32_16x16x32_bf16 v[26:29], v[148:151], v[188:191], v[26:29]
	v_mfma_f32_16x16x32_bf16 v[14:17], v[140:143], v[196:199], v[14:17]
	v_mfma_f32_16x16x32_bf16 v[10:13], v[148:151], v[196:199], v[10:13]
	v_mfma_f32_16x16x32_bf16 v[62:65], v[144:147], v[176:179], v[62:65]
	v_mfma_f32_16x16x32_bf16 v[58:61], v[152:155], v[176:179], v[58:61]
	v_mfma_f32_16x16x32_bf16 v[46:49], v[144:147], v[184:187], v[46:49]
	v_mfma_f32_16x16x32_bf16 v[42:45], v[152:155], v[184:187], v[42:45]
	v_mfma_f32_16x16x32_bf16 v[30:33], v[144:147], v[192:195], v[30:33]
	v_mfma_f32_16x16x32_bf16 v[26:29], v[152:155], v[192:195], v[26:29]
	v_mfma_f32_16x16x32_bf16 v[14:17], v[144:147], v[200:203], v[14:17]
	v_mfma_f32_16x16x32_bf16 v[10:13], v[152:155], v[200:203], v[10:13]
	v_mfma_f32_16x16x32_bf16 v[54:57], v[156:159], v[172:175], v[54:57]
	v_mfma_f32_16x16x32_bf16 v[50:53], v[164:167], v[172:175], v[50:53]
	v_mfma_f32_16x16x32_bf16 v[38:41], v[156:159], v[180:183], v[38:41]
	v_mfma_f32_16x16x32_bf16 v[34:37], v[164:167], v[180:183], v[34:37]
	v_mfma_f32_16x16x32_bf16 v[22:25], v[156:159], v[188:191], v[22:25]
	v_mfma_f32_16x16x32_bf16 v[18:21], v[164:167], v[188:191], v[18:21]
	v_mfma_f32_16x16x32_bf16 v[6:9], v[156:159], v[196:199], v[6:9]
	v_mfma_f32_16x16x32_bf16 v[2:5], v[164:167], v[196:199], v[2:5]
	v_mfma_f32_16x16x32_bf16 v[54:57], v[160:163], v[176:179], v[54:57]
	v_mfma_f32_16x16x32_bf16 v[50:53], v[168:171], v[176:179], v[50:53]
	v_mfma_f32_16x16x32_bf16 v[38:41], v[160:163], v[184:187], v[38:41]
	v_mfma_f32_16x16x32_bf16 v[34:37], v[168:171], v[184:187], v[34:37]
	v_mfma_f32_16x16x32_bf16 v[22:25], v[160:163], v[192:195], v[22:25]
	v_mfma_f32_16x16x32_bf16 v[18:21], v[168:171], v[192:195], v[18:21]
	v_mfma_f32_16x16x32_bf16 v[6:9], v[160:163], v[200:203], v[6:9]
	v_mfma_f32_16x16x32_bf16 v[2:5], v[168:171], v[200:203], v[2:5]
	s_setprio 0
	s_barrier
	v_add_u32_e32 v152, s91, v138
	v_add_u32_e32 v168, s13, v138
	ds_read_b128 v[140:143], v152
	ds_read_b128 v[144:147], v152 offset:1024
	ds_read_b128 v[148:151], v152 offset:2048
	ds_read_b128 v[152:155], v152 offset:3072
	ds_read_b128 v[156:159], v168
	ds_read_b128 v[160:163], v168 offset:1024
	ds_read_b128 v[164:167], v168 offset:2048
	ds_read_b128 v[168:171], v168 offset:3072
	s_mov_b32 m0, s84
	v_lshl_add_u64 v[218:219], s[52:53], 0, v[128:129]
	ds_read_b128 v[172:175], v139 offset:32768
	ds_read_b128 v[176:179], v139 offset:33792
	ds_read_b128 v[180:183], v139 offset:34816
	ds_read_b128 v[184:187], v139 offset:35840
	ds_read_b128 v[188:191], v139 offset:36864
	ds_read_b128 v[192:195], v139 offset:37888
	ds_read_b128 v[196:199], v139 offset:38912
	ds_read_b128 v[200:203], v139 offset:39936
	global_load_lds_dwordx4 v[218:219], off
	v_lshl_add_u64 v[218:219], s[52:53], 0, v[124:125]
	s_mov_b32 m0, s90
	s_nop 0
	global_load_lds_dwordx4 v[218:219], off
	s_waitcnt vmcnt(8)
	s_waitcnt lgkmcnt(0)
	s_barrier
	s_setprio 1
	s_waitcnt lgkmcnt(0)
	v_mfma_f32_16x16x32_bf16 v[134:137], v[140:143], v[172:175], v[134:137]
	v_mfma_f32_16x16x32_bf16 v[130:133], v[148:151], v[172:175], v[130:133]
	v_mfma_f32_16x16x32_bf16 v[110:113], v[140:143], v[180:183], v[110:113]
	v_mfma_f32_16x16x32_bf16 v[106:109], v[148:151], v[180:183], v[106:109]
	v_mfma_f32_16x16x32_bf16 v[94:97], v[140:143], v[188:191], v[94:97]
	v_mfma_f32_16x16x32_bf16 v[90:93], v[148:151], v[188:191], v[90:93]
	v_mfma_f32_16x16x32_bf16 v[78:81], v[140:143], v[196:199], v[78:81]
	v_mfma_f32_16x16x32_bf16 v[74:77], v[148:151], v[196:199], v[74:77]
	v_mfma_f32_16x16x32_bf16 v[134:137], v[144:147], v[176:179], v[134:137]
	v_mfma_f32_16x16x32_bf16 v[130:133], v[152:155], v[176:179], v[130:133]
	v_mfma_f32_16x16x32_bf16 v[110:113], v[144:147], v[184:187], v[110:113]
	v_mfma_f32_16x16x32_bf16 v[106:109], v[152:155], v[184:187], v[106:109]
	v_mfma_f32_16x16x32_bf16 v[94:97], v[144:147], v[192:195], v[94:97]
	v_mfma_f32_16x16x32_bf16 v[90:93], v[152:155], v[192:195], v[90:93]
	v_mfma_f32_16x16x32_bf16 v[78:81], v[144:147], v[200:203], v[78:81]
	v_mfma_f32_16x16x32_bf16 v[74:77], v[152:155], v[200:203], v[74:77]
	v_mfma_f32_16x16x32_bf16 v[118:121], v[156:159], v[172:175], v[118:121]
	v_mfma_f32_16x16x32_bf16 v[114:117], v[164:167], v[172:175], v[114:117]
	v_mfma_f32_16x16x32_bf16 v[102:105], v[156:159], v[180:183], v[102:105]
	v_mfma_f32_16x16x32_bf16 v[98:101], v[164:167], v[180:183], v[98:101]
	v_mfma_f32_16x16x32_bf16 v[86:89], v[156:159], v[188:191], v[86:89]
	v_mfma_f32_16x16x32_bf16 v[82:85], v[164:167], v[188:191], v[82:85]
	v_mfma_f32_16x16x32_bf16 v[70:73], v[156:159], v[196:199], v[70:73]
	v_mfma_f32_16x16x32_bf16 v[66:69], v[164:167], v[196:199], v[66:69]
	v_mfma_f32_16x16x32_bf16 v[118:121], v[160:163], v[176:179], v[118:121]
	v_mfma_f32_16x16x32_bf16 v[114:117], v[168:171], v[176:179], v[114:117]
	v_mfma_f32_16x16x32_bf16 v[102:105], v[160:163], v[184:187], v[102:105]
	v_mfma_f32_16x16x32_bf16 v[98:101], v[168:171], v[184:187], v[98:101]
	v_mfma_f32_16x16x32_bf16 v[86:89], v[160:163], v[192:195], v[86:89]
	v_mfma_f32_16x16x32_bf16 v[82:85], v[168:171], v[192:195], v[82:85]
	v_mfma_f32_16x16x32_bf16 v[70:73], v[160:163], v[200:203], v[70:73]
	v_mfma_f32_16x16x32_bf16 v[66:69], v[168:171], v[200:203], v[66:69]
	s_setprio 0
	s_barrier
	s_mov_b32 m0, vcc_hi
	v_lshl_add_u64 v[204:205], v[204:205], 0, s[56:57]
	ds_read_b128 v[172:175], v139 offset:49152
	ds_read_b128 v[176:179], v139 offset:50176
	ds_read_b128 v[180:183], v139 offset:51200
	ds_read_b128 v[184:187], v139 offset:52224
	ds_read_b128 v[188:191], v139 offset:53248
	ds_read_b128 v[192:195], v139 offset:54272
	ds_read_b128 v[196:199], v139 offset:55296
	ds_read_b128 v[200:203], v139 offset:56320
	global_load_lds_dwordx4 v[204:205], off
	v_lshl_add_u64 v[204:205], v[206:207], 0, s[56:57]
	s_mov_b32 m0, vcc_lo
	s_nop 0
	global_load_lds_dwordx4 v[204:205], off
	v_lshl_add_u64 v[204:205], s[48:49], 0, v[126:127]
	s_mov_b32 m0, s50
	s_nop 0
	global_load_lds_dwordx4 v[204:205], off
	v_lshl_add_u64 v[204:205], s[48:49], 0, v[122:123]
	s_mov_b32 m0, s12
	s_nop 0
	global_load_lds_dwordx4 v[204:205], off
	v_lshl_add_u64 v[204:205], v[208:209], 0, s[56:57]
	s_mov_b32 m0, s68
	s_nop 0
	global_load_lds_dwordx4 v[204:205], off
	v_lshl_add_u64 v[204:205], v[216:217], 0, s[56:57]
	s_mov_b32 m0, s93
	s_nop 0
	global_load_lds_dwordx4 v[204:205], off
	s_waitcnt vmcnt(8)
	s_waitcnt lgkmcnt(0)
	s_barrier
	s_setprio 1
	s_waitcnt lgkmcnt(0)
	v_mfma_f32_16x16x32_bf16 v[62:65], v[140:143], v[172:175], v[62:65]
	v_mfma_f32_16x16x32_bf16 v[58:61], v[148:151], v[172:175], v[58:61]
	v_mfma_f32_16x16x32_bf16 v[46:49], v[140:143], v[180:183], v[46:49]
	v_mfma_f32_16x16x32_bf16 v[42:45], v[148:151], v[180:183], v[42:45]
	v_mfma_f32_16x16x32_bf16 v[30:33], v[140:143], v[188:191], v[30:33]
	v_mfma_f32_16x16x32_bf16 v[26:29], v[148:151], v[188:191], v[26:29]
	v_mfma_f32_16x16x32_bf16 v[14:17], v[140:143], v[196:199], v[14:17]
	v_mfma_f32_16x16x32_bf16 v[10:13], v[148:151], v[196:199], v[10:13]
	v_mfma_f32_16x16x32_bf16 v[62:65], v[144:147], v[176:179], v[62:65]
	v_mfma_f32_16x16x32_bf16 v[58:61], v[152:155], v[176:179], v[58:61]
	v_mfma_f32_16x16x32_bf16 v[46:49], v[144:147], v[184:187], v[46:49]
	v_mfma_f32_16x16x32_bf16 v[42:45], v[152:155], v[184:187], v[42:45]
	v_mfma_f32_16x16x32_bf16 v[30:33], v[144:147], v[192:195], v[30:33]
	v_mfma_f32_16x16x32_bf16 v[26:29], v[152:155], v[192:195], v[26:29]
	v_mfma_f32_16x16x32_bf16 v[14:17], v[144:147], v[200:203], v[14:17]
	v_mfma_f32_16x16x32_bf16 v[10:13], v[152:155], v[200:203], v[10:13]
	v_mfma_f32_16x16x32_bf16 v[54:57], v[156:159], v[172:175], v[54:57]
	v_mfma_f32_16x16x32_bf16 v[50:53], v[164:167], v[172:175], v[50:53]
	v_mfma_f32_16x16x32_bf16 v[38:41], v[156:159], v[180:183], v[38:41]
	v_mfma_f32_16x16x32_bf16 v[34:37], v[164:167], v[180:183], v[34:37]
	v_mfma_f32_16x16x32_bf16 v[22:25], v[156:159], v[188:191], v[22:25]
	v_mfma_f32_16x16x32_bf16 v[18:21], v[164:167], v[188:191], v[18:21]
	v_mfma_f32_16x16x32_bf16 v[6:9], v[156:159], v[196:199], v[6:9]
	v_mfma_f32_16x16x32_bf16 v[2:5], v[164:167], v[196:199], v[2:5]
	v_mfma_f32_16x16x32_bf16 v[54:57], v[160:163], v[176:179], v[54:57]
	v_mfma_f32_16x16x32_bf16 v[50:53], v[168:171], v[176:179], v[50:53]
	v_mfma_f32_16x16x32_bf16 v[38:41], v[160:163], v[184:187], v[38:41]
	v_mfma_f32_16x16x32_bf16 v[34:37], v[168:171], v[184:187], v[34:37]
	v_mfma_f32_16x16x32_bf16 v[22:25], v[160:163], v[192:195], v[22:25]
	v_mfma_f32_16x16x32_bf16 v[18:21], v[168:171], v[192:195], v[18:21]
	v_mfma_f32_16x16x32_bf16 v[6:9], v[160:163], v[200:203], v[6:9]
	v_mfma_f32_16x16x32_bf16 v[2:5], v[168:171], v[200:203], v[2:5]
	s_setprio 0
	s_barrier
	s_movk_i32 s12, 0x100
	s_andn2_b64 vcc, exec, s[46:47]
	s_mov_b64 s[48:49], -1
	s_mov_b64 s[46:47], 0
	s_cbranch_vccz .LBB0_2467
	s_andn2_b64 vcc, exec, s[40:41]
	s_cbranch_vccnz .LBB0_2459
	v_mov_b32_e32 v2, 0
	s_mov_b32 s14, s34
	s_mov_b32 s95, s36
	s_mov_b64 s[28:29], s[44:45]
	s_mov_b64 s[30:31], s[42:43]
	s_mov_b32 s94, s58
	v_mov_b32_e32 v3, v2
	v_mov_b32_e32 v4, v2
	v_mov_b32_e32 v5, v2
	v_mov_b32_e32 v6, v2
	v_mov_b32_e32 v7, v2
	v_mov_b32_e32 v8, v2
	v_mov_b32_e32 v9, v2
	v_mov_b32_e32 v18, v2
	v_mov_b32_e32 v19, v2
	v_mov_b32_e32 v20, v2
	v_mov_b32_e32 v21, v2
	v_mov_b32_e32 v22, v2
	v_mov_b32_e32 v23, v2
	v_mov_b32_e32 v24, v2
	v_mov_b32_e32 v25, v2
	v_mov_b32_e32 v34, v2
	v_mov_b32_e32 v35, v2
	v_mov_b32_e32 v36, v2
	v_mov_b32_e32 v37, v2
	v_mov_b32_e32 v38, v2
	v_mov_b32_e32 v39, v2
	v_mov_b32_e32 v40, v2
	v_mov_b32_e32 v41, v2
	v_mov_b32_e32 v50, v2
	v_mov_b32_e32 v51, v2
	v_mov_b32_e32 v52, v2
	v_mov_b32_e32 v53, v2
	v_mov_b32_e32 v54, v2
	v_mov_b32_e32 v55, v2
	v_mov_b32_e32 v56, v2
	v_mov_b32_e32 v57, v2
	v_mov_b32_e32 v10, v2
	v_mov_b32_e32 v11, v2
	v_mov_b32_e32 v12, v2
	v_mov_b32_e32 v13, v2
	v_mov_b32_e32 v14, v2
	v_mov_b32_e32 v15, v2
	v_mov_b32_e32 v16, v2
	v_mov_b32_e32 v17, v2
	v_mov_b32_e32 v26, v2
	v_mov_b32_e32 v27, v2
	v_mov_b32_e32 v28, v2
	v_mov_b32_e32 v29, v2
	v_mov_b32_e32 v30, v2
	v_mov_b32_e32 v31, v2
	v_mov_b32_e32 v32, v2
	v_mov_b32_e32 v33, v2
	v_mov_b32_e32 v42, v2
	v_mov_b32_e32 v43, v2
	v_mov_b32_e32 v44, v2
	v_mov_b32_e32 v45, v2
	v_mov_b32_e32 v46, v2
	v_mov_b32_e32 v47, v2
	v_mov_b32_e32 v48, v2
	v_mov_b32_e32 v49, v2
	v_mov_b32_e32 v58, v2
	v_mov_b32_e32 v59, v2
	v_mov_b32_e32 v60, v2
	v_mov_b32_e32 v61, v2
	v_mov_b32_e32 v62, v2
	v_mov_b32_e32 v63, v2
	v_mov_b32_e32 v64, v2
	v_mov_b32_e32 v65, v2
	v_mov_b32_e32 v66, v2
	v_mov_b32_e32 v67, v2
	v_mov_b32_e32 v68, v2
	v_mov_b32_e32 v69, v2
	v_mov_b32_e32 v70, v2
	v_mov_b32_e32 v71, v2
	v_mov_b32_e32 v72, v2
	v_mov_b32_e32 v73, v2
	v_mov_b32_e32 v82, v2
	v_mov_b32_e32 v83, v2
	v_mov_b32_e32 v84, v2
	v_mov_b32_e32 v85, v2
	v_mov_b32_e32 v86, v2
	v_mov_b32_e32 v87, v2
	v_mov_b32_e32 v88, v2
	v_mov_b32_e32 v89, v2
	v_mov_b32_e32 v98, v2
	v_mov_b32_e32 v99, v2
	v_mov_b32_e32 v100, v2
	v_mov_b32_e32 v101, v2
	v_mov_b32_e32 v102, v2
	v_mov_b32_e32 v103, v2
	v_mov_b32_e32 v104, v2
	v_mov_b32_e32 v105, v2
	v_mov_b32_e32 v114, v2
	v_mov_b32_e32 v115, v2
	v_mov_b32_e32 v116, v2
	v_mov_b32_e32 v117, v2
	v_mov_b32_e32 v118, v2
	v_mov_b32_e32 v119, v2
	v_mov_b32_e32 v120, v2
	v_mov_b32_e32 v121, v2
	v_mov_b32_e32 v74, v2
	v_mov_b32_e32 v75, v2
	v_mov_b32_e32 v76, v2
	v_mov_b32_e32 v77, v2
	v_mov_b32_e32 v78, v2
	v_mov_b32_e32 v79, v2
	v_mov_b32_e32 v80, v2
	v_mov_b32_e32 v81, v2
	v_mov_b32_e32 v90, v2
	v_mov_b32_e32 v91, v2
	v_mov_b32_e32 v92, v2
	v_mov_b32_e32 v93, v2
	v_mov_b32_e32 v94, v2
	v_mov_b32_e32 v95, v2
	v_mov_b32_e32 v96, v2
	v_mov_b32_e32 v97, v2
	v_mov_b32_e32 v106, v2
	v_mov_b32_e32 v107, v2
	v_mov_b32_e32 v108, v2
	v_mov_b32_e32 v109, v2
	v_mov_b32_e32 v110, v2
	v_mov_b32_e32 v111, v2
	v_mov_b32_e32 v112, v2
	v_mov_b32_e32 v113, v2
	v_mov_b32_e32 v130, v2
	v_mov_b32_e32 v131, v2
	v_mov_b32_e32 v132, v2
	v_mov_b32_e32 v133, v2
	v_mov_b32_e32 v134, v2
	v_mov_b32_e32 v135, v2
	v_mov_b32_e32 v136, v2
	v_mov_b32_e32 v137, v2
	s_branch .LBB0_2459

.LBB0_2626:
	s_add_u32 s26, s6, 0xfffc0080
	s_addc_u32 s27, s7, -1
	s_add_i32 s50, 0, 0x10000
	s_cmp_eq_u32 s49, 12
	s_cselect_b32 s29, s21, s27
	s_cselect_b32 s28, s33, s26
	v_add_u32_e32 v0, s50, v181
	s_cselect_b32 s27, s19, s48
	s_cselect_b32 s26, s40, s41
	s_add_i32 s58, 0, 0x14000
	ds_read_b128 v[130:133], v0
	ds_read_b128 v[134:137], v0 offset:1024
	ds_read_b128 v[138:141], v0 offset:2048
	ds_read_b128 v[142:145], v0 offset:3072
	v_add_u32_e32 v0, s58, v181
	ds_read_b128 v[146:149], v0
	ds_read_b128 v[150:153], v0 offset:1024
	ds_read_b128 v[154:157], v0 offset:2048
	ds_read_b128 v[170:173], v0 offset:3072
	v_lshl_add_u64 v[178:179], s[6:7], 0, v[168:169]
	s_add_i32 m0, s36, 0xc000
	ds_read_b128 v[174:177], v183
	ds_read_b128 v[184:187], v183 offset:1024
	ds_read_b128 v[188:191], v183 offset:2048
	ds_read_b128 v[192:195], v183 offset:3072
	ds_read_b128 v[196:199], v183 offset:4096
	ds_read_b128 v[200:203], v183 offset:5120
	ds_read_b128 v[204:207], v183 offset:6144
	ds_read_b128 v[216:219], v183 offset:7168
	global_load_lds_dwordx4 v[178:179], off
	v_lshl_add_u64 v[178:179], s[6:7], 0, v[166:167]
	s_add_i32 m0, s36, 0xe000
	s_nop 0
	global_load_lds_dwordx4 v[178:179], off
	s_waitcnt vmcnt(8)
	s_waitcnt lgkmcnt(0)
	s_barrier
	s_setprio 1
	s_waitcnt lgkmcnt(0)
	v_mfma_f32_16x16x32_bf16 v[126:129], v[130:133], v[174:177], v[126:129]
	v_mfma_f32_16x16x32_bf16 v[122:125], v[138:141], v[174:177], v[122:125]
	v_mfma_f32_16x16x32_bf16 v[110:113], v[130:133], v[188:191], v[110:113]
	v_mfma_f32_16x16x32_bf16 v[106:109], v[138:141], v[188:191], v[106:109]
	v_mfma_f32_16x16x32_bf16 v[94:97], v[130:133], v[196:199], v[94:97]
	v_mfma_f32_16x16x32_bf16 v[90:93], v[138:141], v[196:199], v[90:93]
	v_mfma_f32_16x16x32_bf16 v[78:81], v[130:133], v[204:207], v[78:81]
	v_mfma_f32_16x16x32_bf16 v[74:77], v[138:141], v[204:207], v[74:77]
	v_mfma_f32_16x16x32_bf16 v[126:129], v[134:137], v[184:187], v[126:129]
	v_mfma_f32_16x16x32_bf16 v[122:125], v[142:145], v[184:187], v[122:125]
	v_mfma_f32_16x16x32_bf16 v[110:113], v[134:137], v[192:195], v[110:113]
	v_mfma_f32_16x16x32_bf16 v[106:109], v[142:145], v[192:195], v[106:109]
	v_mfma_f32_16x16x32_bf16 v[94:97], v[134:137], v[200:203], v[94:97]
	v_mfma_f32_16x16x32_bf16 v[90:93], v[142:145], v[200:203], v[90:93]
	v_mfma_f32_16x16x32_bf16 v[78:81], v[134:137], v[216:219], v[78:81]
	v_mfma_f32_16x16x32_bf16 v[74:77], v[142:145], v[216:219], v[74:77]
	v_mfma_f32_16x16x32_bf16 v[118:121], v[146:149], v[174:177], v[118:121]
	v_mfma_f32_16x16x32_bf16 v[114:117], v[154:157], v[174:177], v[114:117]
	v_mfma_f32_16x16x32_bf16 v[102:105], v[146:149], v[188:191], v[102:105]
	v_mfma_f32_16x16x32_bf16 v[98:101], v[154:157], v[188:191], v[98:101]
	v_mfma_f32_16x16x32_bf16 v[86:89], v[146:149], v[196:199], v[86:89]
	v_mfma_f32_16x16x32_bf16 v[82:85], v[154:157], v[196:199], v[82:85]
	v_mfma_f32_16x16x32_bf16 v[70:73], v[146:149], v[204:207], v[70:73]
	v_mfma_f32_16x16x32_bf16 v[66:69], v[154:157], v[204:207], v[66:69]
	v_mfma_f32_16x16x32_bf16 v[118:121], v[150:153], v[184:187], v[118:121]
	v_mfma_f32_16x16x32_bf16 v[114:117], v[170:173], v[184:187], v[114:117]
	v_mfma_f32_16x16x32_bf16 v[102:105], v[150:153], v[192:195], v[102:105]
	v_mfma_f32_16x16x32_bf16 v[98:101], v[170:173], v[192:195], v[98:101]
	v_mfma_f32_16x16x32_bf16 v[86:89], v[150:153], v[200:203], v[86:89]
	v_mfma_f32_16x16x32_bf16 v[82:85], v[170:173], v[200:203], v[82:85]
	v_mfma_f32_16x16x32_bf16 v[70:73], v[150:153], v[216:219], v[70:73]
	v_mfma_f32_16x16x32_bf16 v[66:69], v[170:173], v[216:219], v[66:69]
	s_setprio 0
	s_barrier
	s_add_i32 s50, s50, s35
	v_lshl_add_u64 v[178:179], s[26:27], 0, v[162:163]
	s_mov_b32 m0, s50
	ds_read_b128 v[174:177], v183 offset:16384
	ds_read_b128 v[184:187], v183 offset:17408
	ds_read_b128 v[188:191], v183 offset:18432
	ds_read_b128 v[192:195], v183 offset:19456
	ds_read_b128 v[196:199], v183 offset:20480
	ds_read_b128 v[200:203], v183 offset:21504
	ds_read_b128 v[204:207], v183 offset:22528
	ds_read_b128 v[216:219], v183 offset:23552
	global_load_lds_dwordx4 v[178:179], off
	s_add_i32 m0, s50, 0x2000
	s_add_u32 s52, s26, 0x40000
	v_lshl_add_u64 v[208:209], s[26:27], 0, v[158:159]
	s_addc_u32 s53, s27, 0
	s_add_i32 s50, s58, s35
	global_load_lds_dwordx4 v[208:209], off
	v_lshl_add_u64 v[220:221], s[52:53], 0, v[162:163]
	s_mov_b32 m0, s50
	v_lshl_add_u64 v[222:223], s[28:29], 0, v[160:161]
	global_load_lds_dwordx4 v[220:221], off
	v_lshl_add_u64 v[220:221], s[52:53], 0, v[158:159]
	s_add_i32 m0, s50, 0x2000
	s_nop 0
	global_load_lds_dwordx4 v[220:221], off
	v_lshl_add_u64 v[220:221], s[28:29], 0, v[164:165]
	s_mov_b32 m0, s36
	s_nop 0
	global_load_lds_dwordx4 v[220:221], off
	s_mov_b32 m0, s37
	s_nop 0
	global_load_lds_dwordx4 v[222:223], off
	s_waitcnt vmcnt(8)
	s_waitcnt lgkmcnt(0)
	s_barrier
	s_setprio 1
	s_waitcnt lgkmcnt(0)
	v_mfma_f32_16x16x32_bf16 v[62:65], v[130:133], v[174:177], v[62:65]
	v_mfma_f32_16x16x32_bf16 v[58:61], v[138:141], v[174:177], v[58:61]
	v_mfma_f32_16x16x32_bf16 v[46:49], v[130:133], v[188:191], v[46:49]
	v_mfma_f32_16x16x32_bf16 v[42:45], v[138:141], v[188:191], v[42:45]
	v_mfma_f32_16x16x32_bf16 v[30:33], v[130:133], v[196:199], v[30:33]
	v_mfma_f32_16x16x32_bf16 v[26:29], v[138:141], v[196:199], v[26:29]
	v_mfma_f32_16x16x32_bf16 v[14:17], v[130:133], v[204:207], v[14:17]
	v_mfma_f32_16x16x32_bf16 v[10:13], v[138:141], v[204:207], v[10:13]
	v_mfma_f32_16x16x32_bf16 v[62:65], v[134:137], v[184:187], v[62:65]
	v_mfma_f32_16x16x32_bf16 v[58:61], v[142:145], v[184:187], v[58:61]
	v_mfma_f32_16x16x32_bf16 v[46:49], v[134:137], v[192:195], v[46:49]
	v_mfma_f32_16x16x32_bf16 v[42:45], v[142:145], v[192:195], v[42:45]
	v_mfma_f32_16x16x32_bf16 v[30:33], v[134:137], v[200:203], v[30:33]
	v_mfma_f32_16x16x32_bf16 v[26:29], v[142:145], v[200:203], v[26:29]
	v_mfma_f32_16x16x32_bf16 v[14:17], v[134:137], v[216:219], v[14:17]
	v_mfma_f32_16x16x32_bf16 v[10:13], v[142:145], v[216:219], v[10:13]
	v_mfma_f32_16x16x32_bf16 v[54:57], v[146:149], v[174:177], v[54:57]
	v_mfma_f32_16x16x32_bf16 v[50:53], v[154:157], v[174:177], v[50:53]
	v_mfma_f32_16x16x32_bf16 v[38:41], v[146:149], v[188:191], v[38:41]
	v_mfma_f32_16x16x32_bf16 v[34:37], v[154:157], v[188:191], v[34:37]
	v_mfma_f32_16x16x32_bf16 v[22:25], v[146:149], v[196:199], v[22:25]
	v_mfma_f32_16x16x32_bf16 v[18:21], v[154:157], v[196:199], v[18:21]
	v_mfma_f32_16x16x32_bf16 v[6:9], v[146:149], v[204:207], v[6:9]
	v_mfma_f32_16x16x32_bf16 v[2:5], v[154:157], v[204:207], v[2:5]
	v_mfma_f32_16x16x32_bf16 v[54:57], v[150:153], v[184:187], v[54:57]
	v_mfma_f32_16x16x32_bf16 v[50:53], v[170:173], v[184:187], v[50:53]
	v_mfma_f32_16x16x32_bf16 v[38:41], v[150:153], v[192:195], v[38:41]
	v_mfma_f32_16x16x32_bf16 v[34:37], v[170:173], v[192:195], v[34:37]
	v_mfma_f32_16x16x32_bf16 v[22:25], v[150:153], v[200:203], v[22:25]
	v_mfma_f32_16x16x32_bf16 v[18:21], v[170:173], v[200:203], v[18:21]
	v_mfma_f32_16x16x32_bf16 v[6:9], v[150:153], v[216:219], v[6:9]
	v_mfma_f32_16x16x32_bf16 v[2:5], v[170:173], v[216:219], v[2:5]
	s_setprio 0
	s_barrier
	s_add_i32 s50, 0, 0x18000
	v_add_u32_e32 v0, s50, v181
	s_add_i32 s52, 0, 0x1c000
	ds_read_b128 v[130:133], v0
	ds_read_b128 v[134:137], v0 offset:1024
	ds_read_b128 v[138:141], v0 offset:2048
	ds_read_b128 v[142:145], v0 offset:3072
	v_add_u32_e32 v0, s52, v181
	ds_read_b128 v[146:149], v0
	ds_read_b128 v[150:153], v0 offset:1024
	ds_read_b128 v[154:157], v0 offset:2048
	ds_read_b128 v[170:173], v0 offset:3072
	s_add_u32 s28, s28, 0x40000
	s_addc_u32 s29, s29, 0
	s_mov_b32 m0, s42
	v_lshl_add_u64 v[224:225], s[28:29], 0, v[164:165]
	ds_read_b128 v[174:177], v183 offset:32768
	ds_read_b128 v[184:187], v183 offset:33792
	ds_read_b128 v[188:191], v183 offset:34816
	ds_read_b128 v[192:195], v183 offset:35840
	ds_read_b128 v[196:199], v183 offset:36864
	ds_read_b128 v[200:203], v183 offset:37888
	ds_read_b128 v[204:207], v183 offset:38912
	ds_read_b128 v[216:219], v183 offset:39936
	global_load_lds_dwordx4 v[224:225], off
	v_lshl_add_u64 v[224:225], s[28:29], 0, v[160:161]
	s_mov_b32 m0, s43
	s_nop 0
	global_load_lds_dwordx4 v[224:225], off
	s_waitcnt vmcnt(8)
	s_waitcnt lgkmcnt(0)
	s_barrier
	s_setprio 1
	s_waitcnt lgkmcnt(0)
	v_mfma_f32_16x16x32_bf16 v[126:129], v[130:133], v[174:177], v[126:129]
	v_mfma_f32_16x16x32_bf16 v[122:125], v[138:141], v[174:177], v[122:125]
	v_mfma_f32_16x16x32_bf16 v[110:113], v[130:133], v[188:191], v[110:113]
	v_mfma_f32_16x16x32_bf16 v[106:109], v[138:141], v[188:191], v[106:109]
	v_mfma_f32_16x16x32_bf16 v[94:97], v[130:133], v[196:199], v[94:97]
	v_mfma_f32_16x16x32_bf16 v[90:93], v[138:141], v[196:199], v[90:93]
	v_mfma_f32_16x16x32_bf16 v[78:81], v[130:133], v[204:207], v[78:81]
	v_mfma_f32_16x16x32_bf16 v[74:77], v[138:141], v[204:207], v[74:77]
	v_mfma_f32_16x16x32_bf16 v[126:129], v[134:137], v[184:187], v[126:129]
	v_mfma_f32_16x16x32_bf16 v[122:125], v[142:145], v[184:187], v[122:125]
	v_mfma_f32_16x16x32_bf16 v[110:113], v[134:137], v[192:195], v[110:113]
	v_mfma_f32_16x16x32_bf16 v[106:109], v[142:145], v[192:195], v[106:109]
	v_mfma_f32_16x16x32_bf16 v[94:97], v[134:137], v[200:203], v[94:97]
	v_mfma_f32_16x16x32_bf16 v[90:93], v[142:145], v[200:203], v[90:93]
	v_mfma_f32_16x16x32_bf16 v[78:81], v[134:137], v[216:219], v[78:81]
	v_mfma_f32_16x16x32_bf16 v[74:77], v[142:145], v[216:219], v[74:77]
	v_mfma_f32_16x16x32_bf16 v[118:121], v[146:149], v[174:177], v[118:121]
	v_mfma_f32_16x16x32_bf16 v[114:117], v[154:157], v[174:177], v[114:117]
	v_mfma_f32_16x16x32_bf16 v[102:105], v[146:149], v[188:191], v[102:105]
	v_mfma_f32_16x16x32_bf16 v[98:101], v[154:157], v[188:191], v[98:101]
	v_mfma_f32_16x16x32_bf16 v[86:89], v[146:149], v[196:199], v[86:89]
	v_mfma_f32_16x16x32_bf16 v[82:85], v[154:157], v[196:199], v[82:85]
	v_mfma_f32_16x16x32_bf16 v[70:73], v[146:149], v[204:207], v[70:73]
	v_mfma_f32_16x16x32_bf16 v[66:69], v[154:157], v[204:207], v[66:69]
	v_mfma_f32_16x16x32_bf16 v[118:121], v[150:153], v[184:187], v[118:121]
	v_mfma_f32_16x16x32_bf16 v[114:117], v[170:173], v[184:187], v[114:117]
	v_mfma_f32_16x16x32_bf16 v[102:105], v[150:153], v[192:195], v[102:105]
	v_mfma_f32_16x16x32_bf16 v[98:101], v[170:173], v[192:195], v[98:101]
	v_mfma_f32_16x16x32_bf16 v[86:89], v[150:153], v[200:203], v[86:89]
	v_mfma_f32_16x16x32_bf16 v[82:85], v[170:173], v[200:203], v[82:85]
	v_mfma_f32_16x16x32_bf16 v[70:73], v[150:153], v[216:219], v[70:73]
	v_mfma_f32_16x16x32_bf16 v[66:69], v[170:173], v[216:219], v[66:69]
	s_setprio 0
	s_barrier
	s_add_i32 s28, s50, s35
	v_lshl_add_u64 v[178:179], v[178:179], 0, s[56:57]
	s_mov_b32 m0, s28
	ds_read_b128 v[174:177], v183 offset:49152
	ds_read_b128 v[184:187], v183 offset:50176
	ds_read_b128 v[188:191], v183 offset:51200
	ds_read_b128 v[192:195], v183 offset:52224
	ds_read_b128 v[196:199], v183 offset:53248
	ds_read_b128 v[200:203], v183 offset:54272
	ds_read_b128 v[204:207], v183 offset:55296
	ds_read_b128 v[216:219], v183 offset:56320
	global_load_lds_dwordx4 v[178:179], off
	s_add_i32 m0, s28, 0x2000
	s_add_u32 s26, s26, 0x40080
	v_lshl_add_u64 v[178:179], v[208:209], 0, s[56:57]
	s_addc_u32 s27, s27, 0
	s_add_i32 s28, s52, s35
	global_load_lds_dwordx4 v[178:179], off
	v_lshl_add_u64 v[178:179], s[26:27], 0, v[162:163]
	s_mov_b32 m0, s28
	s_nop 0
	global_load_lds_dwordx4 v[178:179], off
	v_lshl_add_u64 v[178:179], s[26:27], 0, v[158:159]
	s_add_i32 m0, s28, 0x2000
	s_nop 0
	global_load_lds_dwordx4 v[178:179], off
	v_lshl_add_u64 v[178:179], v[220:221], 0, s[56:57]
	s_mov_b32 m0, s44
	s_nop 0
	global_load_lds_dwordx4 v[178:179], off
	v_lshl_add_u64 v[178:179], v[222:223], 0, s[56:57]
	s_mov_b32 m0, s45
	s_nop 0
	global_load_lds_dwordx4 v[178:179], off
	s_waitcnt vmcnt(8)
	s_waitcnt lgkmcnt(0)
	s_barrier
	s_setprio 1
	s_waitcnt lgkmcnt(0)
	v_mfma_f32_16x16x32_bf16 v[62:65], v[130:133], v[174:177], v[62:65]
	v_mfma_f32_16x16x32_bf16 v[58:61], v[138:141], v[174:177], v[58:61]
	v_mfma_f32_16x16x32_bf16 v[46:49], v[130:133], v[188:191], v[46:49]
	v_mfma_f32_16x16x32_bf16 v[42:45], v[138:141], v[188:191], v[42:45]
	v_mfma_f32_16x16x32_bf16 v[30:33], v[130:133], v[196:199], v[30:33]
	v_mfma_f32_16x16x32_bf16 v[26:29], v[138:141], v[196:199], v[26:29]
	v_mfma_f32_16x16x32_bf16 v[14:17], v[130:133], v[204:207], v[14:17]
	v_mfma_f32_16x16x32_bf16 v[10:13], v[138:141], v[204:207], v[10:13]
	v_mfma_f32_16x16x32_bf16 v[62:65], v[134:137], v[184:187], v[62:65]
	v_mfma_f32_16x16x32_bf16 v[58:61], v[142:145], v[184:187], v[58:61]
	v_mfma_f32_16x16x32_bf16 v[46:49], v[134:137], v[192:195], v[46:49]
	v_mfma_f32_16x16x32_bf16 v[42:45], v[142:145], v[192:195], v[42:45]
	v_mfma_f32_16x16x32_bf16 v[30:33], v[134:137], v[200:203], v[30:33]
	v_mfma_f32_16x16x32_bf16 v[26:29], v[142:145], v[200:203], v[26:29]
	v_mfma_f32_16x16x32_bf16 v[14:17], v[134:137], v[216:219], v[14:17]
	v_mfma_f32_16x16x32_bf16 v[10:13], v[142:145], v[216:219], v[10:13]
	v_mfma_f32_16x16x32_bf16 v[54:57], v[146:149], v[174:177], v[54:57]
	v_mfma_f32_16x16x32_bf16 v[50:53], v[154:157], v[174:177], v[50:53]
	v_mfma_f32_16x16x32_bf16 v[38:41], v[146:149], v[188:191], v[38:41]
	v_mfma_f32_16x16x32_bf16 v[34:37], v[154:157], v[188:191], v[34:37]
	v_mfma_f32_16x16x32_bf16 v[22:25], v[146:149], v[196:199], v[22:25]
	v_mfma_f32_16x16x32_bf16 v[18:21], v[154:157], v[196:199], v[18:21]
	v_mfma_f32_16x16x32_bf16 v[6:9], v[146:149], v[204:207], v[6:9]
	v_mfma_f32_16x16x32_bf16 v[2:5], v[154:157], v[204:207], v[2:5]
	v_mfma_f32_16x16x32_bf16 v[54:57], v[150:153], v[184:187], v[54:57]
	v_mfma_f32_16x16x32_bf16 v[50:53], v[170:173], v[184:187], v[50:53]
	v_mfma_f32_16x16x32_bf16 v[38:41], v[150:153], v[192:195], v[38:41]
	v_mfma_f32_16x16x32_bf16 v[34:37], v[170:173], v[192:195], v[34:37]
	v_mfma_f32_16x16x32_bf16 v[22:25], v[150:153], v[200:203], v[22:25]
	v_mfma_f32_16x16x32_bf16 v[18:21], v[170:173], v[200:203], v[18:21]
	v_mfma_f32_16x16x32_bf16 v[6:9], v[150:153], v[216:219], v[6:9]
	v_mfma_f32_16x16x32_bf16 v[2:5], v[170:173], v[216:219], v[2:5]
	s_setprio 0
	s_barrier
	s_add_i32 s49, s49, 2
	s_add_u32 s41, s41, 0x100
	s_addc_u32 s48, s48, 0
	s_add_u32 s6, s6, 0x100
	s_addc_u32 s7, s7, 0
	s_cmp_gt_u32 s49, 13
	s_cbranch_scc0 .LBB0_2626
	s_and_b64 vcc, exec, s[16:17]
	s_cbranch_vccz .LBB0_2629
	s_barrier

.LBB0_2703:
	s_add_u32 s44, s24, s36
	s_addc_u32 s45, s25, s37
	s_add_u32 s44, s44, 0x100
	s_addc_u32 s45, s45, 0
	s_add_u32 s50, s59, s36
	s_addc_u32 s64, s82, s37
	s_add_i32 s65, 0, 0x10000
	s_cmpk_eq_i32 s36, 0x1f00
	s_cselect_b32 s47, s29, s45
	s_cselect_b32 s46, s83, s44
	s_cselect_b32 s45, s27, s64
	s_cselect_b32 s44, s84, s50
	s_add_i32 s50, 0, 0x14000
	v_add_u32_e32 v160, s65, v146
	v_add_u32_e32 v164, s50, v146
	ds_read_b128 v[148:151], v160
	ds_read_b128 v[152:155], v160 offset:1024
	ds_read_b128 v[156:159], v160 offset:2048
	ds_read_b128 v[160:163], v160 offset:3072
	ds_read_b128 v[168:171], v164
	ds_read_b128 v[172:175], v164 offset:1024
	ds_read_b128 v[176:179], v164 offset:2048
	ds_read_b128 v[180:183], v164 offset:3072
	v_lshl_add_u64 v[164:165], v[144:145], 0, s[36:37]
	s_add_i32 m0, s4, 0xc000
	ds_read_b128 v[184:187], v147
	ds_read_b128 v[188:191], v147 offset:1024
	ds_read_b128 v[192:195], v147 offset:2048
	ds_read_b128 v[196:199], v147 offset:3072
	ds_read_b128 v[200:203], v147 offset:4096
	ds_read_b128 v[204:207], v147 offset:5120
	ds_read_b128 v[216:219], v147 offset:6144
	ds_read_b128 v[220:223], v147 offset:7168
	global_load_lds_dwordx4 v[164:165], off
	v_lshl_add_u64 v[164:165], v[142:143], 0, s[36:37]
	s_add_i32 m0, s4, 0xe000
	s_nop 0
	global_load_lds_dwordx4 v[164:165], off
	s_waitcnt vmcnt(8)
	s_waitcnt lgkmcnt(0)
	s_barrier
	s_setprio 1
	s_waitcnt lgkmcnt(0)
	v_mfma_f32_16x16x32_bf16 v[134:137], v[148:151], v[184:187], v[134:137]
	v_mfma_f32_16x16x32_bf16 v[130:133], v[156:159], v[184:187], v[130:133]
	v_mfma_f32_16x16x32_bf16 v[110:113], v[148:151], v[192:195], v[110:113]
	v_mfma_f32_16x16x32_bf16 v[106:109], v[156:159], v[192:195], v[106:109]
	v_mfma_f32_16x16x32_bf16 v[94:97], v[148:151], v[200:203], v[94:97]
	v_mfma_f32_16x16x32_bf16 v[90:93], v[156:159], v[200:203], v[90:93]
	v_mfma_f32_16x16x32_bf16 v[78:81], v[148:151], v[216:219], v[78:81]
	v_mfma_f32_16x16x32_bf16 v[74:77], v[156:159], v[216:219], v[74:77]
	v_mfma_f32_16x16x32_bf16 v[134:137], v[152:155], v[188:191], v[134:137]
	v_mfma_f32_16x16x32_bf16 v[130:133], v[160:163], v[188:191], v[130:133]
	v_mfma_f32_16x16x32_bf16 v[110:113], v[152:155], v[196:199], v[110:113]
	v_mfma_f32_16x16x32_bf16 v[106:109], v[160:163], v[196:199], v[106:109]
	v_mfma_f32_16x16x32_bf16 v[94:97], v[152:155], v[204:207], v[94:97]
	v_mfma_f32_16x16x32_bf16 v[90:93], v[160:163], v[204:207], v[90:93]
	v_mfma_f32_16x16x32_bf16 v[78:81], v[152:155], v[220:223], v[78:81]
	v_mfma_f32_16x16x32_bf16 v[74:77], v[160:163], v[220:223], v[74:77]
	v_mfma_f32_16x16x32_bf16 v[122:125], v[168:171], v[184:187], v[122:125]
	v_mfma_f32_16x16x32_bf16 v[114:117], v[176:179], v[184:187], v[114:117]
	v_mfma_f32_16x16x32_bf16 v[102:105], v[168:171], v[192:195], v[102:105]
	v_mfma_f32_16x16x32_bf16 v[98:101], v[176:179], v[192:195], v[98:101]
	v_mfma_f32_16x16x32_bf16 v[86:89], v[168:171], v[200:203], v[86:89]
	v_mfma_f32_16x16x32_bf16 v[82:85], v[176:179], v[200:203], v[82:85]
	v_mfma_f32_16x16x32_bf16 v[70:73], v[168:171], v[216:219], v[70:73]
	v_mfma_f32_16x16x32_bf16 v[66:69], v[176:179], v[216:219], v[66:69]
	v_mfma_f32_16x16x32_bf16 v[122:125], v[172:175], v[188:191], v[122:125]
	v_mfma_f32_16x16x32_bf16 v[114:117], v[180:183], v[188:191], v[114:117]
	v_mfma_f32_16x16x32_bf16 v[102:105], v[172:175], v[196:199], v[102:105]
	v_mfma_f32_16x16x32_bf16 v[98:101], v[180:183], v[196:199], v[98:101]
	v_mfma_f32_16x16x32_bf16 v[86:89], v[172:175], v[204:207], v[86:89]
	v_mfma_f32_16x16x32_bf16 v[82:85], v[180:183], v[204:207], v[82:85]
	v_mfma_f32_16x16x32_bf16 v[70:73], v[172:175], v[220:223], v[70:73]
	v_mfma_f32_16x16x32_bf16 v[66:69], v[180:183], v[220:223], v[66:69]
	s_setprio 0
	s_barrier
	s_add_i32 s64, s65, s77
	v_lshl_add_u64 v[164:165], s[44:45], 0, v[126:127]
	s_mov_b32 m0, s64
	ds_read_b128 v[184:187], v147 offset:16384
	ds_read_b128 v[188:191], v147 offset:17408
	ds_read_b128 v[192:195], v147 offset:18432
	ds_read_b128 v[196:199], v147 offset:19456
	ds_read_b128 v[200:203], v147 offset:20480
	ds_read_b128 v[204:207], v147 offset:21504
	ds_read_b128 v[216:219], v147 offset:22528
	ds_read_b128 v[220:223], v147 offset:23552
	global_load_lds_dwordx4 v[164:165], off
	s_add_i32 m0, s64, 0x2000
	s_add_u32 s92, s44, 0x100000
	v_lshl_add_u64 v[208:209], s[44:45], 0, v[118:119]
	s_addc_u32 s93, s45, 0
	s_add_i32 s50, s50, s77
	global_load_lds_dwordx4 v[208:209], off
	v_lshl_add_u64 v[224:225], s[92:93], 0, v[126:127]
	s_mov_b32 m0, s50
	v_lshl_add_u64 v[242:243], s[46:47], 0, v[120:121]
	global_load_lds_dwordx4 v[224:225], off
	v_lshl_add_u64 v[224:225], s[92:93], 0, v[118:119]
	s_add_i32 m0, s50, 0x2000
	s_nop 0
	global_load_lds_dwordx4 v[224:225], off
	v_lshl_add_u64 v[224:225], s[46:47], 0, v[128:129]
	s_mov_b32 m0, s4
	s_nop 0
	global_load_lds_dwordx4 v[224:225], off
	s_mov_b32 m0, s33
	s_nop 0
	global_load_lds_dwordx4 v[242:243], off
	s_waitcnt vmcnt(8)
	s_waitcnt lgkmcnt(0)
	s_barrier
	s_setprio 1
	s_waitcnt lgkmcnt(0)
	v_mfma_f32_16x16x32_bf16 v[62:65], v[148:151], v[184:187], v[62:65]
	v_mfma_f32_16x16x32_bf16 v[58:61], v[156:159], v[184:187], v[58:61]
	v_mfma_f32_16x16x32_bf16 v[46:49], v[148:151], v[192:195], v[46:49]
	v_mfma_f32_16x16x32_bf16 v[42:45], v[156:159], v[192:195], v[42:45]
	v_mfma_f32_16x16x32_bf16 v[30:33], v[148:151], v[200:203], v[30:33]
	v_mfma_f32_16x16x32_bf16 v[26:29], v[156:159], v[200:203], v[26:29]
	v_mfma_f32_16x16x32_bf16 v[14:17], v[148:151], v[216:219], v[14:17]
	v_mfma_f32_16x16x32_bf16 v[10:13], v[156:159], v[216:219], v[10:13]
	v_mfma_f32_16x16x32_bf16 v[62:65], v[152:155], v[188:191], v[62:65]
	v_mfma_f32_16x16x32_bf16 v[58:61], v[160:163], v[188:191], v[58:61]
	v_mfma_f32_16x16x32_bf16 v[46:49], v[152:155], v[196:199], v[46:49]
	v_mfma_f32_16x16x32_bf16 v[42:45], v[160:163], v[196:199], v[42:45]
	v_mfma_f32_16x16x32_bf16 v[30:33], v[152:155], v[204:207], v[30:33]
	v_mfma_f32_16x16x32_bf16 v[26:29], v[160:163], v[204:207], v[26:29]
	v_mfma_f32_16x16x32_bf16 v[14:17], v[152:155], v[220:223], v[14:17]
	v_mfma_f32_16x16x32_bf16 v[10:13], v[160:163], v[220:223], v[10:13]
	v_mfma_f32_16x16x32_bf16 v[54:57], v[168:171], v[184:187], v[54:57]
	v_mfma_f32_16x16x32_bf16 v[50:53], v[176:179], v[184:187], v[50:53]
	v_mfma_f32_16x16x32_bf16 v[38:41], v[168:171], v[192:195], v[38:41]
	v_mfma_f32_16x16x32_bf16 v[34:37], v[176:179], v[192:195], v[34:37]
	v_mfma_f32_16x16x32_bf16 v[22:25], v[168:171], v[200:203], v[22:25]
	v_mfma_f32_16x16x32_bf16 v[18:21], v[176:179], v[200:203], v[18:21]
	v_mfma_f32_16x16x32_bf16 v[6:9], v[168:171], v[216:219], v[6:9]
	v_mfma_f32_16x16x32_bf16 v[2:5], v[176:179], v[216:219], v[2:5]
	v_mfma_f32_16x16x32_bf16 v[54:57], v[172:175], v[188:191], v[54:57]
	v_mfma_f32_16x16x32_bf16 v[50:53], v[180:183], v[188:191], v[50:53]
	v_mfma_f32_16x16x32_bf16 v[38:41], v[172:175], v[196:199], v[38:41]
	v_mfma_f32_16x16x32_bf16 v[34:37], v[180:183], v[196:199], v[34:37]
	v_mfma_f32_16x16x32_bf16 v[22:25], v[172:175], v[204:207], v[22:25]
	v_mfma_f32_16x16x32_bf16 v[18:21], v[180:183], v[204:207], v[18:21]
	v_mfma_f32_16x16x32_bf16 v[6:9], v[172:175], v[220:223], v[6:9]
	v_mfma_f32_16x16x32_bf16 v[2:5], v[180:183], v[220:223], v[2:5]
	s_setprio 0
	s_barrier
	s_add_i32 s50, 0, 0x18000
	s_add_i32 s64, 0, 0x1c000
	v_add_u32_e32 v160, s50, v146
	v_add_u32_e32 v167, s64, v146
	ds_read_b128 v[148:151], v160
	ds_read_b128 v[152:155], v160 offset:1024
	ds_read_b128 v[156:159], v160 offset:2048
	ds_read_b128 v[160:163], v160 offset:3072
	ds_read_b128 v[168:171], v167
	ds_read_b128 v[172:175], v167 offset:1024
	ds_read_b128 v[176:179], v167 offset:2048
	ds_read_b128 v[180:183], v167 offset:3072
	s_add_u32 s46, s46, 0x100000
	s_addc_u32 s47, s47, 0
	s_mov_b32 m0, s78
	v_lshl_add_u64 v[244:245], s[46:47], 0, v[128:129]
	ds_read_b128 v[184:187], v147 offset:32768
	ds_read_b128 v[188:191], v147 offset:33792
	ds_read_b128 v[192:195], v147 offset:34816
	ds_read_b128 v[196:199], v147 offset:35840
	ds_read_b128 v[200:203], v147 offset:36864
	ds_read_b128 v[204:207], v147 offset:37888
	ds_read_b128 v[216:219], v147 offset:38912
	ds_read_b128 v[220:223], v147 offset:39936
	global_load_lds_dwordx4 v[244:245], off
	v_lshl_add_u64 v[244:245], s[46:47], 0, v[120:121]
	s_mov_b32 m0, s79
	s_nop 0
	global_load_lds_dwordx4 v[244:245], off
	s_waitcnt vmcnt(8)
	s_waitcnt lgkmcnt(0)
	s_barrier
	s_setprio 1
	s_waitcnt lgkmcnt(0)
	v_mfma_f32_16x16x32_bf16 v[134:137], v[148:151], v[184:187], v[134:137]
	v_mfma_f32_16x16x32_bf16 v[130:133], v[156:159], v[184:187], v[130:133]
	v_mfma_f32_16x16x32_bf16 v[110:113], v[148:151], v[192:195], v[110:113]
	v_mfma_f32_16x16x32_bf16 v[106:109], v[156:159], v[192:195], v[106:109]
	v_mfma_f32_16x16x32_bf16 v[94:97], v[148:151], v[200:203], v[94:97]
	v_mfma_f32_16x16x32_bf16 v[90:93], v[156:159], v[200:203], v[90:93]
	v_mfma_f32_16x16x32_bf16 v[78:81], v[148:151], v[216:219], v[78:81]
	v_mfma_f32_16x16x32_bf16 v[74:77], v[156:159], v[216:219], v[74:77]
	v_mfma_f32_16x16x32_bf16 v[134:137], v[152:155], v[188:191], v[134:137]
	v_mfma_f32_16x16x32_bf16 v[130:133], v[160:163], v[188:191], v[130:133]
	v_mfma_f32_16x16x32_bf16 v[110:113], v[152:155], v[196:199], v[110:113]
	v_mfma_f32_16x16x32_bf16 v[106:109], v[160:163], v[196:199], v[106:109]
	v_mfma_f32_16x16x32_bf16 v[94:97], v[152:155], v[204:207], v[94:97]
	v_mfma_f32_16x16x32_bf16 v[90:93], v[160:163], v[204:207], v[90:93]
	v_mfma_f32_16x16x32_bf16 v[78:81], v[152:155], v[220:223], v[78:81]
	v_mfma_f32_16x16x32_bf16 v[74:77], v[160:163], v[220:223], v[74:77]
	v_mfma_f32_16x16x32_bf16 v[122:125], v[168:171], v[184:187], v[122:125]
	v_mfma_f32_16x16x32_bf16 v[114:117], v[176:179], v[184:187], v[114:117]
	v_mfma_f32_16x16x32_bf16 v[102:105], v[168:171], v[192:195], v[102:105]
	v_mfma_f32_16x16x32_bf16 v[98:101], v[176:179], v[192:195], v[98:101]
	v_mfma_f32_16x16x32_bf16 v[86:89], v[168:171], v[200:203], v[86:89]
	v_mfma_f32_16x16x32_bf16 v[82:85], v[176:179], v[200:203], v[82:85]
	v_mfma_f32_16x16x32_bf16 v[70:73], v[168:171], v[216:219], v[70:73]
	v_mfma_f32_16x16x32_bf16 v[66:69], v[176:179], v[216:219], v[66:69]
	v_mfma_f32_16x16x32_bf16 v[122:125], v[172:175], v[188:191], v[122:125]
	v_mfma_f32_16x16x32_bf16 v[114:117], v[180:183], v[188:191], v[114:117]
	v_mfma_f32_16x16x32_bf16 v[102:105], v[172:175], v[196:199], v[102:105]
	v_mfma_f32_16x16x32_bf16 v[98:101], v[180:183], v[196:199], v[98:101]
	v_mfma_f32_16x16x32_bf16 v[86:89], v[172:175], v[204:207], v[86:89]
	v_mfma_f32_16x16x32_bf16 v[82:85], v[180:183], v[204:207], v[82:85]
	v_mfma_f32_16x16x32_bf16 v[70:73], v[172:175], v[220:223], v[70:73]
	v_mfma_f32_16x16x32_bf16 v[66:69], v[180:183], v[220:223], v[66:69]
	s_setprio 0
	s_barrier
	s_add_i32 s46, s50, s77
	v_lshl_add_u64 v[164:165], v[164:165], 0, s[56:57]
	s_mov_b32 m0, s46
	ds_read_b128 v[184:187], v147 offset:49152
	ds_read_b128 v[188:191], v147 offset:50176
	ds_read_b128 v[192:195], v147 offset:51200
	ds_read_b128 v[196:199], v147 offset:52224
	ds_read_b128 v[200:203], v147 offset:53248
	ds_read_b128 v[204:207], v147 offset:54272
	ds_read_b128 v[216:219], v147 offset:55296
	ds_read_b128 v[220:223], v147 offset:56320
	global_load_lds_dwordx4 v[164:165], off
	s_add_i32 m0, s46, 0x2000
	s_add_u32 s44, s44, 0x100080
	v_lshl_add_u64 v[164:165], v[208:209], 0, s[56:57]
	s_addc_u32 s45, s45, 0
	s_add_i32 s46, s64, s77
	global_load_lds_dwordx4 v[164:165], off
	v_lshl_add_u64 v[164:165], s[44:45], 0, v[126:127]
	s_mov_b32 m0, s46
	s_nop 0
	global_load_lds_dwordx4 v[164:165], off
	v_lshl_add_u64 v[164:165], s[44:45], 0, v[118:119]
	s_add_i32 m0, s46, 0x2000
	s_nop 0
	global_load_lds_dwordx4 v[164:165], off
	v_lshl_add_u64 v[164:165], v[224:225], 0, s[56:57]
	s_mov_b32 m0, s80
	s_nop 0
	global_load_lds_dwordx4 v[164:165], off
	v_lshl_add_u64 v[164:165], v[242:243], 0, s[56:57]
	s_mov_b32 m0, s81
	s_nop 0
	global_load_lds_dwordx4 v[164:165], off
	s_waitcnt vmcnt(8)
	s_waitcnt lgkmcnt(0)
	s_barrier
	s_setprio 1
	s_waitcnt lgkmcnt(0)
	v_mfma_f32_16x16x32_bf16 v[62:65], v[148:151], v[184:187], v[62:65]
	v_mfma_f32_16x16x32_bf16 v[58:61], v[156:159], v[184:187], v[58:61]
	v_mfma_f32_16x16x32_bf16 v[46:49], v[148:151], v[192:195], v[46:49]
	v_mfma_f32_16x16x32_bf16 v[42:45], v[156:159], v[192:195], v[42:45]
	v_mfma_f32_16x16x32_bf16 v[30:33], v[148:151], v[200:203], v[30:33]
	v_mfma_f32_16x16x32_bf16 v[26:29], v[156:159], v[200:203], v[26:29]
	v_mfma_f32_16x16x32_bf16 v[14:17], v[148:151], v[216:219], v[14:17]
	v_mfma_f32_16x16x32_bf16 v[10:13], v[156:159], v[216:219], v[10:13]
	v_mfma_f32_16x16x32_bf16 v[62:65], v[152:155], v[188:191], v[62:65]
	v_mfma_f32_16x16x32_bf16 v[58:61], v[160:163], v[188:191], v[58:61]
	v_mfma_f32_16x16x32_bf16 v[46:49], v[152:155], v[196:199], v[46:49]
	v_mfma_f32_16x16x32_bf16 v[42:45], v[160:163], v[196:199], v[42:45]
	v_mfma_f32_16x16x32_bf16 v[30:33], v[152:155], v[204:207], v[30:33]
	v_mfma_f32_16x16x32_bf16 v[26:29], v[160:163], v[204:207], v[26:29]
	v_mfma_f32_16x16x32_bf16 v[14:17], v[152:155], v[220:223], v[14:17]
	v_mfma_f32_16x16x32_bf16 v[10:13], v[160:163], v[220:223], v[10:13]
	v_mfma_f32_16x16x32_bf16 v[54:57], v[168:171], v[184:187], v[54:57]
	v_mfma_f32_16x16x32_bf16 v[50:53], v[176:179], v[184:187], v[50:53]
	v_mfma_f32_16x16x32_bf16 v[38:41], v[168:171], v[192:195], v[38:41]
	v_mfma_f32_16x16x32_bf16 v[34:37], v[176:179], v[192:195], v[34:37]
	v_mfma_f32_16x16x32_bf16 v[22:25], v[168:171], v[200:203], v[22:25]
	v_mfma_f32_16x16x32_bf16 v[18:21], v[176:179], v[200:203], v[18:21]
	v_mfma_f32_16x16x32_bf16 v[6:9], v[168:171], v[216:219], v[6:9]
	v_mfma_f32_16x16x32_bf16 v[2:5], v[176:179], v[216:219], v[2:5]
	v_mfma_f32_16x16x32_bf16 v[54:57], v[172:175], v[188:191], v[54:57]
	v_mfma_f32_16x16x32_bf16 v[50:53], v[180:183], v[188:191], v[50:53]
	v_mfma_f32_16x16x32_bf16 v[38:41], v[172:175], v[196:199], v[38:41]
	v_mfma_f32_16x16x32_bf16 v[34:37], v[180:183], v[196:199], v[34:37]
	v_mfma_f32_16x16x32_bf16 v[22:25], v[172:175], v[204:207], v[22:25]
	v_mfma_f32_16x16x32_bf16 v[18:21], v[180:183], v[204:207], v[18:21]
	v_mfma_f32_16x16x32_bf16 v[6:9], v[172:175], v[220:223], v[6:9]
	v_mfma_f32_16x16x32_bf16 v[2:5], v[180:183], v[220:223], v[2:5]
	s_setprio 0
	s_barrier
	s_add_i32 s85, s85, 2
	s_add_u32 s36, s36, 0x100
	s_addc_u32 s37, s37, 0
	s_cmp_gt_u32 s85, 61
	s_cbranch_scc0 .LBB0_2703
	s_add_u32 s36, s59, 0xffffff00
	s_addc_u32 s37, s82, -1
	s_andn2_b64 vcc, exec, s[42:43]
	s_cbranch_vccnz .LBB0_2706
	v_mov_b32_e32 v2, 0
	s_mov_b32 s12, s26
	s_mov_b32 s53, s28
	s_mov_b64 s[24:25], s[34:35]
	s_mov_b32 s68, s58
	v_mov_b32_e32 v3, v2
	v_mov_b32_e32 v4, v2
	v_mov_b32_e32 v5, v2
	v_mov_b32_e32 v6, v2
	v_mov_b32_e32 v7, v2
	v_mov_b32_e32 v8, v2
	v_mov_b32_e32 v9, v2
	v_mov_b32_e32 v18, v2
	v_mov_b32_e32 v19, v2
	v_mov_b32_e32 v20, v2
	v_mov_b32_e32 v21, v2
	v_mov_b32_e32 v22, v2
	v_mov_b32_e32 v23, v2
	v_mov_b32_e32 v24, v2
	v_mov_b32_e32 v25, v2
	v_mov_b32_e32 v34, v2
	v_mov_b32_e32 v35, v2
	v_mov_b32_e32 v36, v2
	v_mov_b32_e32 v37, v2
	v_mov_b32_e32 v38, v2
	v_mov_b32_e32 v39, v2
	v_mov_b32_e32 v40, v2
	v_mov_b32_e32 v41, v2
	v_mov_b32_e32 v50, v2
	v_mov_b32_e32 v51, v2
	v_mov_b32_e32 v52, v2
	v_mov_b32_e32 v53, v2
	v_mov_b32_e32 v54, v2
	v_mov_b32_e32 v55, v2
	v_mov_b32_e32 v56, v2
	v_mov_b32_e32 v57, v2
	v_mov_b32_e32 v10, v2
	v_mov_b32_e32 v11, v2
	v_mov_b32_e32 v12, v2
	v_mov_b32_e32 v13, v2
	v_mov_b32_e32 v14, v2
	v_mov_b32_e32 v15, v2
	v_mov_b32_e32 v16, v2
	v_mov_b32_e32 v17, v2
	v_mov_b32_e32 v26, v2
	v_mov_b32_e32 v27, v2
	v_mov_b32_e32 v28, v2
	v_mov_b32_e32 v29, v2
	v_mov_b32_e32 v30, v2
	v_mov_b32_e32 v31, v2
	v_mov_b32_e32 v32, v2
	v_mov_b32_e32 v33, v2
	v_mov_b32_e32 v42, v2
	v_mov_b32_e32 v43, v2
	v_mov_b32_e32 v44, v2
	v_mov_b32_e32 v45, v2
	v_mov_b32_e32 v46, v2
	v_mov_b32_e32 v47, v2
	v_mov_b32_e32 v48, v2
	v_mov_b32_e32 v49, v2
	v_mov_b32_e32 v58, v2
	v_mov_b32_e32 v59, v2
	v_mov_b32_e32 v60, v2
	v_mov_b32_e32 v61, v2
	v_mov_b32_e32 v62, v2
	v_mov_b32_e32 v63, v2
	v_mov_b32_e32 v64, v2
	v_mov_b32_e32 v65, v2
	v_mov_b32_e32 v66, v2
	v_mov_b32_e32 v67, v2
	v_mov_b32_e32 v68, v2
	v_mov_b32_e32 v69, v2
	v_mov_b32_e32 v70, v2
	v_mov_b32_e32 v71, v2
	v_mov_b32_e32 v72, v2
	v_mov_b32_e32 v73, v2
	v_mov_b32_e32 v82, v2
	v_mov_b32_e32 v83, v2
	v_mov_b32_e32 v84, v2
	v_mov_b32_e32 v85, v2
	v_mov_b32_e32 v86, v2
	v_mov_b32_e32 v87, v2
	v_mov_b32_e32 v88, v2
	v_mov_b32_e32 v89, v2
	v_mov_b32_e32 v98, v2
	v_mov_b32_e32 v99, v2
	v_mov_b32_e32 v100, v2
	v_mov_b32_e32 v101, v2
	v_mov_b32_e32 v102, v2
	v_mov_b32_e32 v103, v2
	v_mov_b32_e32 v104, v2
	v_mov_b32_e32 v105, v2
	v_mov_b32_e32 v114, v2
	v_mov_b32_e32 v115, v2
	v_mov_b32_e32 v116, v2
	v_mov_b32_e32 v117, v2
	v_mov_b32_e32 v122, v2
	v_mov_b32_e32 v123, v2
	v_mov_b32_e32 v124, v2
	v_mov_b32_e32 v125, v2
	v_mov_b32_e32 v74, v2
	v_mov_b32_e32 v75, v2
	v_mov_b32_e32 v76, v2
	v_mov_b32_e32 v77, v2
	v_mov_b32_e32 v78, v2
	v_mov_b32_e32 v79, v2
	v_mov_b32_e32 v80, v2
	v_mov_b32_e32 v81, v2
	v_mov_b32_e32 v90, v2
	v_mov_b32_e32 v91, v2
	v_mov_b32_e32 v92, v2
	v_mov_b32_e32 v93, v2
	v_mov_b32_e32 v94, v2
	v_mov_b32_e32 v95, v2
	v_mov_b32_e32 v96, v2
	v_mov_b32_e32 v97, v2
	v_mov_b32_e32 v106, v2
	v_mov_b32_e32 v107, v2
	v_mov_b32_e32 v108, v2
	v_mov_b32_e32 v109, v2
	v_mov_b32_e32 v110, v2
	v_mov_b32_e32 v111, v2
	v_mov_b32_e32 v112, v2
	v_mov_b32_e32 v113, v2
	v_mov_b32_e32 v130, v2
	v_mov_b32_e32 v131, v2
	v_mov_b32_e32 v132, v2
	v_mov_b32_e32 v133, v2
	v_mov_b32_e32 v134, v2
	v_mov_b32_e32 v135, v2
	v_mov_b32_e32 v136, v2
	v_mov_b32_e32 v137, v2
	s_movk_i32 s92, 0x2b20
	s_andn2_b64 vcc, exec, s[40:41]
	s_cbranch_vccnz .LBB0_2707
	s_branch .LBB0_2708

.LBB0_2796:
	s_add_u32 s44, s24, s36
	s_addc_u32 s45, s25, s37
	s_add_u32 s44, s44, 0x100
	s_addc_u32 s45, s45, 0
	s_add_u32 s50, s59, s36
	s_addc_u32 s64, s81, s37
	s_add_i32 s65, 0, 0x10000
	s_cmpk_eq_i32 s36, 0x1f00
	s_cselect_b32 s47, s29, s45
	s_cselect_b32 s46, s82, s44
	s_cselect_b32 s45, s27, s64
	s_cselect_b32 s44, s83, s50
	s_add_i32 s50, 0, 0x14000
	v_add_u32_e32 v160, s65, v146
	v_add_u32_e32 v164, s50, v146
	ds_read_b128 v[148:151], v160
	ds_read_b128 v[152:155], v160 offset:1024
	ds_read_b128 v[156:159], v160 offset:2048
	ds_read_b128 v[160:163], v160 offset:3072
	ds_read_b128 v[168:171], v164
	ds_read_b128 v[172:175], v164 offset:1024
	ds_read_b128 v[176:179], v164 offset:2048
	ds_read_b128 v[180:183], v164 offset:3072
	v_lshl_add_u64 v[164:165], v[144:145], 0, s[36:37]
	s_add_i32 m0, s4, 0xc000
	ds_read_b128 v[184:187], v147
	ds_read_b128 v[188:191], v147 offset:1024
	ds_read_b128 v[192:195], v147 offset:2048
	ds_read_b128 v[196:199], v147 offset:3072
	ds_read_b128 v[200:203], v147 offset:4096
	ds_read_b128 v[204:207], v147 offset:5120
	ds_read_b128 v[216:219], v147 offset:6144
	ds_read_b128 v[220:223], v147 offset:7168
	global_load_lds_dwordx4 v[164:165], off
	v_lshl_add_u64 v[164:165], v[142:143], 0, s[36:37]
	s_add_i32 m0, s4, 0xe000
	s_nop 0
	global_load_lds_dwordx4 v[164:165], off
	s_waitcnt vmcnt(8)
	s_waitcnt lgkmcnt(0)
	s_barrier
	s_setprio 1
	s_waitcnt lgkmcnt(0)
	v_mfma_f32_16x16x32_bf16 v[134:137], v[148:151], v[184:187], v[134:137]
	v_mfma_f32_16x16x32_bf16 v[130:133], v[156:159], v[184:187], v[130:133]
	v_mfma_f32_16x16x32_bf16 v[110:113], v[148:151], v[192:195], v[110:113]
	v_mfma_f32_16x16x32_bf16 v[106:109], v[156:159], v[192:195], v[106:109]
	v_mfma_f32_16x16x32_bf16 v[94:97], v[148:151], v[200:203], v[94:97]
	v_mfma_f32_16x16x32_bf16 v[90:93], v[156:159], v[200:203], v[90:93]
	v_mfma_f32_16x16x32_bf16 v[78:81], v[148:151], v[216:219], v[78:81]
	v_mfma_f32_16x16x32_bf16 v[74:77], v[156:159], v[216:219], v[74:77]
	v_mfma_f32_16x16x32_bf16 v[134:137], v[152:155], v[188:191], v[134:137]
	v_mfma_f32_16x16x32_bf16 v[130:133], v[160:163], v[188:191], v[130:133]
	v_mfma_f32_16x16x32_bf16 v[110:113], v[152:155], v[196:199], v[110:113]
	v_mfma_f32_16x16x32_bf16 v[106:109], v[160:163], v[196:199], v[106:109]
	v_mfma_f32_16x16x32_bf16 v[94:97], v[152:155], v[204:207], v[94:97]
	v_mfma_f32_16x16x32_bf16 v[90:93], v[160:163], v[204:207], v[90:93]
	v_mfma_f32_16x16x32_bf16 v[78:81], v[152:155], v[220:223], v[78:81]
	v_mfma_f32_16x16x32_bf16 v[74:77], v[160:163], v[220:223], v[74:77]
	v_mfma_f32_16x16x32_bf16 v[122:125], v[168:171], v[184:187], v[122:125]
	v_mfma_f32_16x16x32_bf16 v[114:117], v[176:179], v[184:187], v[114:117]
	v_mfma_f32_16x16x32_bf16 v[102:105], v[168:171], v[192:195], v[102:105]
	v_mfma_f32_16x16x32_bf16 v[98:101], v[176:179], v[192:195], v[98:101]
	v_mfma_f32_16x16x32_bf16 v[86:89], v[168:171], v[200:203], v[86:89]
	v_mfma_f32_16x16x32_bf16 v[82:85], v[176:179], v[200:203], v[82:85]
	v_mfma_f32_16x16x32_bf16 v[70:73], v[168:171], v[216:219], v[70:73]
	v_mfma_f32_16x16x32_bf16 v[66:69], v[176:179], v[216:219], v[66:69]
	v_mfma_f32_16x16x32_bf16 v[122:125], v[172:175], v[188:191], v[122:125]
	v_mfma_f32_16x16x32_bf16 v[114:117], v[180:183], v[188:191], v[114:117]
	v_mfma_f32_16x16x32_bf16 v[102:105], v[172:175], v[196:199], v[102:105]
	v_mfma_f32_16x16x32_bf16 v[98:101], v[180:183], v[196:199], v[98:101]
	v_mfma_f32_16x16x32_bf16 v[86:89], v[172:175], v[204:207], v[86:89]
	v_mfma_f32_16x16x32_bf16 v[82:85], v[180:183], v[204:207], v[82:85]
	v_mfma_f32_16x16x32_bf16 v[70:73], v[172:175], v[220:223], v[70:73]
	v_mfma_f32_16x16x32_bf16 v[66:69], v[180:183], v[220:223], v[66:69]
	s_setprio 0
	s_barrier
	s_add_i32 s64, s65, s71
	v_lshl_add_u64 v[164:165], s[44:45], 0, v[126:127]
	s_mov_b32 m0, s64
	ds_read_b128 v[184:187], v147 offset:16384
	ds_read_b128 v[188:191], v147 offset:17408
	ds_read_b128 v[192:195], v147 offset:18432
	ds_read_b128 v[196:199], v147 offset:19456
	ds_read_b128 v[200:203], v147 offset:20480
	ds_read_b128 v[204:207], v147 offset:21504
	ds_read_b128 v[216:219], v147 offset:22528
	ds_read_b128 v[220:223], v147 offset:23552
	global_load_lds_dwordx4 v[164:165], off
	s_add_i32 m0, s64, 0x2000
	s_add_u32 s92, s44, 0x100000
	v_lshl_add_u64 v[208:209], s[44:45], 0, v[118:119]
	s_addc_u32 s93, s45, 0
	s_add_i32 s50, s50, s71
	global_load_lds_dwordx4 v[208:209], off
	v_lshl_add_u64 v[224:225], s[92:93], 0, v[126:127]
	s_mov_b32 m0, s50
	v_lshl_add_u64 v[242:243], s[46:47], 0, v[120:121]
	global_load_lds_dwordx4 v[224:225], off
	v_lshl_add_u64 v[224:225], s[92:93], 0, v[118:119]
	s_add_i32 m0, s50, 0x2000
	s_nop 0
	global_load_lds_dwordx4 v[224:225], off
	v_lshl_add_u64 v[224:225], s[46:47], 0, v[128:129]
	s_mov_b32 m0, s4
	s_nop 0
	global_load_lds_dwordx4 v[224:225], off
	s_mov_b32 m0, s33
	s_nop 0
	global_load_lds_dwordx4 v[242:243], off
	s_waitcnt vmcnt(8)
	s_waitcnt lgkmcnt(0)
	s_barrier
	s_setprio 1
	s_waitcnt lgkmcnt(0)
	v_mfma_f32_16x16x32_bf16 v[62:65], v[148:151], v[184:187], v[62:65]
	v_mfma_f32_16x16x32_bf16 v[58:61], v[156:159], v[184:187], v[58:61]
	v_mfma_f32_16x16x32_bf16 v[46:49], v[148:151], v[192:195], v[46:49]
	v_mfma_f32_16x16x32_bf16 v[42:45], v[156:159], v[192:195], v[42:45]
	v_mfma_f32_16x16x32_bf16 v[30:33], v[148:151], v[200:203], v[30:33]
	v_mfma_f32_16x16x32_bf16 v[26:29], v[156:159], v[200:203], v[26:29]
	v_mfma_f32_16x16x32_bf16 v[14:17], v[148:151], v[216:219], v[14:17]
	v_mfma_f32_16x16x32_bf16 v[10:13], v[156:159], v[216:219], v[10:13]
	v_mfma_f32_16x16x32_bf16 v[62:65], v[152:155], v[188:191], v[62:65]
	v_mfma_f32_16x16x32_bf16 v[58:61], v[160:163], v[188:191], v[58:61]
	v_mfma_f32_16x16x32_bf16 v[46:49], v[152:155], v[196:199], v[46:49]
	v_mfma_f32_16x16x32_bf16 v[42:45], v[160:163], v[196:199], v[42:45]
	v_mfma_f32_16x16x32_bf16 v[30:33], v[152:155], v[204:207], v[30:33]
	v_mfma_f32_16x16x32_bf16 v[26:29], v[160:163], v[204:207], v[26:29]
	v_mfma_f32_16x16x32_bf16 v[14:17], v[152:155], v[220:223], v[14:17]
	v_mfma_f32_16x16x32_bf16 v[10:13], v[160:163], v[220:223], v[10:13]
	v_mfma_f32_16x16x32_bf16 v[54:57], v[168:171], v[184:187], v[54:57]
	v_mfma_f32_16x16x32_bf16 v[50:53], v[176:179], v[184:187], v[50:53]
	v_mfma_f32_16x16x32_bf16 v[38:41], v[168:171], v[192:195], v[38:41]
	v_mfma_f32_16x16x32_bf16 v[34:37], v[176:179], v[192:195], v[34:37]
	v_mfma_f32_16x16x32_bf16 v[22:25], v[168:171], v[200:203], v[22:25]
	v_mfma_f32_16x16x32_bf16 v[18:21], v[176:179], v[200:203], v[18:21]
	v_mfma_f32_16x16x32_bf16 v[6:9], v[168:171], v[216:219], v[6:9]
	v_mfma_f32_16x16x32_bf16 v[2:5], v[176:179], v[216:219], v[2:5]
	v_mfma_f32_16x16x32_bf16 v[54:57], v[172:175], v[188:191], v[54:57]
	v_mfma_f32_16x16x32_bf16 v[50:53], v[180:183], v[188:191], v[50:53]
	v_mfma_f32_16x16x32_bf16 v[38:41], v[172:175], v[196:199], v[38:41]
	v_mfma_f32_16x16x32_bf16 v[34:37], v[180:183], v[196:199], v[34:37]
	v_mfma_f32_16x16x32_bf16 v[22:25], v[172:175], v[204:207], v[22:25]
	v_mfma_f32_16x16x32_bf16 v[18:21], v[180:183], v[204:207], v[18:21]
	v_mfma_f32_16x16x32_bf16 v[6:9], v[172:175], v[220:223], v[6:9]
	v_mfma_f32_16x16x32_bf16 v[2:5], v[180:183], v[220:223], v[2:5]
	s_setprio 0
	s_barrier
	s_add_i32 s50, 0, 0x18000
	s_add_i32 s64, 0, 0x1c000
	v_add_u32_e32 v160, s50, v146
	v_add_u32_e32 v167, s64, v146
	ds_read_b128 v[148:151], v160
	ds_read_b128 v[152:155], v160 offset:1024
	ds_read_b128 v[156:159], v160 offset:2048
	ds_read_b128 v[160:163], v160 offset:3072
	ds_read_b128 v[168:171], v167
	ds_read_b128 v[172:175], v167 offset:1024
	ds_read_b128 v[176:179], v167 offset:2048
	ds_read_b128 v[180:183], v167 offset:3072
	s_add_u32 s46, s46, 0x100000
	s_addc_u32 s47, s47, 0
	s_mov_b32 m0, s76
	v_lshl_add_u64 v[244:245], s[46:47], 0, v[128:129]
	ds_read_b128 v[184:187], v147 offset:32768
	ds_read_b128 v[188:191], v147 offset:33792
	ds_read_b128 v[192:195], v147 offset:34816
	ds_read_b128 v[196:199], v147 offset:35840
	ds_read_b128 v[200:203], v147 offset:36864
	ds_read_b128 v[204:207], v147 offset:37888
	ds_read_b128 v[216:219], v147 offset:38912
	ds_read_b128 v[220:223], v147 offset:39936
	global_load_lds_dwordx4 v[244:245], off
	v_lshl_add_u64 v[244:245], s[46:47], 0, v[120:121]
	s_mov_b32 m0, s77
	s_nop 0
	global_load_lds_dwordx4 v[244:245], off
	s_waitcnt vmcnt(8)
	s_waitcnt lgkmcnt(0)
	s_barrier
	s_setprio 1
	s_waitcnt lgkmcnt(0)
	v_mfma_f32_16x16x32_bf16 v[134:137], v[148:151], v[184:187], v[134:137]
	v_mfma_f32_16x16x32_bf16 v[130:133], v[156:159], v[184:187], v[130:133]
	v_mfma_f32_16x16x32_bf16 v[110:113], v[148:151], v[192:195], v[110:113]
	v_mfma_f32_16x16x32_bf16 v[106:109], v[156:159], v[192:195], v[106:109]
	v_mfma_f32_16x16x32_bf16 v[94:97], v[148:151], v[200:203], v[94:97]
	v_mfma_f32_16x16x32_bf16 v[90:93], v[156:159], v[200:203], v[90:93]
	v_mfma_f32_16x16x32_bf16 v[78:81], v[148:151], v[216:219], v[78:81]
	v_mfma_f32_16x16x32_bf16 v[74:77], v[156:159], v[216:219], v[74:77]
	v_mfma_f32_16x16x32_bf16 v[134:137], v[152:155], v[188:191], v[134:137]
	v_mfma_f32_16x16x32_bf16 v[130:133], v[160:163], v[188:191], v[130:133]
	v_mfma_f32_16x16x32_bf16 v[110:113], v[152:155], v[196:199], v[110:113]
	v_mfma_f32_16x16x32_bf16 v[106:109], v[160:163], v[196:199], v[106:109]
	v_mfma_f32_16x16x32_bf16 v[94:97], v[152:155], v[204:207], v[94:97]
	v_mfma_f32_16x16x32_bf16 v[90:93], v[160:163], v[204:207], v[90:93]
	v_mfma_f32_16x16x32_bf16 v[78:81], v[152:155], v[220:223], v[78:81]
	v_mfma_f32_16x16x32_bf16 v[74:77], v[160:163], v[220:223], v[74:77]
	v_mfma_f32_16x16x32_bf16 v[122:125], v[168:171], v[184:187], v[122:125]
	v_mfma_f32_16x16x32_bf16 v[114:117], v[176:179], v[184:187], v[114:117]
	v_mfma_f32_16x16x32_bf16 v[102:105], v[168:171], v[192:195], v[102:105]
	v_mfma_f32_16x16x32_bf16 v[98:101], v[176:179], v[192:195], v[98:101]
	v_mfma_f32_16x16x32_bf16 v[86:89], v[168:171], v[200:203], v[86:89]
	v_mfma_f32_16x16x32_bf16 v[82:85], v[176:179], v[200:203], v[82:85]
	v_mfma_f32_16x16x32_bf16 v[70:73], v[168:171], v[216:219], v[70:73]
	v_mfma_f32_16x16x32_bf16 v[66:69], v[176:179], v[216:219], v[66:69]
	v_mfma_f32_16x16x32_bf16 v[122:125], v[172:175], v[188:191], v[122:125]
	v_mfma_f32_16x16x32_bf16 v[114:117], v[180:183], v[188:191], v[114:117]
	v_mfma_f32_16x16x32_bf16 v[102:105], v[172:175], v[196:199], v[102:105]
	v_mfma_f32_16x16x32_bf16 v[98:101], v[180:183], v[196:199], v[98:101]
	v_mfma_f32_16x16x32_bf16 v[86:89], v[172:175], v[204:207], v[86:89]
	v_mfma_f32_16x16x32_bf16 v[82:85], v[180:183], v[204:207], v[82:85]
	v_mfma_f32_16x16x32_bf16 v[70:73], v[172:175], v[220:223], v[70:73]
	v_mfma_f32_16x16x32_bf16 v[66:69], v[180:183], v[220:223], v[66:69]
	s_setprio 0
	s_barrier
	s_add_i32 s46, s50, s71
	v_lshl_add_u64 v[164:165], v[164:165], 0, s[56:57]
	s_mov_b32 m0, s46
	ds_read_b128 v[184:187], v147 offset:49152
	ds_read_b128 v[188:191], v147 offset:50176
	ds_read_b128 v[192:195], v147 offset:51200
	ds_read_b128 v[196:199], v147 offset:52224
	ds_read_b128 v[200:203], v147 offset:53248
	ds_read_b128 v[204:207], v147 offset:54272
	ds_read_b128 v[216:219], v147 offset:55296
	ds_read_b128 v[220:223], v147 offset:56320
	global_load_lds_dwordx4 v[164:165], off
	s_add_i32 m0, s46, 0x2000
	s_add_u32 s44, s44, 0x100080
	v_lshl_add_u64 v[164:165], v[208:209], 0, s[56:57]
	s_addc_u32 s45, s45, 0
	s_add_i32 s46, s64, s71
	global_load_lds_dwordx4 v[164:165], off
	v_lshl_add_u64 v[164:165], s[44:45], 0, v[126:127]
	s_mov_b32 m0, s46
	s_nop 0
	global_load_lds_dwordx4 v[164:165], off
	v_lshl_add_u64 v[164:165], s[44:45], 0, v[118:119]
	s_add_i32 m0, s46, 0x2000
	s_nop 0
	global_load_lds_dwordx4 v[164:165], off
	v_lshl_add_u64 v[164:165], v[224:225], 0, s[56:57]
	s_mov_b32 m0, s78
	s_nop 0
	global_load_lds_dwordx4 v[164:165], off
	v_lshl_add_u64 v[164:165], v[242:243], 0, s[56:57]
	s_mov_b32 m0, s79
	s_nop 0
	global_load_lds_dwordx4 v[164:165], off
	s_waitcnt vmcnt(8)
	s_waitcnt lgkmcnt(0)
	s_barrier
	s_setprio 1
	s_waitcnt lgkmcnt(0)
	v_mfma_f32_16x16x32_bf16 v[62:65], v[148:151], v[184:187], v[62:65]
	v_mfma_f32_16x16x32_bf16 v[58:61], v[156:159], v[184:187], v[58:61]
	v_mfma_f32_16x16x32_bf16 v[46:49], v[148:151], v[192:195], v[46:49]
	v_mfma_f32_16x16x32_bf16 v[42:45], v[156:159], v[192:195], v[42:45]
	v_mfma_f32_16x16x32_bf16 v[30:33], v[148:151], v[200:203], v[30:33]
	v_mfma_f32_16x16x32_bf16 v[26:29], v[156:159], v[200:203], v[26:29]
	v_mfma_f32_16x16x32_bf16 v[14:17], v[148:151], v[216:219], v[14:17]
	v_mfma_f32_16x16x32_bf16 v[10:13], v[156:159], v[216:219], v[10:13]
	v_mfma_f32_16x16x32_bf16 v[62:65], v[152:155], v[188:191], v[62:65]
	v_mfma_f32_16x16x32_bf16 v[58:61], v[160:163], v[188:191], v[58:61]
	v_mfma_f32_16x16x32_bf16 v[46:49], v[152:155], v[196:199], v[46:49]
	v_mfma_f32_16x16x32_bf16 v[42:45], v[160:163], v[196:199], v[42:45]
	v_mfma_f32_16x16x32_bf16 v[30:33], v[152:155], v[204:207], v[30:33]
	v_mfma_f32_16x16x32_bf16 v[26:29], v[160:163], v[204:207], v[26:29]
	v_mfma_f32_16x16x32_bf16 v[14:17], v[152:155], v[220:223], v[14:17]
	v_mfma_f32_16x16x32_bf16 v[10:13], v[160:163], v[220:223], v[10:13]
	v_mfma_f32_16x16x32_bf16 v[54:57], v[168:171], v[184:187], v[54:57]
	v_mfma_f32_16x16x32_bf16 v[50:53], v[176:179], v[184:187], v[50:53]
	v_mfma_f32_16x16x32_bf16 v[38:41], v[168:171], v[192:195], v[38:41]
	v_mfma_f32_16x16x32_bf16 v[34:37], v[176:179], v[192:195], v[34:37]
	v_mfma_f32_16x16x32_bf16 v[22:25], v[168:171], v[200:203], v[22:25]
	v_mfma_f32_16x16x32_bf16 v[18:21], v[176:179], v[200:203], v[18:21]
	v_mfma_f32_16x16x32_bf16 v[6:9], v[168:171], v[216:219], v[6:9]
	v_mfma_f32_16x16x32_bf16 v[2:5], v[176:179], v[216:219], v[2:5]
	v_mfma_f32_16x16x32_bf16 v[54:57], v[172:175], v[188:191], v[54:57]
	v_mfma_f32_16x16x32_bf16 v[50:53], v[180:183], v[188:191], v[50:53]
	v_mfma_f32_16x16x32_bf16 v[38:41], v[172:175], v[196:199], v[38:41]
	v_mfma_f32_16x16x32_bf16 v[34:37], v[180:183], v[196:199], v[34:37]
	v_mfma_f32_16x16x32_bf16 v[22:25], v[172:175], v[204:207], v[22:25]
	v_mfma_f32_16x16x32_bf16 v[18:21], v[180:183], v[204:207], v[18:21]
	v_mfma_f32_16x16x32_bf16 v[6:9], v[172:175], v[220:223], v[6:9]
	v_mfma_f32_16x16x32_bf16 v[2:5], v[180:183], v[220:223], v[2:5]
	s_setprio 0
	s_barrier
	s_add_i32 s84, s84, 2
	s_add_u32 s36, s36, 0x100
	s_addc_u32 s37, s37, 0
	s_cmp_gt_u32 s84, 61
	s_cbranch_scc0 .LBB0_2796
	s_add_u32 s36, s59, 0xffffff00
	s_addc_u32 s37, s81, -1
	s_andn2_b64 vcc, exec, s[42:43]
	s_cbranch_vccnz .LBB0_2799
	v_mov_b32_e32 v2, 0
	s_mov_b32 s12, s26
	s_mov_b32 s80, s28
	s_mov_b64 s[24:25], s[34:35]
	s_mov_b32 s68, s58
	v_mov_b32_e32 v3, v2
	v_mov_b32_e32 v4, v2
	v_mov_b32_e32 v5, v2
	v_mov_b32_e32 v6, v2
	v_mov_b32_e32 v7, v2
	v_mov_b32_e32 v8, v2
	v_mov_b32_e32 v9, v2
	v_mov_b32_e32 v18, v2
	v_mov_b32_e32 v19, v2
	v_mov_b32_e32 v20, v2
	v_mov_b32_e32 v21, v2
	v_mov_b32_e32 v22, v2
	v_mov_b32_e32 v23, v2
	v_mov_b32_e32 v24, v2
	v_mov_b32_e32 v25, v2
	v_mov_b32_e32 v34, v2
	v_mov_b32_e32 v35, v2
	v_mov_b32_e32 v36, v2
	v_mov_b32_e32 v37, v2
	v_mov_b32_e32 v38, v2
	v_mov_b32_e32 v39, v2
	v_mov_b32_e32 v40, v2
	v_mov_b32_e32 v41, v2
	v_mov_b32_e32 v50, v2
	v_mov_b32_e32 v51, v2
	v_mov_b32_e32 v52, v2
	v_mov_b32_e32 v53, v2
	v_mov_b32_e32 v54, v2
	v_mov_b32_e32 v55, v2
	v_mov_b32_e32 v56, v2
	v_mov_b32_e32 v57, v2
	v_mov_b32_e32 v10, v2
	v_mov_b32_e32 v11, v2
	v_mov_b32_e32 v12, v2
	v_mov_b32_e32 v13, v2
	v_mov_b32_e32 v14, v2
	v_mov_b32_e32 v15, v2
	v_mov_b32_e32 v16, v2
	v_mov_b32_e32 v17, v2
	v_mov_b32_e32 v26, v2
	v_mov_b32_e32 v27, v2
	v_mov_b32_e32 v28, v2
	v_mov_b32_e32 v29, v2
	v_mov_b32_e32 v30, v2
	v_mov_b32_e32 v31, v2
	v_mov_b32_e32 v32, v2
	v_mov_b32_e32 v33, v2
	v_mov_b32_e32 v42, v2
	v_mov_b32_e32 v43, v2
	v_mov_b32_e32 v44, v2
	v_mov_b32_e32 v45, v2
	v_mov_b32_e32 v46, v2
	v_mov_b32_e32 v47, v2
	v_mov_b32_e32 v48, v2
	v_mov_b32_e32 v49, v2
	v_mov_b32_e32 v58, v2
	v_mov_b32_e32 v59, v2
	v_mov_b32_e32 v60, v2
	v_mov_b32_e32 v61, v2
	v_mov_b32_e32 v62, v2
	v_mov_b32_e32 v63, v2
	v_mov_b32_e32 v64, v2
	v_mov_b32_e32 v65, v2
	v_mov_b32_e32 v66, v2
	v_mov_b32_e32 v67, v2
	v_mov_b32_e32 v68, v2
	v_mov_b32_e32 v69, v2
	v_mov_b32_e32 v70, v2
	v_mov_b32_e32 v71, v2
	v_mov_b32_e32 v72, v2
	v_mov_b32_e32 v73, v2
	v_mov_b32_e32 v82, v2
	v_mov_b32_e32 v83, v2
	v_mov_b32_e32 v84, v2
	v_mov_b32_e32 v85, v2
	v_mov_b32_e32 v86, v2
	v_mov_b32_e32 v87, v2
	v_mov_b32_e32 v88, v2
	v_mov_b32_e32 v89, v2
	v_mov_b32_e32 v98, v2
	v_mov_b32_e32 v99, v2
	v_mov_b32_e32 v100, v2
	v_mov_b32_e32 v101, v2
	v_mov_b32_e32 v102, v2
	v_mov_b32_e32 v103, v2
	v_mov_b32_e32 v104, v2
	v_mov_b32_e32 v105, v2
	v_mov_b32_e32 v114, v2
	v_mov_b32_e32 v115, v2
	v_mov_b32_e32 v116, v2
	v_mov_b32_e32 v117, v2
	v_mov_b32_e32 v122, v2
	v_mov_b32_e32 v123, v2
	v_mov_b32_e32 v124, v2
	v_mov_b32_e32 v125, v2
	v_mov_b32_e32 v74, v2
	v_mov_b32_e32 v75, v2
	v_mov_b32_e32 v76, v2
	v_mov_b32_e32 v77, v2
	v_mov_b32_e32 v78, v2
	v_mov_b32_e32 v79, v2
	v_mov_b32_e32 v80, v2
	v_mov_b32_e32 v81, v2
	v_mov_b32_e32 v90, v2
	v_mov_b32_e32 v91, v2
	v_mov_b32_e32 v92, v2
	v_mov_b32_e32 v93, v2
	v_mov_b32_e32 v94, v2
	v_mov_b32_e32 v95, v2
	v_mov_b32_e32 v96, v2
	v_mov_b32_e32 v97, v2
	v_mov_b32_e32 v106, v2
	v_mov_b32_e32 v107, v2
	v_mov_b32_e32 v108, v2
	v_mov_b32_e32 v109, v2
	v_mov_b32_e32 v110, v2
	v_mov_b32_e32 v111, v2
	v_mov_b32_e32 v112, v2
	v_mov_b32_e32 v113, v2
	v_mov_b32_e32 v130, v2
	v_mov_b32_e32 v131, v2
	v_mov_b32_e32 v132, v2
	v_mov_b32_e32 v133, v2
	v_mov_b32_e32 v134, v2
	v_mov_b32_e32 v135, v2
	v_mov_b32_e32 v136, v2
	v_mov_b32_e32 v137, v2
	s_movk_i32 s92, 0x2b20
	s_andn2_b64 vcc, exec, s[40:41]
	s_cbranch_vccnz .LBB0_2800
	s_branch .LBB0_2801

.LBB0_2891:
	s_add_u32 s44, s24, s36
	s_addc_u32 s45, s25, s37
	s_add_u32 s44, s44, 0x100
	s_addc_u32 s45, s45, 0
	s_add_u32 s50, s59, s36
	s_addc_u32 s64, s81, s37
	s_add_i32 s65, 0, 0x10000
	s_cmpk_eq_i32 s36, 0x1f00
	s_cselect_b32 s47, s29, s45
	s_cselect_b32 s46, s82, s44
	s_cselect_b32 s45, s27, s64
	s_cselect_b32 s44, s83, s50
	s_add_i32 s50, 0, 0x14000
	v_add_u32_e32 v160, s65, v146
	v_add_u32_e32 v164, s50, v146
	ds_read_b128 v[148:151], v160
	ds_read_b128 v[152:155], v160 offset:1024
	ds_read_b128 v[156:159], v160 offset:2048
	ds_read_b128 v[160:163], v160 offset:3072
	ds_read_b128 v[168:171], v164
	ds_read_b128 v[172:175], v164 offset:1024
	ds_read_b128 v[176:179], v164 offset:2048
	ds_read_b128 v[180:183], v164 offset:3072
	v_lshl_add_u64 v[164:165], v[144:145], 0, s[36:37]
	s_add_i32 m0, s4, 0xc000
	ds_read_b128 v[184:187], v147
	ds_read_b128 v[188:191], v147 offset:1024
	ds_read_b128 v[192:195], v147 offset:2048
	ds_read_b128 v[196:199], v147 offset:3072
	ds_read_b128 v[200:203], v147 offset:4096
	ds_read_b128 v[204:207], v147 offset:5120
	ds_read_b128 v[216:219], v147 offset:6144
	ds_read_b128 v[220:223], v147 offset:7168
	global_load_lds_dwordx4 v[164:165], off
	v_lshl_add_u64 v[164:165], v[142:143], 0, s[36:37]
	s_add_i32 m0, s4, 0xe000
	s_nop 0
	global_load_lds_dwordx4 v[164:165], off
	s_waitcnt vmcnt(8)
	s_waitcnt lgkmcnt(0)
	s_barrier
	s_setprio 1
	s_waitcnt lgkmcnt(0)
	v_mfma_f32_16x16x32_bf16 v[134:137], v[148:151], v[184:187], v[134:137]
	v_mfma_f32_16x16x32_bf16 v[130:133], v[156:159], v[184:187], v[130:133]
	v_mfma_f32_16x16x32_bf16 v[110:113], v[148:151], v[192:195], v[110:113]
	v_mfma_f32_16x16x32_bf16 v[106:109], v[156:159], v[192:195], v[106:109]
	v_mfma_f32_16x16x32_bf16 v[94:97], v[148:151], v[200:203], v[94:97]
	v_mfma_f32_16x16x32_bf16 v[90:93], v[156:159], v[200:203], v[90:93]
	v_mfma_f32_16x16x32_bf16 v[78:81], v[148:151], v[216:219], v[78:81]
	v_mfma_f32_16x16x32_bf16 v[74:77], v[156:159], v[216:219], v[74:77]
	v_mfma_f32_16x16x32_bf16 v[134:137], v[152:155], v[188:191], v[134:137]
	v_mfma_f32_16x16x32_bf16 v[130:133], v[160:163], v[188:191], v[130:133]
	v_mfma_f32_16x16x32_bf16 v[110:113], v[152:155], v[196:199], v[110:113]
	v_mfma_f32_16x16x32_bf16 v[106:109], v[160:163], v[196:199], v[106:109]
	v_mfma_f32_16x16x32_bf16 v[94:97], v[152:155], v[204:207], v[94:97]
	v_mfma_f32_16x16x32_bf16 v[90:93], v[160:163], v[204:207], v[90:93]
	v_mfma_f32_16x16x32_bf16 v[78:81], v[152:155], v[220:223], v[78:81]
	v_mfma_f32_16x16x32_bf16 v[74:77], v[160:163], v[220:223], v[74:77]
	v_mfma_f32_16x16x32_bf16 v[118:121], v[168:171], v[184:187], v[118:121]
	v_mfma_f32_16x16x32_bf16 v[114:117], v[176:179], v[184:187], v[114:117]
	v_mfma_f32_16x16x32_bf16 v[102:105], v[168:171], v[192:195], v[102:105]
	v_mfma_f32_16x16x32_bf16 v[98:101], v[176:179], v[192:195], v[98:101]
	v_mfma_f32_16x16x32_bf16 v[86:89], v[168:171], v[200:203], v[86:89]
	v_mfma_f32_16x16x32_bf16 v[82:85], v[176:179], v[200:203], v[82:85]
	v_mfma_f32_16x16x32_bf16 v[70:73], v[168:171], v[216:219], v[70:73]
	v_mfma_f32_16x16x32_bf16 v[66:69], v[176:179], v[216:219], v[66:69]
	v_mfma_f32_16x16x32_bf16 v[118:121], v[172:175], v[188:191], v[118:121]
	v_mfma_f32_16x16x32_bf16 v[114:117], v[180:183], v[188:191], v[114:117]
	v_mfma_f32_16x16x32_bf16 v[102:105], v[172:175], v[196:199], v[102:105]
	v_mfma_f32_16x16x32_bf16 v[98:101], v[180:183], v[196:199], v[98:101]
	v_mfma_f32_16x16x32_bf16 v[86:89], v[172:175], v[204:207], v[86:89]
	v_mfma_f32_16x16x32_bf16 v[82:85], v[180:183], v[204:207], v[82:85]
	v_mfma_f32_16x16x32_bf16 v[70:73], v[172:175], v[220:223], v[70:73]
	v_mfma_f32_16x16x32_bf16 v[66:69], v[180:183], v[220:223], v[66:69]
	s_setprio 0
	s_barrier
	s_add_i32 s64, s65, s76
	v_lshl_add_u64 v[164:165], s[44:45], 0, v[126:127]
	s_mov_b32 m0, s64
	ds_read_b128 v[184:187], v147 offset:16384
	ds_read_b128 v[188:191], v147 offset:17408
	ds_read_b128 v[192:195], v147 offset:18432
	ds_read_b128 v[196:199], v147 offset:19456
	ds_read_b128 v[200:203], v147 offset:20480
	ds_read_b128 v[204:207], v147 offset:21504
	ds_read_b128 v[216:219], v147 offset:22528
	ds_read_b128 v[220:223], v147 offset:23552
	global_load_lds_dwordx4 v[164:165], off
	s_add_i32 m0, s64, 0x2000
	s_add_u32 s92, s44, 0x100000
	v_lshl_add_u64 v[208:209], s[44:45], 0, v[122:123]
	s_addc_u32 s93, s45, 0
	s_add_i32 s50, s50, s76
	global_load_lds_dwordx4 v[208:209], off
	v_lshl_add_u64 v[240:241], s[92:93], 0, v[126:127]
	s_mov_b32 m0, s50
	v_lshl_add_u64 v[242:243], s[46:47], 0, v[124:125]
	global_load_lds_dwordx4 v[240:241], off
	v_lshl_add_u64 v[240:241], s[92:93], 0, v[122:123]
	s_add_i32 m0, s50, 0x2000
	s_nop 0
	global_load_lds_dwordx4 v[240:241], off
	v_lshl_add_u64 v[240:241], s[46:47], 0, v[128:129]
	s_mov_b32 m0, s4
	s_nop 0
	global_load_lds_dwordx4 v[240:241], off
	s_mov_b32 m0, s33
	s_nop 0
	global_load_lds_dwordx4 v[242:243], off
	s_waitcnt vmcnt(8)
	s_waitcnt lgkmcnt(0)
	s_barrier
	s_setprio 1
	s_waitcnt lgkmcnt(0)
	v_mfma_f32_16x16x32_bf16 v[62:65], v[148:151], v[184:187], v[62:65]
	v_mfma_f32_16x16x32_bf16 v[58:61], v[156:159], v[184:187], v[58:61]
	v_mfma_f32_16x16x32_bf16 v[46:49], v[148:151], v[192:195], v[46:49]
	v_mfma_f32_16x16x32_bf16 v[42:45], v[156:159], v[192:195], v[42:45]
	v_mfma_f32_16x16x32_bf16 v[30:33], v[148:151], v[200:203], v[30:33]
	v_mfma_f32_16x16x32_bf16 v[26:29], v[156:159], v[200:203], v[26:29]
	v_mfma_f32_16x16x32_bf16 v[14:17], v[148:151], v[216:219], v[14:17]
	v_mfma_f32_16x16x32_bf16 v[10:13], v[156:159], v[216:219], v[10:13]
	v_mfma_f32_16x16x32_bf16 v[62:65], v[152:155], v[188:191], v[62:65]
	v_mfma_f32_16x16x32_bf16 v[58:61], v[160:163], v[188:191], v[58:61]
	v_mfma_f32_16x16x32_bf16 v[46:49], v[152:155], v[196:199], v[46:49]
	v_mfma_f32_16x16x32_bf16 v[42:45], v[160:163], v[196:199], v[42:45]
	v_mfma_f32_16x16x32_bf16 v[30:33], v[152:155], v[204:207], v[30:33]
	v_mfma_f32_16x16x32_bf16 v[26:29], v[160:163], v[204:207], v[26:29]
	v_mfma_f32_16x16x32_bf16 v[14:17], v[152:155], v[220:223], v[14:17]
	v_mfma_f32_16x16x32_bf16 v[10:13], v[160:163], v[220:223], v[10:13]
	v_mfma_f32_16x16x32_bf16 v[54:57], v[168:171], v[184:187], v[54:57]
	v_mfma_f32_16x16x32_bf16 v[50:53], v[176:179], v[184:187], v[50:53]
	v_mfma_f32_16x16x32_bf16 v[38:41], v[168:171], v[192:195], v[38:41]
	v_mfma_f32_16x16x32_bf16 v[34:37], v[176:179], v[192:195], v[34:37]
	v_mfma_f32_16x16x32_bf16 v[22:25], v[168:171], v[200:203], v[22:25]
	v_mfma_f32_16x16x32_bf16 v[18:21], v[176:179], v[200:203], v[18:21]
	v_mfma_f32_16x16x32_bf16 v[6:9], v[168:171], v[216:219], v[6:9]
	v_mfma_f32_16x16x32_bf16 v[2:5], v[176:179], v[216:219], v[2:5]
	v_mfma_f32_16x16x32_bf16 v[54:57], v[172:175], v[188:191], v[54:57]
	v_mfma_f32_16x16x32_bf16 v[50:53], v[180:183], v[188:191], v[50:53]
	v_mfma_f32_16x16x32_bf16 v[38:41], v[172:175], v[196:199], v[38:41]
	v_mfma_f32_16x16x32_bf16 v[34:37], v[180:183], v[196:199], v[34:37]
	v_mfma_f32_16x16x32_bf16 v[22:25], v[172:175], v[204:207], v[22:25]
	v_mfma_f32_16x16x32_bf16 v[18:21], v[180:183], v[204:207], v[18:21]
	v_mfma_f32_16x16x32_bf16 v[6:9], v[172:175], v[220:223], v[6:9]
	v_mfma_f32_16x16x32_bf16 v[2:5], v[180:183], v[220:223], v[2:5]
	s_setprio 0
	s_barrier
	s_add_i32 s50, 0, 0x18000
	s_add_i32 s64, 0, 0x1c000
	v_add_u32_e32 v160, s50, v146
	v_add_u32_e32 v167, s64, v146
	ds_read_b128 v[148:151], v160
	ds_read_b128 v[152:155], v160 offset:1024
	ds_read_b128 v[156:159], v160 offset:2048
	ds_read_b128 v[160:163], v160 offset:3072
	ds_read_b128 v[168:171], v167
	ds_read_b128 v[172:175], v167 offset:1024
	ds_read_b128 v[176:179], v167 offset:2048
	ds_read_b128 v[180:183], v167 offset:3072
	s_add_u32 s46, s46, 0x100000
	s_addc_u32 s47, s47, 0
	s_mov_b32 m0, s77
	v_lshl_add_u64 v[244:245], s[46:47], 0, v[128:129]
	ds_read_b128 v[184:187], v147 offset:32768
	ds_read_b128 v[188:191], v147 offset:33792
	ds_read_b128 v[192:195], v147 offset:34816
	ds_read_b128 v[196:199], v147 offset:35840
	ds_read_b128 v[200:203], v147 offset:36864
	ds_read_b128 v[204:207], v147 offset:37888
	ds_read_b128 v[216:219], v147 offset:38912
	ds_read_b128 v[220:223], v147 offset:39936
	global_load_lds_dwordx4 v[244:245], off
	v_lshl_add_u64 v[244:245], s[46:47], 0, v[124:125]
	s_mov_b32 m0, s78
	s_nop 0
	global_load_lds_dwordx4 v[244:245], off
	s_waitcnt vmcnt(8)
	s_waitcnt lgkmcnt(0)
	s_barrier
	s_setprio 1
	s_waitcnt lgkmcnt(0)
	v_mfma_f32_16x16x32_bf16 v[134:137], v[148:151], v[184:187], v[134:137]
	v_mfma_f32_16x16x32_bf16 v[130:133], v[156:159], v[184:187], v[130:133]
	v_mfma_f32_16x16x32_bf16 v[110:113], v[148:151], v[192:195], v[110:113]
	v_mfma_f32_16x16x32_bf16 v[106:109], v[156:159], v[192:195], v[106:109]
	v_mfma_f32_16x16x32_bf16 v[94:97], v[148:151], v[200:203], v[94:97]
	v_mfma_f32_16x16x32_bf16 v[90:93], v[156:159], v[200:203], v[90:93]
	v_mfma_f32_16x16x32_bf16 v[78:81], v[148:151], v[216:219], v[78:81]
	v_mfma_f32_16x16x32_bf16 v[74:77], v[156:159], v[216:219], v[74:77]
	v_mfma_f32_16x16x32_bf16 v[134:137], v[152:155], v[188:191], v[134:137]
	v_mfma_f32_16x16x32_bf16 v[130:133], v[160:163], v[188:191], v[130:133]
	v_mfma_f32_16x16x32_bf16 v[110:113], v[152:155], v[196:199], v[110:113]
	v_mfma_f32_16x16x32_bf16 v[106:109], v[160:163], v[196:199], v[106:109]
	v_mfma_f32_16x16x32_bf16 v[94:97], v[152:155], v[204:207], v[94:97]
	v_mfma_f32_16x16x32_bf16 v[90:93], v[160:163], v[204:207], v[90:93]
	v_mfma_f32_16x16x32_bf16 v[78:81], v[152:155], v[220:223], v[78:81]
	v_mfma_f32_16x16x32_bf16 v[74:77], v[160:163], v[220:223], v[74:77]
	v_mfma_f32_16x16x32_bf16 v[118:121], v[168:171], v[184:187], v[118:121]
	v_mfma_f32_16x16x32_bf16 v[114:117], v[176:179], v[184:187], v[114:117]
	v_mfma_f32_16x16x32_bf16 v[102:105], v[168:171], v[192:195], v[102:105]
	v_mfma_f32_16x16x32_bf16 v[98:101], v[176:179], v[192:195], v[98:101]
	v_mfma_f32_16x16x32_bf16 v[86:89], v[168:171], v[200:203], v[86:89]
	v_mfma_f32_16x16x32_bf16 v[82:85], v[176:179], v[200:203], v[82:85]
	v_mfma_f32_16x16x32_bf16 v[70:73], v[168:171], v[216:219], v[70:73]
	v_mfma_f32_16x16x32_bf16 v[66:69], v[176:179], v[216:219], v[66:69]
	v_mfma_f32_16x16x32_bf16 v[118:121], v[172:175], v[188:191], v[118:121]
	v_mfma_f32_16x16x32_bf16 v[114:117], v[180:183], v[188:191], v[114:117]
	v_mfma_f32_16x16x32_bf16 v[102:105], v[172:175], v[196:199], v[102:105]
	v_mfma_f32_16x16x32_bf16 v[98:101], v[180:183], v[196:199], v[98:101]
	v_mfma_f32_16x16x32_bf16 v[86:89], v[172:175], v[204:207], v[86:89]
	v_mfma_f32_16x16x32_bf16 v[82:85], v[180:183], v[204:207], v[82:85]
	v_mfma_f32_16x16x32_bf16 v[70:73], v[172:175], v[220:223], v[70:73]
	v_mfma_f32_16x16x32_bf16 v[66:69], v[180:183], v[220:223], v[66:69]
	s_setprio 0
	s_barrier
	s_add_i32 s46, s50, s76
	v_lshl_add_u64 v[164:165], v[164:165], 0, s[56:57]
	s_mov_b32 m0, s46
	ds_read_b128 v[184:187], v147 offset:49152
	ds_read_b128 v[188:191], v147 offset:50176
	ds_read_b128 v[192:195], v147 offset:51200
	ds_read_b128 v[196:199], v147 offset:52224
	ds_read_b128 v[200:203], v147 offset:53248
	ds_read_b128 v[204:207], v147 offset:54272
	ds_read_b128 v[216:219], v147 offset:55296
	ds_read_b128 v[220:223], v147 offset:56320
	global_load_lds_dwordx4 v[164:165], off
	s_add_i32 m0, s46, 0x2000
	s_add_u32 s44, s44, 0x100080
	v_lshl_add_u64 v[164:165], v[208:209], 0, s[56:57]
	s_addc_u32 s45, s45, 0
	s_add_i32 s46, s64, s76
	global_load_lds_dwordx4 v[164:165], off
	v_lshl_add_u64 v[164:165], s[44:45], 0, v[126:127]
	s_mov_b32 m0, s46
	s_nop 0
	global_load_lds_dwordx4 v[164:165], off
	v_lshl_add_u64 v[164:165], s[44:45], 0, v[122:123]
	s_add_i32 m0, s46, 0x2000
	s_nop 0
	global_load_lds_dwordx4 v[164:165], off
	v_lshl_add_u64 v[164:165], v[240:241], 0, s[56:57]
	s_mov_b32 m0, s79
	s_nop 0
	global_load_lds_dwordx4 v[164:165], off
	v_lshl_add_u64 v[164:165], v[242:243], 0, s[56:57]
	s_mov_b32 m0, s80
	s_nop 0
	global_load_lds_dwordx4 v[164:165], off
	s_waitcnt vmcnt(8)
	s_waitcnt lgkmcnt(0)
	s_barrier
	s_setprio 1
	s_waitcnt lgkmcnt(0)
	v_mfma_f32_16x16x32_bf16 v[62:65], v[148:151], v[184:187], v[62:65]
	v_mfma_f32_16x16x32_bf16 v[58:61], v[156:159], v[184:187], v[58:61]
	v_mfma_f32_16x16x32_bf16 v[46:49], v[148:151], v[192:195], v[46:49]
	v_mfma_f32_16x16x32_bf16 v[42:45], v[156:159], v[192:195], v[42:45]
	v_mfma_f32_16x16x32_bf16 v[30:33], v[148:151], v[200:203], v[30:33]
	v_mfma_f32_16x16x32_bf16 v[26:29], v[156:159], v[200:203], v[26:29]
	v_mfma_f32_16x16x32_bf16 v[14:17], v[148:151], v[216:219], v[14:17]
	v_mfma_f32_16x16x32_bf16 v[10:13], v[156:159], v[216:219], v[10:13]
	v_mfma_f32_16x16x32_bf16 v[62:65], v[152:155], v[188:191], v[62:65]
	v_mfma_f32_16x16x32_bf16 v[58:61], v[160:163], v[188:191], v[58:61]
	v_mfma_f32_16x16x32_bf16 v[46:49], v[152:155], v[196:199], v[46:49]
	v_mfma_f32_16x16x32_bf16 v[42:45], v[160:163], v[196:199], v[42:45]
	v_mfma_f32_16x16x32_bf16 v[30:33], v[152:155], v[204:207], v[30:33]
	v_mfma_f32_16x16x32_bf16 v[26:29], v[160:163], v[204:207], v[26:29]
	v_mfma_f32_16x16x32_bf16 v[14:17], v[152:155], v[220:223], v[14:17]
	v_mfma_f32_16x16x32_bf16 v[10:13], v[160:163], v[220:223], v[10:13]
	v_mfma_f32_16x16x32_bf16 v[54:57], v[168:171], v[184:187], v[54:57]
	v_mfma_f32_16x16x32_bf16 v[50:53], v[176:179], v[184:187], v[50:53]
	v_mfma_f32_16x16x32_bf16 v[38:41], v[168:171], v[192:195], v[38:41]
	v_mfma_f32_16x16x32_bf16 v[34:37], v[176:179], v[192:195], v[34:37]
	v_mfma_f32_16x16x32_bf16 v[22:25], v[168:171], v[200:203], v[22:25]
	v_mfma_f32_16x16x32_bf16 v[18:21], v[176:179], v[200:203], v[18:21]
	v_mfma_f32_16x16x32_bf16 v[6:9], v[168:171], v[216:219], v[6:9]
	v_mfma_f32_16x16x32_bf16 v[2:5], v[176:179], v[216:219], v[2:5]
	v_mfma_f32_16x16x32_bf16 v[54:57], v[172:175], v[188:191], v[54:57]
	v_mfma_f32_16x16x32_bf16 v[50:53], v[180:183], v[188:191], v[50:53]
	v_mfma_f32_16x16x32_bf16 v[38:41], v[172:175], v[196:199], v[38:41]
	v_mfma_f32_16x16x32_bf16 v[34:37], v[180:183], v[196:199], v[34:37]
	v_mfma_f32_16x16x32_bf16 v[22:25], v[172:175], v[204:207], v[22:25]
	v_mfma_f32_16x16x32_bf16 v[18:21], v[180:183], v[204:207], v[18:21]
	v_mfma_f32_16x16x32_bf16 v[6:9], v[172:175], v[220:223], v[6:9]
	v_mfma_f32_16x16x32_bf16 v[2:5], v[180:183], v[220:223], v[2:5]
	s_setprio 0
	s_barrier
	s_add_i32 s84, s84, 2
	s_add_u32 s36, s36, 0x100
	s_addc_u32 s37, s37, 0
	s_cmp_gt_u32 s84, 61
	s_cbranch_scc0 .LBB0_2891
	s_add_u32 s36, s59, 0xffffff00
	s_addc_u32 s37, s81, -1
	s_andn2_b64 vcc, exec, s[42:43]
	s_cbranch_vccnz .LBB0_2894
	v_mov_b32_e32 v2, 0
	s_mov_b32 s20, s26
	s_mov_b32 s52, s28
	s_mov_b64 s[24:25], s[34:35]
	s_mov_b32 s68, s58
	v_mov_b32_e32 v3, v2
	v_mov_b32_e32 v4, v2
	v_mov_b32_e32 v5, v2
	v_mov_b32_e32 v6, v2
	v_mov_b32_e32 v7, v2
	v_mov_b32_e32 v8, v2
	v_mov_b32_e32 v9, v2
	v_mov_b32_e32 v18, v2
	v_mov_b32_e32 v19, v2
	v_mov_b32_e32 v20, v2
	v_mov_b32_e32 v21, v2
	v_mov_b32_e32 v22, v2
	v_mov_b32_e32 v23, v2
	v_mov_b32_e32 v24, v2
	v_mov_b32_e32 v25, v2
	v_mov_b32_e32 v34, v2
	v_mov_b32_e32 v35, v2
	v_mov_b32_e32 v36, v2
	v_mov_b32_e32 v37, v2
	v_mov_b32_e32 v38, v2
	v_mov_b32_e32 v39, v2
	v_mov_b32_e32 v40, v2
	v_mov_b32_e32 v41, v2
	v_mov_b32_e32 v50, v2
	v_mov_b32_e32 v51, v2
	v_mov_b32_e32 v52, v2
	v_mov_b32_e32 v53, v2
	v_mov_b32_e32 v54, v2
	v_mov_b32_e32 v55, v2
	v_mov_b32_e32 v56, v2
	v_mov_b32_e32 v57, v2
	v_mov_b32_e32 v10, v2
	v_mov_b32_e32 v11, v2
	v_mov_b32_e32 v12, v2
	v_mov_b32_e32 v13, v2
	v_mov_b32_e32 v14, v2
	v_mov_b32_e32 v15, v2
	v_mov_b32_e32 v16, v2
	v_mov_b32_e32 v17, v2
	v_mov_b32_e32 v26, v2
	v_mov_b32_e32 v27, v2
	v_mov_b32_e32 v28, v2
	v_mov_b32_e32 v29, v2
	v_mov_b32_e32 v30, v2
	v_mov_b32_e32 v31, v2
	v_mov_b32_e32 v32, v2
	v_mov_b32_e32 v33, v2
	v_mov_b32_e32 v42, v2
	v_mov_b32_e32 v43, v2
	v_mov_b32_e32 v44, v2
	v_mov_b32_e32 v45, v2
	v_mov_b32_e32 v46, v2
	v_mov_b32_e32 v47, v2
	v_mov_b32_e32 v48, v2
	v_mov_b32_e32 v49, v2
	v_mov_b32_e32 v58, v2
	v_mov_b32_e32 v59, v2
	v_mov_b32_e32 v60, v2
	v_mov_b32_e32 v61, v2
	v_mov_b32_e32 v62, v2
	v_mov_b32_e32 v63, v2
	v_mov_b32_e32 v64, v2
	v_mov_b32_e32 v65, v2
	v_mov_b32_e32 v66, v2
	v_mov_b32_e32 v67, v2
	v_mov_b32_e32 v68, v2
	v_mov_b32_e32 v69, v2
	v_mov_b32_e32 v70, v2
	v_mov_b32_e32 v71, v2
	v_mov_b32_e32 v72, v2
	v_mov_b32_e32 v73, v2
	v_mov_b32_e32 v82, v2
	v_mov_b32_e32 v83, v2
	v_mov_b32_e32 v84, v2
	v_mov_b32_e32 v85, v2
	v_mov_b32_e32 v86, v2
	v_mov_b32_e32 v87, v2
	v_mov_b32_e32 v88, v2
	v_mov_b32_e32 v89, v2
	v_mov_b32_e32 v98, v2
	v_mov_b32_e32 v99, v2
	v_mov_b32_e32 v100, v2
	v_mov_b32_e32 v101, v2
	v_mov_b32_e32 v102, v2
	v_mov_b32_e32 v103, v2
	v_mov_b32_e32 v104, v2
	v_mov_b32_e32 v105, v2
	v_mov_b32_e32 v114, v2
	v_mov_b32_e32 v115, v2
	v_mov_b32_e32 v116, v2
	v_mov_b32_e32 v117, v2
	v_mov_b32_e32 v118, v2
	v_mov_b32_e32 v119, v2
	v_mov_b32_e32 v120, v2
	v_mov_b32_e32 v121, v2
	v_mov_b32_e32 v74, v2
	v_mov_b32_e32 v75, v2
	v_mov_b32_e32 v76, v2
	v_mov_b32_e32 v77, v2
	v_mov_b32_e32 v78, v2
	v_mov_b32_e32 v79, v2
	v_mov_b32_e32 v80, v2
	v_mov_b32_e32 v81, v2
	v_mov_b32_e32 v90, v2
	v_mov_b32_e32 v91, v2
	v_mov_b32_e32 v92, v2
	v_mov_b32_e32 v93, v2
	v_mov_b32_e32 v94, v2
	v_mov_b32_e32 v95, v2
	v_mov_b32_e32 v96, v2
	v_mov_b32_e32 v97, v2
	v_mov_b32_e32 v106, v2
	v_mov_b32_e32 v107, v2
	v_mov_b32_e32 v108, v2
	v_mov_b32_e32 v109, v2
	v_mov_b32_e32 v110, v2
	v_mov_b32_e32 v111, v2
	v_mov_b32_e32 v112, v2
	v_mov_b32_e32 v113, v2
	v_mov_b32_e32 v130, v2
	v_mov_b32_e32 v131, v2
	v_mov_b32_e32 v132, v2
	v_mov_b32_e32 v133, v2
	v_mov_b32_e32 v134, v2
	v_mov_b32_e32 v135, v2
	v_mov_b32_e32 v136, v2
	v_mov_b32_e32 v137, v2
	s_movk_i32 s92, 0x2b20
	s_andn2_b64 vcc, exec, s[40:41]
	s_cbranch_vccnz .LBB0_2895
	s_branch .LBB0_2896

.LBB0_2982:
	s_add_u32 s42, s24, s36
	s_addc_u32 s43, s25, s37
	s_add_u32 s42, s42, 0x100
	s_addc_u32 s43, s43, 0
	s_add_u32 s50, s59, s36
	s_addc_u32 s64, s79, s37
	s_add_i32 s65, 0, 0x10000
	s_cmpk_eq_i32 s36, 0x1f00
	s_cselect_b32 s45, s29, s43
	s_cselect_b32 s44, s80, s42
	s_cselect_b32 s43, s27, s64
	s_cselect_b32 s42, s81, s50
	s_add_i32 s50, 0, 0x14000
	v_add_u32_e32 v160, s65, v146
	v_add_u32_e32 v176, s50, v146
	ds_read_b128 v[148:151], v160
	ds_read_b128 v[152:155], v160 offset:1024
	ds_read_b128 v[156:159], v160 offset:2048
	ds_read_b128 v[160:163], v160 offset:3072
	ds_read_b128 v[164:167], v176
	ds_read_b128 v[168:171], v176 offset:1024
	ds_read_b128 v[172:175], v176 offset:2048
	ds_read_b128 v[176:179], v176 offset:3072
	v_lshl_add_u64 v[208:209], v[144:145], 0, s[36:37]
	s_add_i32 m0, s4, 0xc000
	ds_read_b128 v[180:183], v147
	ds_read_b128 v[184:187], v147 offset:1024
	ds_read_b128 v[188:191], v147 offset:2048
	ds_read_b128 v[192:195], v147 offset:3072
	ds_read_b128 v[196:199], v147 offset:4096
	ds_read_b128 v[200:203], v147 offset:5120
	ds_read_b128 v[204:207], v147 offset:6144
	ds_read_b128 v[216:219], v147 offset:7168
	global_load_lds_dwordx4 v[208:209], off
	v_lshl_add_u64 v[208:209], v[142:143], 0, s[36:37]
	s_add_i32 m0, s4, 0xe000
	s_nop 0
	global_load_lds_dwordx4 v[208:209], off
	s_waitcnt vmcnt(8)
	s_waitcnt lgkmcnt(0)
	s_barrier
	s_setprio 1
	s_waitcnt lgkmcnt(0)
	v_mfma_f32_16x16x32_bf16 v[134:137], v[148:151], v[180:183], v[134:137]
	v_mfma_f32_16x16x32_bf16 v[130:133], v[156:159], v[180:183], v[130:133]
	v_mfma_f32_16x16x32_bf16 v[110:113], v[148:151], v[188:191], v[110:113]
	v_mfma_f32_16x16x32_bf16 v[106:109], v[156:159], v[188:191], v[106:109]
	v_mfma_f32_16x16x32_bf16 v[94:97], v[148:151], v[196:199], v[94:97]
	v_mfma_f32_16x16x32_bf16 v[90:93], v[156:159], v[196:199], v[90:93]
	v_mfma_f32_16x16x32_bf16 v[78:81], v[148:151], v[204:207], v[78:81]
	v_mfma_f32_16x16x32_bf16 v[74:77], v[156:159], v[204:207], v[74:77]
	v_mfma_f32_16x16x32_bf16 v[134:137], v[152:155], v[184:187], v[134:137]
	v_mfma_f32_16x16x32_bf16 v[130:133], v[160:163], v[184:187], v[130:133]
	v_mfma_f32_16x16x32_bf16 v[110:113], v[152:155], v[192:195], v[110:113]
	v_mfma_f32_16x16x32_bf16 v[106:109], v[160:163], v[192:195], v[106:109]
	v_mfma_f32_16x16x32_bf16 v[94:97], v[152:155], v[200:203], v[94:97]
	v_mfma_f32_16x16x32_bf16 v[90:93], v[160:163], v[200:203], v[90:93]
	v_mfma_f32_16x16x32_bf16 v[78:81], v[152:155], v[216:219], v[78:81]
	v_mfma_f32_16x16x32_bf16 v[74:77], v[160:163], v[216:219], v[74:77]
	v_mfma_f32_16x16x32_bf16 v[118:121], v[164:167], v[180:183], v[118:121]
	v_mfma_f32_16x16x32_bf16 v[114:117], v[172:175], v[180:183], v[114:117]
	v_mfma_f32_16x16x32_bf16 v[102:105], v[164:167], v[188:191], v[102:105]
	v_mfma_f32_16x16x32_bf16 v[98:101], v[172:175], v[188:191], v[98:101]
	v_mfma_f32_16x16x32_bf16 v[86:89], v[164:167], v[196:199], v[86:89]
	v_mfma_f32_16x16x32_bf16 v[82:85], v[172:175], v[196:199], v[82:85]
	v_mfma_f32_16x16x32_bf16 v[70:73], v[164:167], v[204:207], v[70:73]
	v_mfma_f32_16x16x32_bf16 v[66:69], v[172:175], v[204:207], v[66:69]
	v_mfma_f32_16x16x32_bf16 v[118:121], v[168:171], v[184:187], v[118:121]
	v_mfma_f32_16x16x32_bf16 v[114:117], v[176:179], v[184:187], v[114:117]
	v_mfma_f32_16x16x32_bf16 v[102:105], v[168:171], v[192:195], v[102:105]
	v_mfma_f32_16x16x32_bf16 v[98:101], v[176:179], v[192:195], v[98:101]
	v_mfma_f32_16x16x32_bf16 v[86:89], v[168:171], v[200:203], v[86:89]
	v_mfma_f32_16x16x32_bf16 v[82:85], v[176:179], v[200:203], v[82:85]
	v_mfma_f32_16x16x32_bf16 v[70:73], v[168:171], v[216:219], v[70:73]
	v_mfma_f32_16x16x32_bf16 v[66:69], v[176:179], v[216:219], v[66:69]
	s_setprio 0
	s_barrier
	s_add_i32 s64, s65, s63
	v_lshl_add_u64 v[208:209], s[42:43], 0, v[126:127]
	s_mov_b32 m0, s64
	ds_read_b128 v[180:183], v147 offset:16384
	ds_read_b128 v[184:187], v147 offset:17408
	ds_read_b128 v[188:191], v147 offset:18432
	ds_read_b128 v[192:195], v147 offset:19456
	ds_read_b128 v[196:199], v147 offset:20480
	ds_read_b128 v[200:203], v147 offset:21504
	ds_read_b128 v[204:207], v147 offset:22528
	ds_read_b128 v[216:219], v147 offset:23552
	global_load_lds_dwordx4 v[208:209], off
	s_add_i32 m0, s64, 0x2000
	s_add_u32 s84, s42, 0x100000
	v_lshl_add_u64 v[220:221], s[42:43], 0, v[122:123]
	s_addc_u32 s85, s43, 0
	s_add_i32 s50, s50, s63
	global_load_lds_dwordx4 v[220:221], off
	v_lshl_add_u64 v[222:223], s[84:85], 0, v[126:127]
	s_mov_b32 m0, s50
	v_lshl_add_u64 v[240:241], s[44:45], 0, v[124:125]
	global_load_lds_dwordx4 v[222:223], off
	v_lshl_add_u64 v[222:223], s[84:85], 0, v[122:123]
	s_add_i32 m0, s50, 0x2000
	s_nop 0
	global_load_lds_dwordx4 v[222:223], off
	v_lshl_add_u64 v[222:223], s[44:45], 0, v[128:129]
	s_mov_b32 m0, s4
	s_nop 0
	global_load_lds_dwordx4 v[222:223], off
	s_mov_b32 m0, s33
	s_nop 0
	global_load_lds_dwordx4 v[240:241], off
	s_waitcnt vmcnt(8)
	s_waitcnt lgkmcnt(0)
	s_barrier
	s_setprio 1
	s_waitcnt lgkmcnt(0)
	v_mfma_f32_16x16x32_bf16 v[62:65], v[148:151], v[180:183], v[62:65]
	v_mfma_f32_16x16x32_bf16 v[58:61], v[156:159], v[180:183], v[58:61]
	v_mfma_f32_16x16x32_bf16 v[46:49], v[148:151], v[188:191], v[46:49]
	v_mfma_f32_16x16x32_bf16 v[42:45], v[156:159], v[188:191], v[42:45]
	v_mfma_f32_16x16x32_bf16 v[30:33], v[148:151], v[196:199], v[30:33]
	v_mfma_f32_16x16x32_bf16 v[26:29], v[156:159], v[196:199], v[26:29]
	v_mfma_f32_16x16x32_bf16 v[14:17], v[148:151], v[204:207], v[14:17]
	v_mfma_f32_16x16x32_bf16 v[10:13], v[156:159], v[204:207], v[10:13]
	v_mfma_f32_16x16x32_bf16 v[62:65], v[152:155], v[184:187], v[62:65]
	v_mfma_f32_16x16x32_bf16 v[58:61], v[160:163], v[184:187], v[58:61]
	v_mfma_f32_16x16x32_bf16 v[46:49], v[152:155], v[192:195], v[46:49]
	v_mfma_f32_16x16x32_bf16 v[42:45], v[160:163], v[192:195], v[42:45]
	v_mfma_f32_16x16x32_bf16 v[30:33], v[152:155], v[200:203], v[30:33]
	v_mfma_f32_16x16x32_bf16 v[26:29], v[160:163], v[200:203], v[26:29]
	v_mfma_f32_16x16x32_bf16 v[14:17], v[152:155], v[216:219], v[14:17]
	v_mfma_f32_16x16x32_bf16 v[10:13], v[160:163], v[216:219], v[10:13]
	v_mfma_f32_16x16x32_bf16 v[54:57], v[164:167], v[180:183], v[54:57]
	v_mfma_f32_16x16x32_bf16 v[50:53], v[172:175], v[180:183], v[50:53]
	v_mfma_f32_16x16x32_bf16 v[38:41], v[164:167], v[188:191], v[38:41]
	v_mfma_f32_16x16x32_bf16 v[34:37], v[172:175], v[188:191], v[34:37]
	v_mfma_f32_16x16x32_bf16 v[22:25], v[164:167], v[196:199], v[22:25]
	v_mfma_f32_16x16x32_bf16 v[18:21], v[172:175], v[196:199], v[18:21]
	v_mfma_f32_16x16x32_bf16 v[6:9], v[164:167], v[204:207], v[6:9]
	v_mfma_f32_16x16x32_bf16 v[2:5], v[172:175], v[204:207], v[2:5]
	v_mfma_f32_16x16x32_bf16 v[54:57], v[168:171], v[184:187], v[54:57]
	v_mfma_f32_16x16x32_bf16 v[50:53], v[176:179], v[184:187], v[50:53]
	v_mfma_f32_16x16x32_bf16 v[38:41], v[168:171], v[192:195], v[38:41]
	v_mfma_f32_16x16x32_bf16 v[34:37], v[176:179], v[192:195], v[34:37]
	v_mfma_f32_16x16x32_bf16 v[22:25], v[168:171], v[200:203], v[22:25]
	v_mfma_f32_16x16x32_bf16 v[18:21], v[176:179], v[200:203], v[18:21]
	v_mfma_f32_16x16x32_bf16 v[6:9], v[168:171], v[216:219], v[6:9]
	v_mfma_f32_16x16x32_bf16 v[2:5], v[176:179], v[216:219], v[2:5]
	s_setprio 0
	s_barrier
	s_add_i32 s50, 0, 0x18000
	s_add_i32 s64, 0, 0x1c000
	v_add_u32_e32 v160, s50, v146
	v_add_u32_e32 v176, s64, v146
	ds_read_b128 v[148:151], v160
	ds_read_b128 v[152:155], v160 offset:1024
	ds_read_b128 v[156:159], v160 offset:2048
	ds_read_b128 v[160:163], v160 offset:3072
	ds_read_b128 v[164:167], v176
	ds_read_b128 v[168:171], v176 offset:1024
	ds_read_b128 v[172:175], v176 offset:2048
	ds_read_b128 v[176:179], v176 offset:3072
	s_add_u32 s44, s44, 0x100000
	s_addc_u32 s45, s45, 0
	s_mov_b32 m0, s70
	v_lshl_add_u64 v[242:243], s[44:45], 0, v[128:129]
	ds_read_b128 v[180:183], v147 offset:32768
	ds_read_b128 v[184:187], v147 offset:33792
	ds_read_b128 v[188:191], v147 offset:34816
	ds_read_b128 v[192:195], v147 offset:35840
	ds_read_b128 v[196:199], v147 offset:36864
	ds_read_b128 v[200:203], v147 offset:37888
	ds_read_b128 v[204:207], v147 offset:38912
	ds_read_b128 v[216:219], v147 offset:39936
	global_load_lds_dwordx4 v[242:243], off
	v_lshl_add_u64 v[242:243], s[44:45], 0, v[124:125]
	s_mov_b32 m0, s71
	s_nop 0
	global_load_lds_dwordx4 v[242:243], off
	s_waitcnt vmcnt(8)
	s_waitcnt lgkmcnt(0)
	s_barrier
	s_setprio 1
	s_waitcnt lgkmcnt(0)
	v_mfma_f32_16x16x32_bf16 v[134:137], v[148:151], v[180:183], v[134:137]
	v_mfma_f32_16x16x32_bf16 v[130:133], v[156:159], v[180:183], v[130:133]
	v_mfma_f32_16x16x32_bf16 v[110:113], v[148:151], v[188:191], v[110:113]
	v_mfma_f32_16x16x32_bf16 v[106:109], v[156:159], v[188:191], v[106:109]
	v_mfma_f32_16x16x32_bf16 v[94:97], v[148:151], v[196:199], v[94:97]
	v_mfma_f32_16x16x32_bf16 v[90:93], v[156:159], v[196:199], v[90:93]
	v_mfma_f32_16x16x32_bf16 v[78:81], v[148:151], v[204:207], v[78:81]
	v_mfma_f32_16x16x32_bf16 v[74:77], v[156:159], v[204:207], v[74:77]
	v_mfma_f32_16x16x32_bf16 v[134:137], v[152:155], v[184:187], v[134:137]
	v_mfma_f32_16x16x32_bf16 v[130:133], v[160:163], v[184:187], v[130:133]
	v_mfma_f32_16x16x32_bf16 v[110:113], v[152:155], v[192:195], v[110:113]
	v_mfma_f32_16x16x32_bf16 v[106:109], v[160:163], v[192:195], v[106:109]
	v_mfma_f32_16x16x32_bf16 v[94:97], v[152:155], v[200:203], v[94:97]
	v_mfma_f32_16x16x32_bf16 v[90:93], v[160:163], v[200:203], v[90:93]
	v_mfma_f32_16x16x32_bf16 v[78:81], v[152:155], v[216:219], v[78:81]
	v_mfma_f32_16x16x32_bf16 v[74:77], v[160:163], v[216:219], v[74:77]
	v_mfma_f32_16x16x32_bf16 v[118:121], v[164:167], v[180:183], v[118:121]
	v_mfma_f32_16x16x32_bf16 v[114:117], v[172:175], v[180:183], v[114:117]
	v_mfma_f32_16x16x32_bf16 v[102:105], v[164:167], v[188:191], v[102:105]
	v_mfma_f32_16x16x32_bf16 v[98:101], v[172:175], v[188:191], v[98:101]
	v_mfma_f32_16x16x32_bf16 v[86:89], v[164:167], v[196:199], v[86:89]
	v_mfma_f32_16x16x32_bf16 v[82:85], v[172:175], v[196:199], v[82:85]
	v_mfma_f32_16x16x32_bf16 v[70:73], v[164:167], v[204:207], v[70:73]
	v_mfma_f32_16x16x32_bf16 v[66:69], v[172:175], v[204:207], v[66:69]
	v_mfma_f32_16x16x32_bf16 v[118:121], v[168:171], v[184:187], v[118:121]
	v_mfma_f32_16x16x32_bf16 v[114:117], v[176:179], v[184:187], v[114:117]
	v_mfma_f32_16x16x32_bf16 v[102:105], v[168:171], v[192:195], v[102:105]
	v_mfma_f32_16x16x32_bf16 v[98:101], v[176:179], v[192:195], v[98:101]
	v_mfma_f32_16x16x32_bf16 v[86:89], v[168:171], v[200:203], v[86:89]
	v_mfma_f32_16x16x32_bf16 v[82:85], v[176:179], v[200:203], v[82:85]
	v_mfma_f32_16x16x32_bf16 v[70:73], v[168:171], v[216:219], v[70:73]
	v_mfma_f32_16x16x32_bf16 v[66:69], v[176:179], v[216:219], v[66:69]
	s_setprio 0
	s_barrier
	s_add_i32 s44, s50, s63
	v_lshl_add_u64 v[208:209], v[208:209], 0, s[56:57]
	s_mov_b32 m0, s44
	ds_read_b128 v[180:183], v147 offset:49152
	ds_read_b128 v[184:187], v147 offset:50176
	ds_read_b128 v[188:191], v147 offset:51200
	ds_read_b128 v[192:195], v147 offset:52224
	ds_read_b128 v[196:199], v147 offset:53248
	ds_read_b128 v[200:203], v147 offset:54272
	ds_read_b128 v[204:207], v147 offset:55296
	ds_read_b128 v[216:219], v147 offset:56320
	global_load_lds_dwordx4 v[208:209], off
	s_add_i32 m0, s44, 0x2000
	s_add_u32 s42, s42, 0x100080
	v_lshl_add_u64 v[208:209], v[220:221], 0, s[56:57]
	s_addc_u32 s43, s43, 0
	s_add_i32 s44, s64, s63
	global_load_lds_dwordx4 v[208:209], off
	v_lshl_add_u64 v[208:209], s[42:43], 0, v[126:127]
	s_mov_b32 m0, s44
	s_nop 0
	global_load_lds_dwordx4 v[208:209], off
	v_lshl_add_u64 v[208:209], s[42:43], 0, v[122:123]
	s_add_i32 m0, s44, 0x2000
	s_nop 0
	global_load_lds_dwordx4 v[208:209], off
	v_lshl_add_u64 v[208:209], v[222:223], 0, s[56:57]
	s_mov_b32 m0, s76
	s_nop 0
	global_load_lds_dwordx4 v[208:209], off
	v_lshl_add_u64 v[208:209], v[240:241], 0, s[56:57]
	s_mov_b32 m0, s77
	s_nop 0
	global_load_lds_dwordx4 v[208:209], off
	s_waitcnt vmcnt(8)
	s_waitcnt lgkmcnt(0)
	s_barrier
	s_setprio 1
	s_waitcnt lgkmcnt(0)
	v_mfma_f32_16x16x32_bf16 v[62:65], v[148:151], v[180:183], v[62:65]
	v_mfma_f32_16x16x32_bf16 v[58:61], v[156:159], v[180:183], v[58:61]
	v_mfma_f32_16x16x32_bf16 v[46:49], v[148:151], v[188:191], v[46:49]
	v_mfma_f32_16x16x32_bf16 v[42:45], v[156:159], v[188:191], v[42:45]
	v_mfma_f32_16x16x32_bf16 v[30:33], v[148:151], v[196:199], v[30:33]
	v_mfma_f32_16x16x32_bf16 v[26:29], v[156:159], v[196:199], v[26:29]
	v_mfma_f32_16x16x32_bf16 v[14:17], v[148:151], v[204:207], v[14:17]
	v_mfma_f32_16x16x32_bf16 v[10:13], v[156:159], v[204:207], v[10:13]
	v_mfma_f32_16x16x32_bf16 v[62:65], v[152:155], v[184:187], v[62:65]
	v_mfma_f32_16x16x32_bf16 v[58:61], v[160:163], v[184:187], v[58:61]
	v_mfma_f32_16x16x32_bf16 v[46:49], v[152:155], v[192:195], v[46:49]
	v_mfma_f32_16x16x32_bf16 v[42:45], v[160:163], v[192:195], v[42:45]
	v_mfma_f32_16x16x32_bf16 v[30:33], v[152:155], v[200:203], v[30:33]
	v_mfma_f32_16x16x32_bf16 v[26:29], v[160:163], v[200:203], v[26:29]
	v_mfma_f32_16x16x32_bf16 v[14:17], v[152:155], v[216:219], v[14:17]
	v_mfma_f32_16x16x32_bf16 v[10:13], v[160:163], v[216:219], v[10:13]
	v_mfma_f32_16x16x32_bf16 v[54:57], v[164:167], v[180:183], v[54:57]
	v_mfma_f32_16x16x32_bf16 v[50:53], v[172:175], v[180:183], v[50:53]
	v_mfma_f32_16x16x32_bf16 v[38:41], v[164:167], v[188:191], v[38:41]
	v_mfma_f32_16x16x32_bf16 v[34:37], v[172:175], v[188:191], v[34:37]
	v_mfma_f32_16x16x32_bf16 v[22:25], v[164:167], v[196:199], v[22:25]
	v_mfma_f32_16x16x32_bf16 v[18:21], v[172:175], v[196:199], v[18:21]
	v_mfma_f32_16x16x32_bf16 v[6:9], v[164:167], v[204:207], v[6:9]
	v_mfma_f32_16x16x32_bf16 v[2:5], v[172:175], v[204:207], v[2:5]
	v_mfma_f32_16x16x32_bf16 v[54:57], v[168:171], v[184:187], v[54:57]
	v_mfma_f32_16x16x32_bf16 v[50:53], v[176:179], v[184:187], v[50:53]
	v_mfma_f32_16x16x32_bf16 v[38:41], v[168:171], v[192:195], v[38:41]
	v_mfma_f32_16x16x32_bf16 v[34:37], v[176:179], v[192:195], v[34:37]
	v_mfma_f32_16x16x32_bf16 v[22:25], v[168:171], v[200:203], v[22:25]
	v_mfma_f32_16x16x32_bf16 v[18:21], v[176:179], v[200:203], v[18:21]
	v_mfma_f32_16x16x32_bf16 v[6:9], v[168:171], v[216:219], v[6:9]
	v_mfma_f32_16x16x32_bf16 v[2:5], v[176:179], v[216:219], v[2:5]
	s_setprio 0
	s_barrier
	s_add_i32 s82, s82, 2
	s_add_u32 s36, s36, 0x100
	s_addc_u32 s37, s37, 0
	s_cmp_gt_u32 s82, 61
	s_cbranch_scc0 .LBB0_2982
	s_add_u32 s36, s59, 0xffffff00
	s_addc_u32 s37, s79, -1
	s_andn2_b64 vcc, exec, s[40:41]
	s_cbranch_vccnz .LBB0_2985
	v_mov_b32_e32 v2, 0
	s_mov_b32 s20, s26
	s_mov_b32 s78, s28
	s_mov_b64 s[24:25], s[34:35]
	s_mov_b32 s68, s58
	v_mov_b32_e32 v3, v2
	v_mov_b32_e32 v4, v2
	v_mov_b32_e32 v5, v2
	v_mov_b32_e32 v6, v2
	v_mov_b32_e32 v7, v2
	v_mov_b32_e32 v8, v2
	v_mov_b32_e32 v9, v2
	v_mov_b32_e32 v18, v2
	v_mov_b32_e32 v19, v2
	v_mov_b32_e32 v20, v2
	v_mov_b32_e32 v21, v2
	v_mov_b32_e32 v22, v2
	v_mov_b32_e32 v23, v2
	v_mov_b32_e32 v24, v2
	v_mov_b32_e32 v25, v2
	v_mov_b32_e32 v34, v2
	v_mov_b32_e32 v35, v2
	v_mov_b32_e32 v36, v2
	v_mov_b32_e32 v37, v2
	v_mov_b32_e32 v38, v2
	v_mov_b32_e32 v39, v2
	v_mov_b32_e32 v40, v2
	v_mov_b32_e32 v41, v2
	v_mov_b32_e32 v50, v2
	v_mov_b32_e32 v51, v2
	v_mov_b32_e32 v52, v2
	v_mov_b32_e32 v53, v2
	v_mov_b32_e32 v54, v2
	v_mov_b32_e32 v55, v2
	v_mov_b32_e32 v56, v2
	v_mov_b32_e32 v57, v2
	v_mov_b32_e32 v10, v2
	v_mov_b32_e32 v11, v2
	v_mov_b32_e32 v12, v2
	v_mov_b32_e32 v13, v2
	v_mov_b32_e32 v14, v2
	v_mov_b32_e32 v15, v2
	v_mov_b32_e32 v16, v2
	v_mov_b32_e32 v17, v2
	v_mov_b32_e32 v26, v2
	v_mov_b32_e32 v27, v2
	v_mov_b32_e32 v28, v2
	v_mov_b32_e32 v29, v2
	v_mov_b32_e32 v30, v2
	v_mov_b32_e32 v31, v2
	v_mov_b32_e32 v32, v2
	v_mov_b32_e32 v33, v2
	v_mov_b32_e32 v42, v2
	v_mov_b32_e32 v43, v2
	v_mov_b32_e32 v44, v2
	v_mov_b32_e32 v45, v2
	v_mov_b32_e32 v46, v2
	v_mov_b32_e32 v47, v2
	v_mov_b32_e32 v48, v2
	v_mov_b32_e32 v49, v2
	v_mov_b32_e32 v58, v2
	v_mov_b32_e32 v59, v2
	v_mov_b32_e32 v60, v2
	v_mov_b32_e32 v61, v2
	v_mov_b32_e32 v62, v2
	v_mov_b32_e32 v63, v2
	v_mov_b32_e32 v64, v2
	v_mov_b32_e32 v65, v2
	v_mov_b32_e32 v66, v2
	v_mov_b32_e32 v67, v2
	v_mov_b32_e32 v68, v2
	v_mov_b32_e32 v69, v2
	v_mov_b32_e32 v70, v2
	v_mov_b32_e32 v71, v2
	v_mov_b32_e32 v72, v2
	v_mov_b32_e32 v73, v2
	v_mov_b32_e32 v82, v2
	v_mov_b32_e32 v83, v2
	v_mov_b32_e32 v84, v2
	v_mov_b32_e32 v85, v2
	v_mov_b32_e32 v86, v2
	v_mov_b32_e32 v87, v2
	v_mov_b32_e32 v88, v2
	v_mov_b32_e32 v89, v2
	v_mov_b32_e32 v98, v2
	v_mov_b32_e32 v99, v2
	v_mov_b32_e32 v100, v2
	v_mov_b32_e32 v101, v2
	v_mov_b32_e32 v102, v2
	v_mov_b32_e32 v103, v2
	v_mov_b32_e32 v104, v2
	v_mov_b32_e32 v105, v2
	v_mov_b32_e32 v114, v2
	v_mov_b32_e32 v115, v2
	v_mov_b32_e32 v116, v2
	v_mov_b32_e32 v117, v2
	v_mov_b32_e32 v118, v2
	v_mov_b32_e32 v119, v2
	v_mov_b32_e32 v120, v2
	v_mov_b32_e32 v121, v2
	v_mov_b32_e32 v74, v2
	v_mov_b32_e32 v75, v2
	v_mov_b32_e32 v76, v2
	v_mov_b32_e32 v77, v2
	v_mov_b32_e32 v78, v2
	v_mov_b32_e32 v79, v2
	v_mov_b32_e32 v80, v2
	v_mov_b32_e32 v81, v2
	v_mov_b32_e32 v90, v2
	v_mov_b32_e32 v91, v2
	v_mov_b32_e32 v92, v2
	v_mov_b32_e32 v93, v2
	v_mov_b32_e32 v94, v2
	v_mov_b32_e32 v95, v2
	v_mov_b32_e32 v96, v2
	v_mov_b32_e32 v97, v2
	v_mov_b32_e32 v106, v2
	v_mov_b32_e32 v107, v2
	v_mov_b32_e32 v108, v2
	v_mov_b32_e32 v109, v2
	v_mov_b32_e32 v110, v2
	v_mov_b32_e32 v111, v2
	v_mov_b32_e32 v112, v2
	v_mov_b32_e32 v113, v2
	v_mov_b32_e32 v130, v2
	v_mov_b32_e32 v131, v2
	v_mov_b32_e32 v132, v2
	v_mov_b32_e32 v133, v2
	v_mov_b32_e32 v134, v2
	v_mov_b32_e32 v135, v2
	v_mov_b32_e32 v136, v2
	v_mov_b32_e32 v137, v2
	s_andn2_b64 vcc, exec, s[38:39]
	s_cbranch_vccnz .LBB0_2986
	s_branch .LBB0_2987
